# GEMM K-loops: all 224 per-burst s_setprio flips deleted, one static s_setprio 1 for the younger wave half (waves 4-7) at kernel entry
# speedup vs baseline: 1.0044x; 1.0011x over previous
_Z10fwd_kernel4Args:
	s_load_dwordx2 s[96:97], s[0:1], 0xb0
	v_readfirstlane_b32 s98, v0
	s_nop 3
	s_bitcmp1_b32 s98, 8
	s_cbranch_scc0 .Lprio_done
	s_setprio 1
.Lprio_done:
	s_load_dwordx4 s[4:7], s[0:1], 0xa0
	s_mov_b32 s86, s2
	s_load_dwordx4 s[56:59], s[0:1], 0xb8
	s_load_dword s94, s[0:1], 0xc8
	s_load_dwordx8 s[60:67], s[0:1], 0x80
	v_readfirstlane_b32 s2, v0
	s_waitcnt lgkmcnt(0)
	v_writelane_b32 v254, s4, 0
	s_nop 1
	v_writelane_b32 v254, s5, 1
	v_writelane_b32 v254, s6, 2
	v_writelane_b32 v254, s7, 3
	v_writelane_b32 v254, s2, 4
	s_add_u32 s2, s0, 0xc8
	s_addc_u32 s3, s1, 0
	v_writelane_b32 v254, s2, 5
	s_nop 1
	v_writelane_b32 v254, s3, 6
	s_and_b32 s3, s94, 7
	s_cmp_lg_u32 s3, 0
	s_mov_b32 s3, s86
	s_mov_b32 s2, 0
	v_writelane_b32 v254, s3, 7
	s_cbranch_scc1 .LBB0_2
	s_ashr_i32 s4, s86, 31
	s_lshr_b32 s4, s4, 29
	s_add_i32 s4, s86, s4
	s_and_b32 s5, s4, -8
	s_ashr_i32 s3, s94, 3
	s_sub_i32 s5, s86, s5
	s_mul_i32 s3, s3, s5
	s_ashr_i32 s4, s4, 3
	s_add_i32 s3, s3, s4
	v_writelane_b32 v254, s3, 7

.LBB0_291:
	s_waitcnt lgkmcnt(0)
	s_add_i32 s36, s62, 2
	s_add_u32 s34, s28, 0x8000
	s_addc_u32 s35, s29, 0
	s_barrier
	s_waitcnt lgkmcnt(0)
	v_mfma_i32_16x16x64_i8 v[62:65], v[146:149], v[186:189], v[62:65]
	v_mfma_i32_16x16x64_i8 v[58:61], v[150:153], v[186:189], v[58:61]
	v_mfma_i32_16x16x64_i8 v[54:57], v[146:149], v[178:181], v[54:57]
	v_mfma_i32_16x16x64_i8 v[50:53], v[150:153], v[178:181], v[50:53]
	v_mfma_i32_16x16x64_i8 v[38:41], v[146:149], v[170:173], v[38:41]
	v_mfma_i32_16x16x64_i8 v[34:37], v[150:153], v[170:173], v[34:37]
	v_mfma_i32_16x16x64_i8 v[22:25], v[146:149], v[162:165], v[22:25]
	v_mfma_i32_16x16x64_i8 v[18:21], v[150:153], v[162:165], v[18:21]
	v_mfma_i32_16x16x64_i8 v[62:65], v[158:161], v[190:193], v[62:65]
	v_mfma_i32_16x16x64_i8 v[58:61], v[154:157], v[190:193], v[58:61]
	v_mfma_i32_16x16x64_i8 v[54:57], v[158:161], v[182:185], v[54:57]
	v_mfma_i32_16x16x64_i8 v[50:53], v[154:157], v[182:185], v[50:53]
	v_mfma_i32_16x16x64_i8 v[38:41], v[158:161], v[174:177], v[38:41]
	v_mfma_i32_16x16x64_i8 v[34:37], v[154:157], v[174:177], v[34:37]
	v_mfma_i32_16x16x64_i8 v[22:25], v[158:161], v[166:169], v[22:25]
	v_mfma_i32_16x16x64_i8 v[18:21], v[154:157], v[166:169], v[18:21]
	v_mfma_i32_16x16x64_i8 v[46:49], v[130:133], v[186:189], v[46:49]
	v_mfma_i32_16x16x64_i8 v[42:45], v[134:137], v[186:189], v[42:45]
	v_mfma_i32_16x16x64_i8 v[30:33], v[130:133], v[178:181], v[30:33]
	v_mfma_i32_16x16x64_i8 v[26:29], v[134:137], v[178:181], v[26:29]
	v_mfma_i32_16x16x64_i8 v[14:17], v[130:133], v[170:173], v[14:17]
	v_mfma_i32_16x16x64_i8 v[10:13], v[134:137], v[170:173], v[10:13]
	v_mfma_i32_16x16x64_i8 v[6:9], v[130:133], v[162:165], v[6:9]
	v_mfma_i32_16x16x64_i8 v[2:5], v[134:137], v[162:165], v[2:5]
	v_mfma_i32_16x16x64_i8 v[46:49], v[142:145], v[190:193], v[46:49]
	v_mfma_i32_16x16x64_i8 v[42:45], v[138:141], v[190:193], v[42:45]
	v_mfma_i32_16x16x64_i8 v[30:33], v[142:145], v[182:185], v[30:33]
	v_mfma_i32_16x16x64_i8 v[26:29], v[138:141], v[182:185], v[26:29]
	v_mfma_i32_16x16x64_i8 v[14:17], v[142:145], v[174:177], v[14:17]
	v_mfma_i32_16x16x64_i8 v[10:13], v[138:141], v[174:177], v[10:13]
	v_mfma_i32_16x16x64_i8 v[6:9], v[142:145], v[166:169], v[6:9]
	v_mfma_i32_16x16x64_i8 v[2:5], v[138:141], v[166:169], v[2:5]
	s_barrier
	s_add_i32 s37, 0, 0x18000
	s_add_i32 s65, 0, 0x1c000
	v_add_u32_e32 v134, s37, v232
	v_add_u32_e32 v142, s37, v233
	v_add_u32_e32 v150, s65, v232
	v_add_u32_e32 v158, s65, v233
	ds_read_b128 v[130:133], v134
	ds_read_b128 v[134:137], v134 offset:2048
	ds_read_b128 v[138:141], v142
	ds_read_b128 v[142:145], v142 offset:2048
	ds_read_b128 v[146:149], v150
	ds_read_b128 v[150:153], v150 offset:2048
	ds_read_b128 v[154:157], v158
	ds_read_b128 v[158:161], v158 offset:2048
	s_add_u32 s30, s30, 0x40000
	s_addc_u32 s31, s31, 0
	s_mov_b32 m0, s48
	v_lshl_add_u64 v[238:239], s[30:31], 0, v[194:195]
	ds_read_b128 v[162:165], v236 offset:32768
	ds_read_b128 v[166:169], v236 offset:33792
	ds_read_b128 v[170:173], v236 offset:34816
	ds_read_b128 v[174:177], v236 offset:35840
	ds_read_b128 v[178:181], v236 offset:36864
	ds_read_b128 v[182:185], v236 offset:37888
	ds_read_b128 v[186:189], v236 offset:38912
	ds_read_b128 v[190:193], v236 offset:39936
	global_load_lds_dwordx4 v[238:239], off
	v_lshl_add_u64 v[238:239], s[30:31], 0, v[196:197]
	s_mov_b32 m0, s49
	s_nop 0
	global_load_lds_dwordx4 v[238:239], off
	s_waitcnt vmcnt(8)
	s_waitcnt lgkmcnt(0)
	s_barrier
	s_waitcnt lgkmcnt(0)
	v_mfma_i32_16x16x64_i8 v[126:129], v[130:133], v[162:165], v[126:129]
	v_mfma_i32_16x16x64_i8 v[122:125], v[134:137], v[162:165], v[122:125]
	v_mfma_i32_16x16x64_i8 v[118:121], v[130:133], v[170:173], v[118:121]
	v_mfma_i32_16x16x64_i8 v[114:117], v[134:137], v[170:173], v[114:117]
	v_mfma_i32_16x16x64_i8 v[102:105], v[130:133], v[178:181], v[102:105]
	v_mfma_i32_16x16x64_i8 v[98:101], v[134:137], v[178:181], v[98:101]
	v_mfma_i32_16x16x64_i8 v[86:89], v[130:133], v[186:189], v[86:89]
	v_mfma_i32_16x16x64_i8 v[82:85], v[134:137], v[186:189], v[82:85]
	v_mfma_i32_16x16x64_i8 v[126:129], v[138:141], v[166:169], v[126:129]
	v_mfma_i32_16x16x64_i8 v[122:125], v[142:145], v[166:169], v[122:125]
	v_mfma_i32_16x16x64_i8 v[118:121], v[138:141], v[174:177], v[118:121]
	v_mfma_i32_16x16x64_i8 v[114:117], v[142:145], v[174:177], v[114:117]
	v_mfma_i32_16x16x64_i8 v[102:105], v[138:141], v[182:185], v[102:105]
	v_mfma_i32_16x16x64_i8 v[98:101], v[142:145], v[182:185], v[98:101]
	v_mfma_i32_16x16x64_i8 v[86:89], v[138:141], v[190:193], v[86:89]
	v_mfma_i32_16x16x64_i8 v[82:85], v[142:145], v[190:193], v[82:85]
	v_mfma_i32_16x16x64_i8 v[110:113], v[146:149], v[162:165], v[110:113]
	v_mfma_i32_16x16x64_i8 v[106:109], v[150:153], v[162:165], v[106:109]
	v_mfma_i32_16x16x64_i8 v[94:97], v[146:149], v[170:173], v[94:97]
	v_mfma_i32_16x16x64_i8 v[90:93], v[150:153], v[170:173], v[90:93]
	v_mfma_i32_16x16x64_i8 v[78:81], v[146:149], v[178:181], v[78:81]
	v_mfma_i32_16x16x64_i8 v[74:77], v[150:153], v[178:181], v[74:77]
	v_mfma_i32_16x16x64_i8 v[70:73], v[146:149], v[186:189], v[70:73]
	v_mfma_i32_16x16x64_i8 v[66:69], v[150:153], v[186:189], v[66:69]
	v_mfma_i32_16x16x64_i8 v[110:113], v[154:157], v[166:169], v[110:113]
	v_mfma_i32_16x16x64_i8 v[106:109], v[158:161], v[166:169], v[106:109]
	v_mfma_i32_16x16x64_i8 v[94:97], v[154:157], v[174:177], v[94:97]
	v_mfma_i32_16x16x64_i8 v[90:93], v[158:161], v[174:177], v[90:93]
	v_mfma_i32_16x16x64_i8 v[78:81], v[154:157], v[182:185], v[78:81]
	v_mfma_i32_16x16x64_i8 v[74:77], v[158:161], v[182:185], v[74:77]
	v_mfma_i32_16x16x64_i8 v[70:73], v[154:157], v[190:193], v[70:73]
	v_mfma_i32_16x16x64_i8 v[66:69], v[158:161], v[190:193], v[66:69]
	s_barrier
	s_add_i32 s30, s37, s38
	v_lshl_add_u64 v[238:239], s[34:35], 0, v[198:199]
	s_mov_b32 m0, s30
	ds_read_b128 v[162:165], v236 offset:49152
	ds_read_b128 v[166:169], v236 offset:50176
	ds_read_b128 v[170:173], v236 offset:51200
	ds_read_b128 v[174:177], v236 offset:52224
	ds_read_b128 v[178:181], v236 offset:53248
	ds_read_b128 v[182:185], v236 offset:54272
	ds_read_b128 v[186:189], v236 offset:55296
	ds_read_b128 v[190:193], v236 offset:56320
	global_load_lds_dwordx4 v[238:239], off
	s_add_i32 m0, s30, 0x2000
	s_add_u32 s28, s28, 0x9000
	v_lshl_add_u64 v[238:239], s[34:35], 0, v[200:201]
	s_addc_u32 s29, s29, 0
	s_add_i32 s30, s65, s38
	global_load_lds_dwordx4 v[238:239], off
	v_lshl_add_u64 v[238:239], s[28:29], 0, v[198:199]
	s_mov_b32 m0, s30
	v_lshl_add_u64 v[214:215], v[214:215], 0, s[2:3]
	global_load_lds_dwordx4 v[238:239], off
	v_lshl_add_u64 v[238:239], s[28:29], 0, v[200:201]
	s_add_i32 m0, s30, 0x2000
	s_nop 0
	global_load_lds_dwordx4 v[238:239], off
	s_mov_b32 m0, s50
	s_nop 0
	global_load_lds_dwordx4 v[214:215], off
	v_lshl_add_u64 v[214:215], v[216:217], 0, s[2:3]
	s_mov_b32 m0, s51
	s_nop 0
	global_load_lds_dwordx4 v[214:215], off
	s_waitcnt vmcnt(8)
	s_waitcnt lgkmcnt(0)
	s_barrier
	s_waitcnt lgkmcnt(0)
	v_mfma_i32_16x16x64_i8 v[62:65], v[130:133], v[162:165], v[62:65]
	v_mfma_i32_16x16x64_i8 v[58:61], v[134:137], v[162:165], v[58:61]
	v_mfma_i32_16x16x64_i8 v[54:57], v[130:133], v[170:173], v[54:57]
	v_mfma_i32_16x16x64_i8 v[50:53], v[134:137], v[170:173], v[50:53]
	v_mfma_i32_16x16x64_i8 v[38:41], v[130:133], v[178:181], v[38:41]
	v_mfma_i32_16x16x64_i8 v[34:37], v[134:137], v[178:181], v[34:37]
	v_mfma_i32_16x16x64_i8 v[22:25], v[130:133], v[186:189], v[22:25]
	v_mfma_i32_16x16x64_i8 v[18:21], v[134:137], v[186:189], v[18:21]
	v_mfma_i32_16x16x64_i8 v[62:65], v[138:141], v[166:169], v[62:65]
	v_mfma_i32_16x16x64_i8 v[58:61], v[142:145], v[166:169], v[58:61]
	v_mfma_i32_16x16x64_i8 v[54:57], v[138:141], v[174:177], v[54:57]
	v_mfma_i32_16x16x64_i8 v[50:53], v[142:145], v[174:177], v[50:53]
	v_mfma_i32_16x16x64_i8 v[38:41], v[138:141], v[182:185], v[38:41]
	v_mfma_i32_16x16x64_i8 v[34:37], v[142:145], v[182:185], v[34:37]
	v_mfma_i32_16x16x64_i8 v[22:25], v[138:141], v[190:193], v[22:25]
	v_mfma_i32_16x16x64_i8 v[18:21], v[142:145], v[190:193], v[18:21]
	v_mfma_i32_16x16x64_i8 v[46:49], v[146:149], v[162:165], v[46:49]
	v_mfma_i32_16x16x64_i8 v[42:45], v[150:153], v[162:165], v[42:45]
	v_mfma_i32_16x16x64_i8 v[30:33], v[146:149], v[170:173], v[30:33]
	v_mfma_i32_16x16x64_i8 v[26:29], v[150:153], v[170:173], v[26:29]
	v_mfma_i32_16x16x64_i8 v[14:17], v[146:149], v[178:181], v[14:17]
	v_mfma_i32_16x16x64_i8 v[10:13], v[150:153], v[178:181], v[10:13]
	v_mfma_i32_16x16x64_i8 v[6:9], v[146:149], v[186:189], v[6:9]
	v_mfma_i32_16x16x64_i8 v[2:5], v[150:153], v[186:189], v[2:5]
	v_mfma_i32_16x16x64_i8 v[46:49], v[154:157], v[166:169], v[46:49]
	v_mfma_i32_16x16x64_i8 v[42:45], v[158:161], v[166:169], v[42:45]
	v_mfma_i32_16x16x64_i8 v[30:33], v[154:157], v[174:177], v[30:33]
	v_mfma_i32_16x16x64_i8 v[26:29], v[158:161], v[174:177], v[26:29]
	v_mfma_i32_16x16x64_i8 v[14:17], v[154:157], v[182:185], v[14:17]
	v_mfma_i32_16x16x64_i8 v[10:13], v[158:161], v[182:185], v[10:13]
	v_mfma_i32_16x16x64_i8 v[6:9], v[154:157], v[190:193], v[6:9]
	v_mfma_i32_16x16x64_i8 v[2:5], v[158:161], v[190:193], v[2:5]
	s_barrier
	s_add_u32 s63, s63, 0x10000
	s_addc_u32 s64, s64, 0
	s_add_u32 s26, s26, 0x100
	s_addc_u32 s27, s27, 0
	s_cmp_gt_u32 s62, 13
	s_mov_b32 s62, s36
	s_cbranch_scc1 .LBB0_300

.LBB0_296:
	s_add_u32 s28, s24, s26
	s_addc_u32 s29, s25, s27
	s_add_u32 s28, s28, 0x100
	s_addc_u32 s29, s29, 0
	s_waitcnt lgkmcnt(0)
	s_cmpk_eq_i32 s26, 0x700
	s_cselect_b32 s31, s15, s29
	s_cselect_b32 s30, s23, s28
	s_cselect_b32 s29, s13, s64
	s_cselect_b32 s28, s60, s63
	s_barrier
	s_waitcnt lgkmcnt(0)
	v_mfma_i32_16x16x64_i8 v[126:129], v[146:149], v[186:189], v[126:129]
	v_mfma_i32_16x16x64_i8 v[122:125], v[150:153], v[186:189], v[122:125]
	v_mfma_i32_16x16x64_i8 v[118:121], v[146:149], v[178:181], v[118:121]
	v_mfma_i32_16x16x64_i8 v[114:117], v[150:153], v[178:181], v[114:117]
	v_mfma_i32_16x16x64_i8 v[102:105], v[146:149], v[170:173], v[102:105]
	v_mfma_i32_16x16x64_i8 v[98:101], v[150:153], v[170:173], v[98:101]
	v_mfma_i32_16x16x64_i8 v[86:89], v[146:149], v[162:165], v[86:89]
	v_mfma_i32_16x16x64_i8 v[82:85], v[150:153], v[162:165], v[82:85]
	v_mfma_i32_16x16x64_i8 v[126:129], v[158:161], v[190:193], v[126:129]
	v_mfma_i32_16x16x64_i8 v[122:125], v[154:157], v[190:193], v[122:125]
	v_mfma_i32_16x16x64_i8 v[118:121], v[158:161], v[182:185], v[118:121]
	v_mfma_i32_16x16x64_i8 v[114:117], v[154:157], v[182:185], v[114:117]
	v_mfma_i32_16x16x64_i8 v[102:105], v[158:161], v[174:177], v[102:105]
	v_mfma_i32_16x16x64_i8 v[98:101], v[154:157], v[174:177], v[98:101]
	v_mfma_i32_16x16x64_i8 v[86:89], v[158:161], v[166:169], v[86:89]
	v_mfma_i32_16x16x64_i8 v[82:85], v[154:157], v[166:169], v[82:85]
	v_mfma_i32_16x16x64_i8 v[110:113], v[130:133], v[186:189], v[110:113]
	v_mfma_i32_16x16x64_i8 v[106:109], v[134:137], v[186:189], v[106:109]
	v_mfma_i32_16x16x64_i8 v[94:97], v[130:133], v[178:181], v[94:97]
	v_mfma_i32_16x16x64_i8 v[90:93], v[134:137], v[178:181], v[90:93]
	v_mfma_i32_16x16x64_i8 v[78:81], v[130:133], v[170:173], v[78:81]
	v_mfma_i32_16x16x64_i8 v[74:77], v[134:137], v[170:173], v[74:77]
	v_mfma_i32_16x16x64_i8 v[70:73], v[130:133], v[162:165], v[70:73]
	v_mfma_i32_16x16x64_i8 v[66:69], v[134:137], v[162:165], v[66:69]
	v_mfma_i32_16x16x64_i8 v[110:113], v[142:145], v[190:193], v[110:113]
	v_mfma_i32_16x16x64_i8 v[106:109], v[138:141], v[190:193], v[106:109]
	v_mfma_i32_16x16x64_i8 v[94:97], v[142:145], v[182:185], v[94:97]
	v_mfma_i32_16x16x64_i8 v[90:93], v[138:141], v[182:185], v[90:93]
	v_mfma_i32_16x16x64_i8 v[78:81], v[142:145], v[174:177], v[78:81]
	v_mfma_i32_16x16x64_i8 v[74:77], v[138:141], v[174:177], v[74:77]
	v_mfma_i32_16x16x64_i8 v[70:73], v[142:145], v[166:169], v[70:73]
	v_mfma_i32_16x16x64_i8 v[66:69], v[138:141], v[166:169], v[66:69]
	s_barrier
	s_mov_b32 m0, s42
	v_lshl_add_u64 v[214:215], s[28:29], 0, v[198:199]
	s_add_u32 s36, s28, 0x1000
	ds_read_b128 v[186:189], v236 offset:16384
	ds_read_b128 v[190:193], v236 offset:17408
	ds_read_b128 v[178:181], v236 offset:18432
	ds_read_b128 v[182:185], v236 offset:19456
	ds_read_b128 v[170:173], v236 offset:20480
	ds_read_b128 v[174:177], v236 offset:21504
	ds_read_b128 v[162:165], v236 offset:22528
	ds_read_b128 v[166:169], v236 offset:23552
	global_load_lds_dwordx4 v[214:215], off
	v_lshl_add_u64 v[214:215], s[28:29], 0, v[200:201]
	s_mov_b32 m0, s43
	s_addc_u32 s37, s29, 0
	global_load_lds_dwordx4 v[214:215], off
	v_lshl_add_u64 v[214:215], s[36:37], 0, v[198:199]
	s_mov_b32 m0, s44
	v_lshl_add_u64 v[216:217], s[30:31], 0, v[196:197]
	global_load_lds_dwordx4 v[214:215], off
	v_lshl_add_u64 v[214:215], s[36:37], 0, v[200:201]
	s_mov_b32 m0, s45
	s_mov_b64 s[36:37], -1
	global_load_lds_dwordx4 v[214:215], off
	v_lshl_add_u64 v[214:215], s[30:31], 0, v[194:195]
	s_mov_b32 m0, s41
	s_and_b64 vcc, exec, s[34:35]
	global_load_lds_dwordx4 v[214:215], off
	s_mov_b32 m0, s47
	s_nop 0
	global_load_lds_dwordx4 v[216:217], off
	s_cbranch_vccz .LBB0_298
	s_waitcnt vmcnt(8)
	s_mov_b64 s[36:37], 0

.LBB0_592:
	s_waitcnt lgkmcnt(0)
	s_add_i32 s38, s62, 2
	s_add_u32 s36, s30, 0x8000
	s_addc_u32 s37, s31, 0
	s_barrier
	s_waitcnt lgkmcnt(0)
	v_mfma_i32_16x16x64_i8 v[62:65], v[146:149], v[186:189], v[62:65]
	v_mfma_i32_16x16x64_i8 v[58:61], v[150:153], v[186:189], v[58:61]
	v_mfma_i32_16x16x64_i8 v[54:57], v[146:149], v[178:181], v[54:57]
	v_mfma_i32_16x16x64_i8 v[50:53], v[150:153], v[178:181], v[50:53]
	v_mfma_i32_16x16x64_i8 v[38:41], v[146:149], v[170:173], v[38:41]
	v_mfma_i32_16x16x64_i8 v[34:37], v[150:153], v[170:173], v[34:37]
	v_mfma_i32_16x16x64_i8 v[22:25], v[146:149], v[162:165], v[22:25]
	v_mfma_i32_16x16x64_i8 v[18:21], v[150:153], v[162:165], v[18:21]
	v_mfma_i32_16x16x64_i8 v[62:65], v[158:161], v[190:193], v[62:65]
	v_mfma_i32_16x16x64_i8 v[58:61], v[154:157], v[190:193], v[58:61]
	v_mfma_i32_16x16x64_i8 v[54:57], v[158:161], v[182:185], v[54:57]
	v_mfma_i32_16x16x64_i8 v[50:53], v[154:157], v[182:185], v[50:53]
	v_mfma_i32_16x16x64_i8 v[38:41], v[158:161], v[174:177], v[38:41]
	v_mfma_i32_16x16x64_i8 v[34:37], v[154:157], v[174:177], v[34:37]
	v_mfma_i32_16x16x64_i8 v[22:25], v[158:161], v[166:169], v[22:25]
	v_mfma_i32_16x16x64_i8 v[18:21], v[154:157], v[166:169], v[18:21]
	v_mfma_i32_16x16x64_i8 v[46:49], v[130:133], v[186:189], v[46:49]
	v_mfma_i32_16x16x64_i8 v[42:45], v[134:137], v[186:189], v[42:45]
	v_mfma_i32_16x16x64_i8 v[30:33], v[130:133], v[178:181], v[30:33]
	v_mfma_i32_16x16x64_i8 v[26:29], v[134:137], v[178:181], v[26:29]
	v_mfma_i32_16x16x64_i8 v[14:17], v[130:133], v[170:173], v[14:17]
	v_mfma_i32_16x16x64_i8 v[10:13], v[134:137], v[170:173], v[10:13]
	v_mfma_i32_16x16x64_i8 v[6:9], v[130:133], v[162:165], v[6:9]
	v_mfma_i32_16x16x64_i8 v[2:5], v[134:137], v[162:165], v[2:5]
	v_mfma_i32_16x16x64_i8 v[46:49], v[142:145], v[190:193], v[46:49]
	v_mfma_i32_16x16x64_i8 v[42:45], v[138:141], v[190:193], v[42:45]
	v_mfma_i32_16x16x64_i8 v[30:33], v[142:145], v[182:185], v[30:33]
	v_mfma_i32_16x16x64_i8 v[26:29], v[138:141], v[182:185], v[26:29]
	v_mfma_i32_16x16x64_i8 v[14:17], v[142:145], v[174:177], v[14:17]
	v_mfma_i32_16x16x64_i8 v[10:13], v[138:141], v[174:177], v[10:13]
	v_mfma_i32_16x16x64_i8 v[6:9], v[142:145], v[166:169], v[6:9]
	v_mfma_i32_16x16x64_i8 v[2:5], v[138:141], v[166:169], v[2:5]
	s_barrier
	s_add_i32 s39, 0, 0x18000
	s_add_i32 s65, 0, 0x1c000
	v_add_u32_e32 v134, s39, v230
	v_add_u32_e32 v142, s39, v231
	v_add_u32_e32 v150, s65, v230
	v_add_u32_e32 v158, s65, v231
	ds_read_b128 v[130:133], v134
	ds_read_b128 v[134:137], v134 offset:2048
	ds_read_b128 v[138:141], v142
	ds_read_b128 v[142:145], v142 offset:2048
	ds_read_b128 v[146:149], v150
	ds_read_b128 v[150:153], v150 offset:2048
	ds_read_b128 v[154:157], v158
	ds_read_b128 v[158:161], v158 offset:2048
	s_add_u32 s34, s34, 0x40000
	s_addc_u32 s35, s35, 0
	s_mov_b32 m0, s50
	v_lshl_add_u64 v[234:235], s[34:35], 0, v[194:195]
	ds_read_b128 v[162:165], v227 offset:32768
	ds_read_b128 v[166:169], v227 offset:33792
	ds_read_b128 v[170:173], v227 offset:34816
	ds_read_b128 v[174:177], v227 offset:35840
	ds_read_b128 v[178:181], v227 offset:36864
	ds_read_b128 v[182:185], v227 offset:37888
	ds_read_b128 v[186:189], v227 offset:38912
	ds_read_b128 v[190:193], v227 offset:39936
	global_load_lds_dwordx4 v[234:235], off
	v_lshl_add_u64 v[234:235], s[34:35], 0, v[196:197]
	s_mov_b32 m0, s51
	s_nop 0
	global_load_lds_dwordx4 v[234:235], off
	s_waitcnt vmcnt(8)
	s_waitcnt lgkmcnt(0)
	s_barrier
	s_waitcnt lgkmcnt(0)
	v_mfma_i32_16x16x64_i8 v[126:129], v[130:133], v[162:165], v[126:129]
	v_mfma_i32_16x16x64_i8 v[122:125], v[134:137], v[162:165], v[122:125]
	v_mfma_i32_16x16x64_i8 v[118:121], v[130:133], v[170:173], v[118:121]
	v_mfma_i32_16x16x64_i8 v[114:117], v[134:137], v[170:173], v[114:117]
	v_mfma_i32_16x16x64_i8 v[102:105], v[130:133], v[178:181], v[102:105]
	v_mfma_i32_16x16x64_i8 v[98:101], v[134:137], v[178:181], v[98:101]
	v_mfma_i32_16x16x64_i8 v[86:89], v[130:133], v[186:189], v[86:89]
	v_mfma_i32_16x16x64_i8 v[82:85], v[134:137], v[186:189], v[82:85]
	v_mfma_i32_16x16x64_i8 v[126:129], v[138:141], v[166:169], v[126:129]
	v_mfma_i32_16x16x64_i8 v[122:125], v[142:145], v[166:169], v[122:125]
	v_mfma_i32_16x16x64_i8 v[118:121], v[138:141], v[174:177], v[118:121]
	v_mfma_i32_16x16x64_i8 v[114:117], v[142:145], v[174:177], v[114:117]
	v_mfma_i32_16x16x64_i8 v[102:105], v[138:141], v[182:185], v[102:105]
	v_mfma_i32_16x16x64_i8 v[98:101], v[142:145], v[182:185], v[98:101]
	v_mfma_i32_16x16x64_i8 v[86:89], v[138:141], v[190:193], v[86:89]
	v_mfma_i32_16x16x64_i8 v[82:85], v[142:145], v[190:193], v[82:85]
	v_mfma_i32_16x16x64_i8 v[110:113], v[146:149], v[162:165], v[110:113]
	v_mfma_i32_16x16x64_i8 v[106:109], v[150:153], v[162:165], v[106:109]
	v_mfma_i32_16x16x64_i8 v[94:97], v[146:149], v[170:173], v[94:97]
	v_mfma_i32_16x16x64_i8 v[90:93], v[150:153], v[170:173], v[90:93]
	v_mfma_i32_16x16x64_i8 v[78:81], v[146:149], v[178:181], v[78:81]
	v_mfma_i32_16x16x64_i8 v[74:77], v[150:153], v[178:181], v[74:77]
	v_mfma_i32_16x16x64_i8 v[70:73], v[146:149], v[186:189], v[70:73]
	v_mfma_i32_16x16x64_i8 v[66:69], v[150:153], v[186:189], v[66:69]
	v_mfma_i32_16x16x64_i8 v[110:113], v[154:157], v[166:169], v[110:113]
	v_mfma_i32_16x16x64_i8 v[106:109], v[158:161], v[166:169], v[106:109]
	v_mfma_i32_16x16x64_i8 v[94:97], v[154:157], v[174:177], v[94:97]
	v_mfma_i32_16x16x64_i8 v[90:93], v[158:161], v[174:177], v[90:93]
	v_mfma_i32_16x16x64_i8 v[78:81], v[154:157], v[182:185], v[78:81]
	v_mfma_i32_16x16x64_i8 v[74:77], v[158:161], v[182:185], v[74:77]
	v_mfma_i32_16x16x64_i8 v[70:73], v[154:157], v[190:193], v[70:73]
	v_mfma_i32_16x16x64_i8 v[66:69], v[158:161], v[190:193], v[66:69]
	s_barrier
	s_add_i32 s34, s39, s42
	v_lshl_add_u64 v[234:235], s[36:37], 0, v[198:199]
	s_mov_b32 m0, s34
	ds_read_b128 v[162:165], v227 offset:49152
	ds_read_b128 v[166:169], v227 offset:50176
	ds_read_b128 v[170:173], v227 offset:51200
	ds_read_b128 v[174:177], v227 offset:52224
	ds_read_b128 v[178:181], v227 offset:53248
	ds_read_b128 v[182:185], v227 offset:54272
	ds_read_b128 v[186:189], v227 offset:55296
	ds_read_b128 v[190:193], v227 offset:56320
	global_load_lds_dwordx4 v[234:235], off
	s_add_i32 m0, s34, 0x2000
	s_add_u32 s30, s30, 0x9000
	v_lshl_add_u64 v[234:235], s[36:37], 0, v[200:201]
	s_addc_u32 s31, s31, 0
	s_add_i32 s34, s65, s42
	global_load_lds_dwordx4 v[234:235], off
	v_lshl_add_u64 v[234:235], s[30:31], 0, v[198:199]
	s_mov_b32 m0, s34
	v_lshl_add_u64 v[214:215], v[214:215], 0, s[2:3]
	global_load_lds_dwordx4 v[234:235], off
	v_lshl_add_u64 v[234:235], s[30:31], 0, v[200:201]
	s_add_i32 m0, s34, 0x2000
	s_nop 0
	global_load_lds_dwordx4 v[234:235], off
	s_mov_b32 m0, s52
	s_nop 0
	global_load_lds_dwordx4 v[214:215], off
	v_lshl_add_u64 v[214:215], v[216:217], 0, s[2:3]
	s_mov_b32 m0, s53
	s_nop 0
	global_load_lds_dwordx4 v[214:215], off
	s_waitcnt vmcnt(8)
	s_waitcnt lgkmcnt(0)
	s_barrier
	s_waitcnt lgkmcnt(0)
	v_mfma_i32_16x16x64_i8 v[62:65], v[130:133], v[162:165], v[62:65]
	v_mfma_i32_16x16x64_i8 v[58:61], v[134:137], v[162:165], v[58:61]
	v_mfma_i32_16x16x64_i8 v[54:57], v[130:133], v[170:173], v[54:57]
	v_mfma_i32_16x16x64_i8 v[50:53], v[134:137], v[170:173], v[50:53]
	v_mfma_i32_16x16x64_i8 v[38:41], v[130:133], v[178:181], v[38:41]
	v_mfma_i32_16x16x64_i8 v[34:37], v[134:137], v[178:181], v[34:37]
	v_mfma_i32_16x16x64_i8 v[22:25], v[130:133], v[186:189], v[22:25]
	v_mfma_i32_16x16x64_i8 v[18:21], v[134:137], v[186:189], v[18:21]
	v_mfma_i32_16x16x64_i8 v[62:65], v[138:141], v[166:169], v[62:65]
	v_mfma_i32_16x16x64_i8 v[58:61], v[142:145], v[166:169], v[58:61]
	v_mfma_i32_16x16x64_i8 v[54:57], v[138:141], v[174:177], v[54:57]
	v_mfma_i32_16x16x64_i8 v[50:53], v[142:145], v[174:177], v[50:53]
	v_mfma_i32_16x16x64_i8 v[38:41], v[138:141], v[182:185], v[38:41]
	v_mfma_i32_16x16x64_i8 v[34:37], v[142:145], v[182:185], v[34:37]
	v_mfma_i32_16x16x64_i8 v[22:25], v[138:141], v[190:193], v[22:25]
	v_mfma_i32_16x16x64_i8 v[18:21], v[142:145], v[190:193], v[18:21]
	v_mfma_i32_16x16x64_i8 v[46:49], v[146:149], v[162:165], v[46:49]
	v_mfma_i32_16x16x64_i8 v[42:45], v[150:153], v[162:165], v[42:45]
	v_mfma_i32_16x16x64_i8 v[30:33], v[146:149], v[170:173], v[30:33]
	v_mfma_i32_16x16x64_i8 v[26:29], v[150:153], v[170:173], v[26:29]
	v_mfma_i32_16x16x64_i8 v[14:17], v[146:149], v[178:181], v[14:17]
	v_mfma_i32_16x16x64_i8 v[10:13], v[150:153], v[178:181], v[10:13]
	v_mfma_i32_16x16x64_i8 v[6:9], v[146:149], v[186:189], v[6:9]
	v_mfma_i32_16x16x64_i8 v[2:5], v[150:153], v[186:189], v[2:5]
	v_mfma_i32_16x16x64_i8 v[46:49], v[154:157], v[166:169], v[46:49]
	v_mfma_i32_16x16x64_i8 v[42:45], v[158:161], v[166:169], v[42:45]
	v_mfma_i32_16x16x64_i8 v[30:33], v[154:157], v[174:177], v[30:33]
	v_mfma_i32_16x16x64_i8 v[26:29], v[158:161], v[174:177], v[26:29]
	v_mfma_i32_16x16x64_i8 v[14:17], v[154:157], v[182:185], v[14:17]
	v_mfma_i32_16x16x64_i8 v[10:13], v[158:161], v[182:185], v[10:13]
	v_mfma_i32_16x16x64_i8 v[6:9], v[154:157], v[190:193], v[6:9]
	v_mfma_i32_16x16x64_i8 v[2:5], v[158:161], v[190:193], v[2:5]
	s_barrier
	s_add_u32 s63, s63, 0x10000
	s_addc_u32 s64, s64, 0
	s_add_u32 s28, s28, 0x100
	s_addc_u32 s29, s29, 0
	s_cmp_gt_u32 s62, 13
	s_mov_b32 s62, s38
	s_cbranch_scc1 .LBB0_601

.LBB0_597:
	s_add_u32 s30, s26, s28
	s_addc_u32 s31, s27, s29
	s_add_u32 s30, s30, 0x100
	s_addc_u32 s31, s31, 0
	s_waitcnt lgkmcnt(0)
	s_cmpk_eq_i32 s28, 0x700
	s_cselect_b32 s35, s15, s31
	s_cselect_b32 s34, s25, s30
	s_cselect_b32 s31, s13, s64
	s_cselect_b32 s30, s60, s63
	s_barrier
	s_waitcnt lgkmcnt(0)
	v_mfma_i32_16x16x64_i8 v[126:129], v[146:149], v[186:189], v[126:129]
	v_mfma_i32_16x16x64_i8 v[122:125], v[150:153], v[186:189], v[122:125]
	v_mfma_i32_16x16x64_i8 v[118:121], v[146:149], v[178:181], v[118:121]
	v_mfma_i32_16x16x64_i8 v[114:117], v[150:153], v[178:181], v[114:117]
	v_mfma_i32_16x16x64_i8 v[102:105], v[146:149], v[170:173], v[102:105]
	v_mfma_i32_16x16x64_i8 v[98:101], v[150:153], v[170:173], v[98:101]
	v_mfma_i32_16x16x64_i8 v[86:89], v[146:149], v[162:165], v[86:89]
	v_mfma_i32_16x16x64_i8 v[82:85], v[150:153], v[162:165], v[82:85]
	v_mfma_i32_16x16x64_i8 v[126:129], v[158:161], v[190:193], v[126:129]
	v_mfma_i32_16x16x64_i8 v[122:125], v[154:157], v[190:193], v[122:125]
	v_mfma_i32_16x16x64_i8 v[118:121], v[158:161], v[182:185], v[118:121]
	v_mfma_i32_16x16x64_i8 v[114:117], v[154:157], v[182:185], v[114:117]
	v_mfma_i32_16x16x64_i8 v[102:105], v[158:161], v[174:177], v[102:105]
	v_mfma_i32_16x16x64_i8 v[98:101], v[154:157], v[174:177], v[98:101]
	v_mfma_i32_16x16x64_i8 v[86:89], v[158:161], v[166:169], v[86:89]
	v_mfma_i32_16x16x64_i8 v[82:85], v[154:157], v[166:169], v[82:85]
	v_mfma_i32_16x16x64_i8 v[110:113], v[130:133], v[186:189], v[110:113]
	v_mfma_i32_16x16x64_i8 v[106:109], v[134:137], v[186:189], v[106:109]
	v_mfma_i32_16x16x64_i8 v[94:97], v[130:133], v[178:181], v[94:97]
	v_mfma_i32_16x16x64_i8 v[90:93], v[134:137], v[178:181], v[90:93]
	v_mfma_i32_16x16x64_i8 v[78:81], v[130:133], v[170:173], v[78:81]
	v_mfma_i32_16x16x64_i8 v[74:77], v[134:137], v[170:173], v[74:77]
	v_mfma_i32_16x16x64_i8 v[70:73], v[130:133], v[162:165], v[70:73]
	v_mfma_i32_16x16x64_i8 v[66:69], v[134:137], v[162:165], v[66:69]
	v_mfma_i32_16x16x64_i8 v[110:113], v[142:145], v[190:193], v[110:113]
	v_mfma_i32_16x16x64_i8 v[106:109], v[138:141], v[190:193], v[106:109]
	v_mfma_i32_16x16x64_i8 v[94:97], v[142:145], v[182:185], v[94:97]
	v_mfma_i32_16x16x64_i8 v[90:93], v[138:141], v[182:185], v[90:93]
	v_mfma_i32_16x16x64_i8 v[78:81], v[142:145], v[174:177], v[78:81]
	v_mfma_i32_16x16x64_i8 v[74:77], v[138:141], v[174:177], v[74:77]
	v_mfma_i32_16x16x64_i8 v[70:73], v[142:145], v[166:169], v[70:73]
	v_mfma_i32_16x16x64_i8 v[66:69], v[138:141], v[166:169], v[66:69]
	s_barrier
	s_mov_b32 m0, s44
	v_lshl_add_u64 v[214:215], s[30:31], 0, v[198:199]
	s_add_u32 s38, s30, 0x1000
	ds_read_b128 v[186:189], v227 offset:16384
	ds_read_b128 v[190:193], v227 offset:17408
	ds_read_b128 v[178:181], v227 offset:18432
	ds_read_b128 v[182:185], v227 offset:19456
	ds_read_b128 v[170:173], v227 offset:20480
	ds_read_b128 v[174:177], v227 offset:21504
	ds_read_b128 v[162:165], v227 offset:22528
	ds_read_b128 v[166:169], v227 offset:23552
	global_load_lds_dwordx4 v[214:215], off
	v_lshl_add_u64 v[214:215], s[30:31], 0, v[200:201]
	s_mov_b32 m0, s45
	s_addc_u32 s39, s31, 0
	global_load_lds_dwordx4 v[214:215], off
	v_lshl_add_u64 v[214:215], s[38:39], 0, v[198:199]
	s_mov_b32 m0, s47
	v_lshl_add_u64 v[216:217], s[34:35], 0, v[196:197]
	global_load_lds_dwordx4 v[214:215], off
	v_lshl_add_u64 v[214:215], s[38:39], 0, v[200:201]
	s_mov_b32 m0, s48
	s_mov_b64 s[38:39], -1
	global_load_lds_dwordx4 v[214:215], off
	v_lshl_add_u64 v[214:215], s[34:35], 0, v[194:195]
	s_mov_b32 m0, s23
	s_and_b64 vcc, exec, s[36:37]
	global_load_lds_dwordx4 v[214:215], off
	s_mov_b32 m0, s49
	s_nop 0
	global_load_lds_dwordx4 v[216:217], off
	s_cbranch_vccz .LBB0_599
	s_waitcnt vmcnt(8)
	s_mov_b64 s[38:39], 0

.LBB0_750:
	s_waitcnt lgkmcnt(0)
	s_add_i32 s34, s55, 2
	s_add_u32 s30, s26, 0x8000
	s_addc_u32 s31, s27, 0
	s_barrier
	s_waitcnt lgkmcnt(0)
	v_mfma_f32_16x16x32_bf16 v[62:65], v[146:149], v[186:189], v[62:65]
	v_mfma_f32_16x16x32_bf16 v[58:61], v[150:153], v[186:189], v[58:61]
	v_mfma_f32_16x16x32_bf16 v[46:49], v[146:149], v[178:181], v[46:49]
	v_mfma_f32_16x16x32_bf16 v[42:45], v[150:153], v[178:181], v[42:45]
	v_mfma_f32_16x16x32_bf16 v[30:33], v[146:149], v[170:173], v[30:33]
	v_mfma_f32_16x16x32_bf16 v[26:29], v[150:153], v[170:173], v[26:29]
	v_mfma_f32_16x16x32_bf16 v[14:17], v[146:149], v[162:165], v[14:17]
	v_mfma_f32_16x16x32_bf16 v[10:13], v[150:153], v[162:165], v[10:13]
	v_mfma_f32_16x16x32_bf16 v[62:65], v[158:161], v[190:193], v[62:65]
	v_mfma_f32_16x16x32_bf16 v[58:61], v[154:157], v[190:193], v[58:61]
	v_mfma_f32_16x16x32_bf16 v[46:49], v[158:161], v[182:185], v[46:49]
	v_mfma_f32_16x16x32_bf16 v[42:45], v[154:157], v[182:185], v[42:45]
	v_mfma_f32_16x16x32_bf16 v[30:33], v[158:161], v[174:177], v[30:33]
	v_mfma_f32_16x16x32_bf16 v[26:29], v[154:157], v[174:177], v[26:29]
	v_mfma_f32_16x16x32_bf16 v[14:17], v[158:161], v[166:169], v[14:17]
	v_mfma_f32_16x16x32_bf16 v[10:13], v[154:157], v[166:169], v[10:13]
	v_mfma_f32_16x16x32_bf16 v[54:57], v[66:69], v[186:189], v[54:57]
	v_mfma_f32_16x16x32_bf16 v[50:53], v[70:73], v[186:189], v[50:53]
	v_mfma_f32_16x16x32_bf16 v[38:41], v[66:69], v[178:181], v[38:41]
	v_mfma_f32_16x16x32_bf16 v[34:37], v[70:73], v[178:181], v[34:37]
	v_mfma_f32_16x16x32_bf16 v[22:25], v[66:69], v[170:173], v[22:25]
	v_mfma_f32_16x16x32_bf16 v[18:21], v[70:73], v[170:173], v[18:21]
	v_mfma_f32_16x16x32_bf16 v[6:9], v[66:69], v[162:165], v[6:9]
	v_mfma_f32_16x16x32_bf16 v[2:5], v[70:73], v[162:165], v[2:5]
	v_mfma_f32_16x16x32_bf16 v[54:57], v[78:81], v[190:193], v[54:57]
	v_mfma_f32_16x16x32_bf16 v[50:53], v[74:77], v[190:193], v[50:53]
	v_mfma_f32_16x16x32_bf16 v[38:41], v[78:81], v[182:185], v[38:41]
	v_mfma_f32_16x16x32_bf16 v[34:37], v[74:77], v[182:185], v[34:37]
	v_mfma_f32_16x16x32_bf16 v[22:25], v[78:81], v[174:177], v[22:25]
	v_mfma_f32_16x16x32_bf16 v[18:21], v[74:77], v[174:177], v[18:21]
	v_mfma_f32_16x16x32_bf16 v[6:9], v[78:81], v[166:169], v[6:9]
	v_mfma_f32_16x16x32_bf16 v[2:5], v[74:77], v[166:169], v[2:5]
	s_barrier
	s_add_i32 s35, 0, 0x18000
	s_add_i32 s58, 0, 0x1c000
	v_add_u32_e32 v70, s35, v219
	v_add_u32_e32 v78, s35, v220
	v_add_u32_e32 v150, s58, v219
	v_add_u32_e32 v158, s58, v220
	ds_read_b128 v[66:69], v70
	ds_read_b128 v[70:73], v70 offset:2048
	ds_read_b128 v[74:77], v78
	ds_read_b128 v[78:81], v78 offset:2048
	ds_read_b128 v[146:149], v150
	ds_read_b128 v[150:153], v150 offset:2048
	ds_read_b128 v[154:157], v158
	ds_read_b128 v[158:161], v158 offset:2048
	s_add_u32 s28, s28, 0x80000
	s_addc_u32 s29, s29, 0
	s_mov_b32 m0, s47
	v_lshl_add_u64 v[228:229], s[28:29], 0, v[194:195]
	ds_read_b128 v[162:165], v226 offset:32768
	ds_read_b128 v[166:169], v226 offset:33792
	ds_read_b128 v[170:173], v226 offset:34816
	ds_read_b128 v[174:177], v226 offset:35840
	ds_read_b128 v[178:181], v226 offset:36864
	ds_read_b128 v[182:185], v226 offset:37888
	ds_read_b128 v[186:189], v226 offset:38912
	ds_read_b128 v[190:193], v226 offset:39936
	global_load_lds_dwordx4 v[228:229], off
	v_lshl_add_u64 v[228:229], s[28:29], 0, v[198:199]
	s_mov_b32 m0, s48
	s_nop 0
	global_load_lds_dwordx4 v[228:229], off
	s_waitcnt vmcnt(8)
	s_waitcnt lgkmcnt(0)
	s_barrier
	s_waitcnt lgkmcnt(0)
	v_mfma_f32_16x16x32_bf16 v[142:145], v[66:69], v[162:165], v[142:145]
	v_mfma_f32_16x16x32_bf16 v[138:141], v[70:73], v[162:165], v[138:141]
	v_mfma_f32_16x16x32_bf16 v[126:129], v[66:69], v[170:173], v[126:129]
	v_mfma_f32_16x16x32_bf16 v[122:125], v[70:73], v[170:173], v[122:125]
	v_mfma_f32_16x16x32_bf16 v[110:113], v[66:69], v[178:181], v[110:113]
	v_mfma_f32_16x16x32_bf16 v[106:109], v[70:73], v[178:181], v[106:109]
	v_mfma_f32_16x16x32_bf16 v[94:97], v[66:69], v[186:189], v[94:97]
	v_mfma_f32_16x16x32_bf16 v[90:93], v[70:73], v[186:189], v[90:93]
	v_mfma_f32_16x16x32_bf16 v[142:145], v[74:77], v[166:169], v[142:145]
	v_mfma_f32_16x16x32_bf16 v[138:141], v[78:81], v[166:169], v[138:141]
	v_mfma_f32_16x16x32_bf16 v[126:129], v[74:77], v[174:177], v[126:129]
	v_mfma_f32_16x16x32_bf16 v[122:125], v[78:81], v[174:177], v[122:125]
	v_mfma_f32_16x16x32_bf16 v[110:113], v[74:77], v[182:185], v[110:113]
	v_mfma_f32_16x16x32_bf16 v[106:109], v[78:81], v[182:185], v[106:109]
	v_mfma_f32_16x16x32_bf16 v[94:97], v[74:77], v[190:193], v[94:97]
	v_mfma_f32_16x16x32_bf16 v[90:93], v[78:81], v[190:193], v[90:93]
	v_mfma_f32_16x16x32_bf16 v[134:137], v[146:149], v[162:165], v[134:137]
	v_mfma_f32_16x16x32_bf16 v[130:133], v[150:153], v[162:165], v[130:133]
	v_mfma_f32_16x16x32_bf16 v[118:121], v[146:149], v[170:173], v[118:121]
	v_mfma_f32_16x16x32_bf16 v[114:117], v[150:153], v[170:173], v[114:117]
	v_mfma_f32_16x16x32_bf16 v[102:105], v[146:149], v[178:181], v[102:105]
	v_mfma_f32_16x16x32_bf16 v[98:101], v[150:153], v[178:181], v[98:101]
	v_mfma_f32_16x16x32_bf16 v[86:89], v[146:149], v[186:189], v[86:89]
	v_mfma_f32_16x16x32_bf16 v[82:85], v[150:153], v[186:189], v[82:85]
	v_mfma_f32_16x16x32_bf16 v[134:137], v[154:157], v[166:169], v[134:137]
	v_mfma_f32_16x16x32_bf16 v[130:133], v[158:161], v[166:169], v[130:133]
	v_mfma_f32_16x16x32_bf16 v[118:121], v[154:157], v[174:177], v[118:121]
	v_mfma_f32_16x16x32_bf16 v[114:117], v[158:161], v[174:177], v[114:117]
	v_mfma_f32_16x16x32_bf16 v[102:105], v[154:157], v[182:185], v[102:105]
	v_mfma_f32_16x16x32_bf16 v[98:101], v[158:161], v[182:185], v[98:101]
	v_mfma_f32_16x16x32_bf16 v[86:89], v[154:157], v[190:193], v[86:89]
	v_mfma_f32_16x16x32_bf16 v[82:85], v[158:161], v[190:193], v[82:85]
	s_barrier
	s_add_i32 s28, s35, s36
	v_lshl_add_u64 v[228:229], s[30:31], 0, v[196:197]
	s_mov_b32 m0, s28
	ds_read_b128 v[162:165], v226 offset:49152
	ds_read_b128 v[166:169], v226 offset:50176
	ds_read_b128 v[170:173], v226 offset:51200
	ds_read_b128 v[174:177], v226 offset:52224
	ds_read_b128 v[178:181], v226 offset:53248
	ds_read_b128 v[182:185], v226 offset:54272
	ds_read_b128 v[186:189], v226 offset:55296
	ds_read_b128 v[190:193], v226 offset:56320
	global_load_lds_dwordx4 v[228:229], off
	s_add_i32 m0, s28, 0x2000
	s_add_u32 s26, s26, 0x9000
	v_lshl_add_u64 v[228:229], s[30:31], 0, v[200:201]
	s_addc_u32 s27, s27, 0
	s_add_i32 s28, s58, s36
	global_load_lds_dwordx4 v[228:229], off
	v_lshl_add_u64 v[228:229], s[26:27], 0, v[196:197]
	s_mov_b32 m0, s28
	v_lshl_add_u64 v[210:211], v[210:211], 0, s[8:9]
	global_load_lds_dwordx4 v[228:229], off
	v_lshl_add_u64 v[228:229], s[26:27], 0, v[200:201]
	s_add_i32 m0, s28, 0x2000
	s_nop 0
	global_load_lds_dwordx4 v[228:229], off
	s_mov_b32 m0, s49
	s_nop 0
	global_load_lds_dwordx4 v[210:211], off
	v_lshl_add_u64 v[210:211], v[212:213], 0, s[8:9]
	s_mov_b32 m0, s50
	s_nop 0
	global_load_lds_dwordx4 v[210:211], off
	s_waitcnt vmcnt(8)
	s_waitcnt lgkmcnt(0)
	s_barrier
	s_waitcnt lgkmcnt(0)
	v_mfma_f32_16x16x32_bf16 v[62:65], v[66:69], v[162:165], v[62:65]
	v_mfma_f32_16x16x32_bf16 v[58:61], v[70:73], v[162:165], v[58:61]
	v_mfma_f32_16x16x32_bf16 v[46:49], v[66:69], v[170:173], v[46:49]
	v_mfma_f32_16x16x32_bf16 v[42:45], v[70:73], v[170:173], v[42:45]
	v_mfma_f32_16x16x32_bf16 v[30:33], v[66:69], v[178:181], v[30:33]
	v_mfma_f32_16x16x32_bf16 v[26:29], v[70:73], v[178:181], v[26:29]
	v_mfma_f32_16x16x32_bf16 v[14:17], v[66:69], v[186:189], v[14:17]
	v_mfma_f32_16x16x32_bf16 v[10:13], v[70:73], v[186:189], v[10:13]
	v_mfma_f32_16x16x32_bf16 v[62:65], v[74:77], v[166:169], v[62:65]
	v_mfma_f32_16x16x32_bf16 v[58:61], v[78:81], v[166:169], v[58:61]
	v_mfma_f32_16x16x32_bf16 v[46:49], v[74:77], v[174:177], v[46:49]
	v_mfma_f32_16x16x32_bf16 v[42:45], v[78:81], v[174:177], v[42:45]
	v_mfma_f32_16x16x32_bf16 v[30:33], v[74:77], v[182:185], v[30:33]
	v_mfma_f32_16x16x32_bf16 v[26:29], v[78:81], v[182:185], v[26:29]
	v_mfma_f32_16x16x32_bf16 v[14:17], v[74:77], v[190:193], v[14:17]
	v_mfma_f32_16x16x32_bf16 v[10:13], v[78:81], v[190:193], v[10:13]
	v_mfma_f32_16x16x32_bf16 v[54:57], v[146:149], v[162:165], v[54:57]
	v_mfma_f32_16x16x32_bf16 v[50:53], v[150:153], v[162:165], v[50:53]
	v_mfma_f32_16x16x32_bf16 v[38:41], v[146:149], v[170:173], v[38:41]
	v_mfma_f32_16x16x32_bf16 v[34:37], v[150:153], v[170:173], v[34:37]
	v_mfma_f32_16x16x32_bf16 v[22:25], v[146:149], v[178:181], v[22:25]
	v_mfma_f32_16x16x32_bf16 v[18:21], v[150:153], v[178:181], v[18:21]
	v_mfma_f32_16x16x32_bf16 v[6:9], v[146:149], v[186:189], v[6:9]
	v_mfma_f32_16x16x32_bf16 v[2:5], v[150:153], v[186:189], v[2:5]
	v_mfma_f32_16x16x32_bf16 v[54:57], v[154:157], v[166:169], v[54:57]
	v_mfma_f32_16x16x32_bf16 v[50:53], v[158:161], v[166:169], v[50:53]
	v_mfma_f32_16x16x32_bf16 v[38:41], v[154:157], v[174:177], v[38:41]
	v_mfma_f32_16x16x32_bf16 v[34:37], v[158:161], v[174:177], v[34:37]
	v_mfma_f32_16x16x32_bf16 v[22:25], v[154:157], v[182:185], v[22:25]
	v_mfma_f32_16x16x32_bf16 v[18:21], v[158:161], v[182:185], v[18:21]
	v_mfma_f32_16x16x32_bf16 v[6:9], v[154:157], v[190:193], v[6:9]
	v_mfma_f32_16x16x32_bf16 v[2:5], v[158:161], v[190:193], v[2:5]
	s_barrier
	s_add_u32 s56, s56, 0x10000
	s_addc_u32 s57, s57, 0
	s_add_u32 s24, s24, 0x100
	s_addc_u32 s25, s25, 0
	s_cmp_gt_u32 s55, 29
	s_mov_b32 s55, s34
	s_cbranch_scc1 .LBB0_759

.LBB0_755:
	s_add_u32 s26, s22, s24
	s_addc_u32 s27, s23, s25
	s_add_u32 s26, s26, 0x100
	s_addc_u32 s27, s27, 0
	s_waitcnt lgkmcnt(0)
	s_cmpk_eq_i32 s24, 0xf00
	s_cselect_b32 s29, s15, s27
	s_cselect_b32 s28, s52, s26
	s_cselect_b32 s27, s13, s57
	s_cselect_b32 s26, s53, s56
	s_barrier
	s_waitcnt lgkmcnt(0)
	v_mfma_f32_16x16x32_bf16 v[142:145], v[146:149], v[186:189], v[142:145]
	v_mfma_f32_16x16x32_bf16 v[138:141], v[150:153], v[186:189], v[138:141]
	v_mfma_f32_16x16x32_bf16 v[126:129], v[146:149], v[178:181], v[126:129]
	v_mfma_f32_16x16x32_bf16 v[122:125], v[150:153], v[178:181], v[122:125]
	v_mfma_f32_16x16x32_bf16 v[110:113], v[146:149], v[170:173], v[110:113]
	v_mfma_f32_16x16x32_bf16 v[106:109], v[150:153], v[170:173], v[106:109]
	v_mfma_f32_16x16x32_bf16 v[94:97], v[146:149], v[162:165], v[94:97]
	v_mfma_f32_16x16x32_bf16 v[90:93], v[150:153], v[162:165], v[90:93]
	v_mfma_f32_16x16x32_bf16 v[142:145], v[158:161], v[190:193], v[142:145]
	v_mfma_f32_16x16x32_bf16 v[138:141], v[154:157], v[190:193], v[138:141]
	v_mfma_f32_16x16x32_bf16 v[126:129], v[158:161], v[182:185], v[126:129]
	v_mfma_f32_16x16x32_bf16 v[122:125], v[154:157], v[182:185], v[122:125]
	v_mfma_f32_16x16x32_bf16 v[110:113], v[158:161], v[174:177], v[110:113]
	v_mfma_f32_16x16x32_bf16 v[106:109], v[154:157], v[174:177], v[106:109]
	v_mfma_f32_16x16x32_bf16 v[94:97], v[158:161], v[166:169], v[94:97]
	v_mfma_f32_16x16x32_bf16 v[90:93], v[154:157], v[166:169], v[90:93]
	v_mfma_f32_16x16x32_bf16 v[134:137], v[66:69], v[186:189], v[134:137]
	v_mfma_f32_16x16x32_bf16 v[130:133], v[70:73], v[186:189], v[130:133]
	v_mfma_f32_16x16x32_bf16 v[118:121], v[66:69], v[178:181], v[118:121]
	v_mfma_f32_16x16x32_bf16 v[114:117], v[70:73], v[178:181], v[114:117]
	v_mfma_f32_16x16x32_bf16 v[102:105], v[66:69], v[170:173], v[102:105]
	v_mfma_f32_16x16x32_bf16 v[98:101], v[70:73], v[170:173], v[98:101]
	v_mfma_f32_16x16x32_bf16 v[86:89], v[66:69], v[162:165], v[86:89]
	v_mfma_f32_16x16x32_bf16 v[82:85], v[70:73], v[162:165], v[82:85]
	v_mfma_f32_16x16x32_bf16 v[134:137], v[78:81], v[190:193], v[134:137]
	v_mfma_f32_16x16x32_bf16 v[130:133], v[74:77], v[190:193], v[130:133]
	v_mfma_f32_16x16x32_bf16 v[118:121], v[78:81], v[182:185], v[118:121]
	v_mfma_f32_16x16x32_bf16 v[114:117], v[74:77], v[182:185], v[114:117]
	v_mfma_f32_16x16x32_bf16 v[102:105], v[78:81], v[174:177], v[102:105]
	v_mfma_f32_16x16x32_bf16 v[98:101], v[74:77], v[174:177], v[98:101]
	v_mfma_f32_16x16x32_bf16 v[86:89], v[78:81], v[166:169], v[86:89]
	v_mfma_f32_16x16x32_bf16 v[82:85], v[74:77], v[166:169], v[82:85]
	s_barrier
	s_mov_b32 m0, s38
	v_lshl_add_u64 v[210:211], s[26:27], 0, v[196:197]
	s_add_u32 s34, s26, 0x1000
	ds_read_b128 v[186:189], v226 offset:16384
	ds_read_b128 v[190:193], v226 offset:17408
	ds_read_b128 v[178:181], v226 offset:18432
	ds_read_b128 v[182:185], v226 offset:19456
	ds_read_b128 v[170:173], v226 offset:20480
	ds_read_b128 v[174:177], v226 offset:21504
	ds_read_b128 v[162:165], v226 offset:22528
	ds_read_b128 v[166:169], v226 offset:23552
	global_load_lds_dwordx4 v[210:211], off
	v_lshl_add_u64 v[210:211], s[26:27], 0, v[200:201]
	s_mov_b32 m0, s39
	s_addc_u32 s35, s27, 0
	global_load_lds_dwordx4 v[210:211], off
	v_lshl_add_u64 v[210:211], s[34:35], 0, v[196:197]
	s_mov_b32 m0, s40
	v_lshl_add_u64 v[212:213], s[28:29], 0, v[198:199]
	global_load_lds_dwordx4 v[210:211], off
	v_lshl_add_u64 v[210:211], s[34:35], 0, v[200:201]
	s_mov_b32 m0, s41
	s_mov_b64 s[34:35], -1
	global_load_lds_dwordx4 v[210:211], off
	v_lshl_add_u64 v[210:211], s[28:29], 0, v[194:195]
	s_mov_b32 m0, s37
	s_and_b64 vcc, exec, s[30:31]
	global_load_lds_dwordx4 v[210:211], off
	s_mov_b32 m0, s46
	s_nop 0
	global_load_lds_dwordx4 v[212:213], off
	s_cbranch_vccz .LBB0_757
	s_waitcnt vmcnt(8)
	s_mov_b64 s[34:35], 0

.LBB0_1051:
	s_waitcnt lgkmcnt(0)
	s_add_i32 s34, s55, 2
	s_add_u32 s30, s26, 0x8000
	s_addc_u32 s31, s27, 0
	s_barrier
	s_waitcnt lgkmcnt(0)
	v_mfma_f32_16x16x32_bf16 v[62:65], v[146:149], v[186:189], v[62:65]
	v_mfma_f32_16x16x32_bf16 v[58:61], v[150:153], v[186:189], v[58:61]
	v_mfma_f32_16x16x32_bf16 v[46:49], v[146:149], v[178:181], v[46:49]
	v_mfma_f32_16x16x32_bf16 v[42:45], v[150:153], v[178:181], v[42:45]
	v_mfma_f32_16x16x32_bf16 v[30:33], v[146:149], v[170:173], v[30:33]
	v_mfma_f32_16x16x32_bf16 v[26:29], v[150:153], v[170:173], v[26:29]
	v_mfma_f32_16x16x32_bf16 v[14:17], v[146:149], v[162:165], v[14:17]
	v_mfma_f32_16x16x32_bf16 v[10:13], v[150:153], v[162:165], v[10:13]
	v_mfma_f32_16x16x32_bf16 v[62:65], v[158:161], v[190:193], v[62:65]
	v_mfma_f32_16x16x32_bf16 v[58:61], v[154:157], v[190:193], v[58:61]
	v_mfma_f32_16x16x32_bf16 v[46:49], v[158:161], v[182:185], v[46:49]
	v_mfma_f32_16x16x32_bf16 v[42:45], v[154:157], v[182:185], v[42:45]
	v_mfma_f32_16x16x32_bf16 v[30:33], v[158:161], v[174:177], v[30:33]
	v_mfma_f32_16x16x32_bf16 v[26:29], v[154:157], v[174:177], v[26:29]
	v_mfma_f32_16x16x32_bf16 v[14:17], v[158:161], v[166:169], v[14:17]
	v_mfma_f32_16x16x32_bf16 v[10:13], v[154:157], v[166:169], v[10:13]
	v_mfma_f32_16x16x32_bf16 v[54:57], v[66:69], v[186:189], v[54:57]
	v_mfma_f32_16x16x32_bf16 v[50:53], v[70:73], v[186:189], v[50:53]
	v_mfma_f32_16x16x32_bf16 v[38:41], v[66:69], v[178:181], v[38:41]
	v_mfma_f32_16x16x32_bf16 v[34:37], v[70:73], v[178:181], v[34:37]
	v_mfma_f32_16x16x32_bf16 v[22:25], v[66:69], v[170:173], v[22:25]
	v_mfma_f32_16x16x32_bf16 v[18:21], v[70:73], v[170:173], v[18:21]
	v_mfma_f32_16x16x32_bf16 v[6:9], v[66:69], v[162:165], v[6:9]
	v_mfma_f32_16x16x32_bf16 v[2:5], v[70:73], v[162:165], v[2:5]
	v_mfma_f32_16x16x32_bf16 v[54:57], v[78:81], v[190:193], v[54:57]
	v_mfma_f32_16x16x32_bf16 v[50:53], v[74:77], v[190:193], v[50:53]
	v_mfma_f32_16x16x32_bf16 v[38:41], v[78:81], v[182:185], v[38:41]
	v_mfma_f32_16x16x32_bf16 v[34:37], v[74:77], v[182:185], v[34:37]
	v_mfma_f32_16x16x32_bf16 v[22:25], v[78:81], v[174:177], v[22:25]
	v_mfma_f32_16x16x32_bf16 v[18:21], v[74:77], v[174:177], v[18:21]
	v_mfma_f32_16x16x32_bf16 v[6:9], v[78:81], v[166:169], v[6:9]
	v_mfma_f32_16x16x32_bf16 v[2:5], v[74:77], v[166:169], v[2:5]
	s_barrier
	s_add_i32 s35, 0, 0x18000
	s_add_i32 s58, 0, 0x1c000
	v_add_u32_e32 v70, s35, v217
	v_add_u32_e32 v78, s35, v218
	v_add_u32_e32 v150, s58, v217
	v_add_u32_e32 v158, s58, v218
	ds_read_b128 v[66:69], v70
	ds_read_b128 v[70:73], v70 offset:2048
	ds_read_b128 v[74:77], v78
	ds_read_b128 v[78:81], v78 offset:2048
	ds_read_b128 v[146:149], v150
	ds_read_b128 v[150:153], v150 offset:2048
	ds_read_b128 v[154:157], v158
	ds_read_b128 v[158:161], v158 offset:2048
	s_add_u32 s28, s28, 0x80000
	s_addc_u32 s29, s29, 0
	s_mov_b32 m0, s48
	v_lshl_add_u64 v[224:225], s[28:29], 0, v[194:195]
	ds_read_b128 v[162:165], v223 offset:32768
	ds_read_b128 v[166:169], v223 offset:33792
	ds_read_b128 v[170:173], v223 offset:34816
	ds_read_b128 v[174:177], v223 offset:35840
	ds_read_b128 v[178:181], v223 offset:36864
	ds_read_b128 v[182:185], v223 offset:37888
	ds_read_b128 v[186:189], v223 offset:38912
	ds_read_b128 v[190:193], v223 offset:39936
	global_load_lds_dwordx4 v[224:225], off
	v_lshl_add_u64 v[224:225], s[28:29], 0, v[198:199]
	s_mov_b32 m0, s49
	s_nop 0
	global_load_lds_dwordx4 v[224:225], off
	s_waitcnt vmcnt(8)
	s_waitcnt lgkmcnt(0)
	s_barrier
	s_waitcnt lgkmcnt(0)
	v_mfma_f32_16x16x32_bf16 v[142:145], v[66:69], v[162:165], v[142:145]
	v_mfma_f32_16x16x32_bf16 v[138:141], v[70:73], v[162:165], v[138:141]
	v_mfma_f32_16x16x32_bf16 v[126:129], v[66:69], v[170:173], v[126:129]
	v_mfma_f32_16x16x32_bf16 v[122:125], v[70:73], v[170:173], v[122:125]
	v_mfma_f32_16x16x32_bf16 v[110:113], v[66:69], v[178:181], v[110:113]
	v_mfma_f32_16x16x32_bf16 v[106:109], v[70:73], v[178:181], v[106:109]
	v_mfma_f32_16x16x32_bf16 v[94:97], v[66:69], v[186:189], v[94:97]
	v_mfma_f32_16x16x32_bf16 v[90:93], v[70:73], v[186:189], v[90:93]
	v_mfma_f32_16x16x32_bf16 v[142:145], v[74:77], v[166:169], v[142:145]
	v_mfma_f32_16x16x32_bf16 v[138:141], v[78:81], v[166:169], v[138:141]
	v_mfma_f32_16x16x32_bf16 v[126:129], v[74:77], v[174:177], v[126:129]
	v_mfma_f32_16x16x32_bf16 v[122:125], v[78:81], v[174:177], v[122:125]
	v_mfma_f32_16x16x32_bf16 v[110:113], v[74:77], v[182:185], v[110:113]
	v_mfma_f32_16x16x32_bf16 v[106:109], v[78:81], v[182:185], v[106:109]
	v_mfma_f32_16x16x32_bf16 v[94:97], v[74:77], v[190:193], v[94:97]
	v_mfma_f32_16x16x32_bf16 v[90:93], v[78:81], v[190:193], v[90:93]
	v_mfma_f32_16x16x32_bf16 v[134:137], v[146:149], v[162:165], v[134:137]
	v_mfma_f32_16x16x32_bf16 v[130:133], v[150:153], v[162:165], v[130:133]
	v_mfma_f32_16x16x32_bf16 v[118:121], v[146:149], v[170:173], v[118:121]
	v_mfma_f32_16x16x32_bf16 v[114:117], v[150:153], v[170:173], v[114:117]
	v_mfma_f32_16x16x32_bf16 v[102:105], v[146:149], v[178:181], v[102:105]
	v_mfma_f32_16x16x32_bf16 v[98:101], v[150:153], v[178:181], v[98:101]
	v_mfma_f32_16x16x32_bf16 v[86:89], v[146:149], v[186:189], v[86:89]
	v_mfma_f32_16x16x32_bf16 v[82:85], v[150:153], v[186:189], v[82:85]
	v_mfma_f32_16x16x32_bf16 v[134:137], v[154:157], v[166:169], v[134:137]
	v_mfma_f32_16x16x32_bf16 v[130:133], v[158:161], v[166:169], v[130:133]
	v_mfma_f32_16x16x32_bf16 v[118:121], v[154:157], v[174:177], v[118:121]
	v_mfma_f32_16x16x32_bf16 v[114:117], v[158:161], v[174:177], v[114:117]
	v_mfma_f32_16x16x32_bf16 v[102:105], v[154:157], v[182:185], v[102:105]
	v_mfma_f32_16x16x32_bf16 v[98:101], v[158:161], v[182:185], v[98:101]
	v_mfma_f32_16x16x32_bf16 v[86:89], v[154:157], v[190:193], v[86:89]
	v_mfma_f32_16x16x32_bf16 v[82:85], v[158:161], v[190:193], v[82:85]
	s_barrier
	s_add_i32 s28, s35, s38
	v_lshl_add_u64 v[224:225], s[30:31], 0, v[196:197]
	s_mov_b32 m0, s28
	ds_read_b128 v[162:165], v223 offset:49152
	ds_read_b128 v[166:169], v223 offset:50176
	ds_read_b128 v[170:173], v223 offset:51200
	ds_read_b128 v[174:177], v223 offset:52224
	ds_read_b128 v[178:181], v223 offset:53248
	ds_read_b128 v[182:185], v223 offset:54272
	ds_read_b128 v[186:189], v223 offset:55296
	ds_read_b128 v[190:193], v223 offset:56320
	global_load_lds_dwordx4 v[224:225], off
	s_add_i32 m0, s28, 0x2000
	s_add_u32 s26, s26, 0x9000
	v_lshl_add_u64 v[224:225], s[30:31], 0, v[200:201]
	s_addc_u32 s27, s27, 0
	s_add_i32 s28, s58, s38
	global_load_lds_dwordx4 v[224:225], off
	v_lshl_add_u64 v[224:225], s[26:27], 0, v[196:197]
	s_mov_b32 m0, s28
	v_lshl_add_u64 v[212:213], v[212:213], 0, s[2:3]
	global_load_lds_dwordx4 v[224:225], off
	v_lshl_add_u64 v[224:225], s[26:27], 0, v[200:201]
	s_add_i32 m0, s28, 0x2000
	s_nop 0
	global_load_lds_dwordx4 v[224:225], off
	s_mov_b32 m0, s50
	s_nop 0
	global_load_lds_dwordx4 v[212:213], off
	v_lshl_add_u64 v[212:213], v[214:215], 0, s[2:3]
	s_mov_b32 m0, s51
	s_nop 0
	global_load_lds_dwordx4 v[212:213], off
	s_waitcnt vmcnt(8)
	s_waitcnt lgkmcnt(0)
	s_barrier
	s_waitcnt lgkmcnt(0)
	v_mfma_f32_16x16x32_bf16 v[62:65], v[66:69], v[162:165], v[62:65]
	v_mfma_f32_16x16x32_bf16 v[58:61], v[70:73], v[162:165], v[58:61]
	v_mfma_f32_16x16x32_bf16 v[46:49], v[66:69], v[170:173], v[46:49]
	v_mfma_f32_16x16x32_bf16 v[42:45], v[70:73], v[170:173], v[42:45]
	v_mfma_f32_16x16x32_bf16 v[30:33], v[66:69], v[178:181], v[30:33]
	v_mfma_f32_16x16x32_bf16 v[26:29], v[70:73], v[178:181], v[26:29]
	v_mfma_f32_16x16x32_bf16 v[14:17], v[66:69], v[186:189], v[14:17]
	v_mfma_f32_16x16x32_bf16 v[10:13], v[70:73], v[186:189], v[10:13]
	v_mfma_f32_16x16x32_bf16 v[62:65], v[74:77], v[166:169], v[62:65]
	v_mfma_f32_16x16x32_bf16 v[58:61], v[78:81], v[166:169], v[58:61]
	v_mfma_f32_16x16x32_bf16 v[46:49], v[74:77], v[174:177], v[46:49]
	v_mfma_f32_16x16x32_bf16 v[42:45], v[78:81], v[174:177], v[42:45]
	v_mfma_f32_16x16x32_bf16 v[30:33], v[74:77], v[182:185], v[30:33]
	v_mfma_f32_16x16x32_bf16 v[26:29], v[78:81], v[182:185], v[26:29]
	v_mfma_f32_16x16x32_bf16 v[14:17], v[74:77], v[190:193], v[14:17]
	v_mfma_f32_16x16x32_bf16 v[10:13], v[78:81], v[190:193], v[10:13]
	v_mfma_f32_16x16x32_bf16 v[54:57], v[146:149], v[162:165], v[54:57]
	v_mfma_f32_16x16x32_bf16 v[50:53], v[150:153], v[162:165], v[50:53]
	v_mfma_f32_16x16x32_bf16 v[38:41], v[146:149], v[170:173], v[38:41]
	v_mfma_f32_16x16x32_bf16 v[34:37], v[150:153], v[170:173], v[34:37]
	v_mfma_f32_16x16x32_bf16 v[22:25], v[146:149], v[178:181], v[22:25]
	v_mfma_f32_16x16x32_bf16 v[18:21], v[150:153], v[178:181], v[18:21]
	v_mfma_f32_16x16x32_bf16 v[6:9], v[146:149], v[186:189], v[6:9]
	v_mfma_f32_16x16x32_bf16 v[2:5], v[150:153], v[186:189], v[2:5]
	v_mfma_f32_16x16x32_bf16 v[54:57], v[154:157], v[166:169], v[54:57]
	v_mfma_f32_16x16x32_bf16 v[50:53], v[158:161], v[166:169], v[50:53]
	v_mfma_f32_16x16x32_bf16 v[38:41], v[154:157], v[174:177], v[38:41]
	v_mfma_f32_16x16x32_bf16 v[34:37], v[158:161], v[174:177], v[34:37]
	v_mfma_f32_16x16x32_bf16 v[22:25], v[154:157], v[182:185], v[22:25]
	v_mfma_f32_16x16x32_bf16 v[18:21], v[158:161], v[182:185], v[18:21]
	v_mfma_f32_16x16x32_bf16 v[6:9], v[154:157], v[190:193], v[6:9]
	v_mfma_f32_16x16x32_bf16 v[2:5], v[158:161], v[190:193], v[2:5]
	s_barrier
	s_add_u32 s56, s56, 0x10000
	s_addc_u32 s57, s57, 0
	s_add_u32 s24, s24, 0x100
	s_addc_u32 s25, s25, 0
	s_cmp_gt_u32 s55, 29
	s_mov_b32 s55, s34
	s_cbranch_scc1 .LBB0_1060

.LBB0_1056:
	s_add_u32 s26, s22, s24
	s_addc_u32 s27, s23, s25
	s_add_u32 s26, s26, 0x100
	s_addc_u32 s27, s27, 0
	s_waitcnt lgkmcnt(0)
	s_cmpk_eq_i32 s24, 0xf00
	s_cselect_b32 s29, s11, s27
	s_cselect_b32 s28, s19, s26
	s_cselect_b32 s27, s9, s57
	s_cselect_b32 s26, s53, s56
	s_barrier
	s_waitcnt lgkmcnt(0)
	v_mfma_f32_16x16x32_bf16 v[142:145], v[146:149], v[186:189], v[142:145]
	v_mfma_f32_16x16x32_bf16 v[138:141], v[150:153], v[186:189], v[138:141]
	v_mfma_f32_16x16x32_bf16 v[126:129], v[146:149], v[178:181], v[126:129]
	v_mfma_f32_16x16x32_bf16 v[122:125], v[150:153], v[178:181], v[122:125]
	v_mfma_f32_16x16x32_bf16 v[110:113], v[146:149], v[170:173], v[110:113]
	v_mfma_f32_16x16x32_bf16 v[106:109], v[150:153], v[170:173], v[106:109]
	v_mfma_f32_16x16x32_bf16 v[94:97], v[146:149], v[162:165], v[94:97]
	v_mfma_f32_16x16x32_bf16 v[90:93], v[150:153], v[162:165], v[90:93]
	v_mfma_f32_16x16x32_bf16 v[142:145], v[158:161], v[190:193], v[142:145]
	v_mfma_f32_16x16x32_bf16 v[138:141], v[154:157], v[190:193], v[138:141]
	v_mfma_f32_16x16x32_bf16 v[126:129], v[158:161], v[182:185], v[126:129]
	v_mfma_f32_16x16x32_bf16 v[122:125], v[154:157], v[182:185], v[122:125]
	v_mfma_f32_16x16x32_bf16 v[110:113], v[158:161], v[174:177], v[110:113]
	v_mfma_f32_16x16x32_bf16 v[106:109], v[154:157], v[174:177], v[106:109]
	v_mfma_f32_16x16x32_bf16 v[94:97], v[158:161], v[166:169], v[94:97]
	v_mfma_f32_16x16x32_bf16 v[90:93], v[154:157], v[166:169], v[90:93]
	v_mfma_f32_16x16x32_bf16 v[134:137], v[66:69], v[186:189], v[134:137]
	v_mfma_f32_16x16x32_bf16 v[130:133], v[70:73], v[186:189], v[130:133]
	v_mfma_f32_16x16x32_bf16 v[118:121], v[66:69], v[178:181], v[118:121]
	v_mfma_f32_16x16x32_bf16 v[114:117], v[70:73], v[178:181], v[114:117]
	v_mfma_f32_16x16x32_bf16 v[102:105], v[66:69], v[170:173], v[102:105]
	v_mfma_f32_16x16x32_bf16 v[98:101], v[70:73], v[170:173], v[98:101]
	v_mfma_f32_16x16x32_bf16 v[86:89], v[66:69], v[162:165], v[86:89]
	v_mfma_f32_16x16x32_bf16 v[82:85], v[70:73], v[162:165], v[82:85]
	v_mfma_f32_16x16x32_bf16 v[134:137], v[78:81], v[190:193], v[134:137]
	v_mfma_f32_16x16x32_bf16 v[130:133], v[74:77], v[190:193], v[130:133]
	v_mfma_f32_16x16x32_bf16 v[118:121], v[78:81], v[182:185], v[118:121]
	v_mfma_f32_16x16x32_bf16 v[114:117], v[74:77], v[182:185], v[114:117]
	v_mfma_f32_16x16x32_bf16 v[102:105], v[78:81], v[174:177], v[102:105]
	v_mfma_f32_16x16x32_bf16 v[98:101], v[74:77], v[174:177], v[98:101]
	v_mfma_f32_16x16x32_bf16 v[86:89], v[78:81], v[166:169], v[86:89]
	v_mfma_f32_16x16x32_bf16 v[82:85], v[74:77], v[166:169], v[82:85]
	s_barrier
	s_mov_b32 m0, s39
	v_lshl_add_u64 v[212:213], s[26:27], 0, v[196:197]
	s_add_u32 s34, s26, 0x1000
	ds_read_b128 v[186:189], v223 offset:16384
	ds_read_b128 v[190:193], v223 offset:17408
	ds_read_b128 v[178:181], v223 offset:18432
	ds_read_b128 v[182:185], v223 offset:19456
	ds_read_b128 v[170:173], v223 offset:20480
	ds_read_b128 v[174:177], v223 offset:21504
	ds_read_b128 v[162:165], v223 offset:22528
	ds_read_b128 v[166:169], v223 offset:23552
	global_load_lds_dwordx4 v[212:213], off
	v_lshl_add_u64 v[212:213], s[26:27], 0, v[200:201]
	s_mov_b32 m0, s40
	s_addc_u32 s35, s27, 0
	global_load_lds_dwordx4 v[212:213], off
	v_lshl_add_u64 v[212:213], s[34:35], 0, v[196:197]
	s_mov_b32 m0, s41
	v_lshl_add_u64 v[214:215], s[28:29], 0, v[198:199]
	global_load_lds_dwordx4 v[212:213], off
	v_lshl_add_u64 v[212:213], s[34:35], 0, v[200:201]
	s_mov_b32 m0, s46
	s_mov_b64 s[34:35], -1
	global_load_lds_dwordx4 v[212:213], off
	v_lshl_add_u64 v[212:213], s[28:29], 0, v[194:195]
	s_mov_b32 m0, s21
	s_and_b64 vcc, exec, s[30:31]
	global_load_lds_dwordx4 v[212:213], off
	s_mov_b32 m0, s47
	s_nop 0
	global_load_lds_dwordx4 v[214:215], off
	s_cbranch_vccz .LBB0_1058
	s_waitcnt vmcnt(8)
	s_mov_b64 s[34:35], 0

.LBB0_1184:
	s_waitcnt lgkmcnt(0)
	s_add_i32 s30, s59, 2
	s_add_u32 s28, s24, 0x8000
	s_addc_u32 s29, s25, 0
	s_barrier
	s_waitcnt lgkmcnt(0)
	v_mfma_i32_16x16x64_i8 v[62:65], v[146:149], v[186:189], v[62:65]
	v_mfma_i32_16x16x64_i8 v[58:61], v[150:153], v[186:189], v[58:61]
	v_mfma_i32_16x16x64_i8 v[46:49], v[146:149], v[178:181], v[46:49]
	v_mfma_i32_16x16x64_i8 v[42:45], v[150:153], v[178:181], v[42:45]
	v_mfma_i32_16x16x64_i8 v[30:33], v[146:149], v[170:173], v[30:33]
	v_mfma_i32_16x16x64_i8 v[26:29], v[150:153], v[170:173], v[26:29]
	v_mfma_i32_16x16x64_i8 v[14:17], v[146:149], v[162:165], v[14:17]
	v_mfma_i32_16x16x64_i8 v[10:13], v[150:153], v[162:165], v[10:13]
	v_mfma_i32_16x16x64_i8 v[62:65], v[158:161], v[190:193], v[62:65]
	v_mfma_i32_16x16x64_i8 v[58:61], v[154:157], v[190:193], v[58:61]
	v_mfma_i32_16x16x64_i8 v[46:49], v[158:161], v[182:185], v[46:49]
	v_mfma_i32_16x16x64_i8 v[42:45], v[154:157], v[182:185], v[42:45]
	v_mfma_i32_16x16x64_i8 v[30:33], v[158:161], v[174:177], v[30:33]
	v_mfma_i32_16x16x64_i8 v[26:29], v[154:157], v[174:177], v[26:29]
	v_mfma_i32_16x16x64_i8 v[14:17], v[158:161], v[166:169], v[14:17]
	v_mfma_i32_16x16x64_i8 v[10:13], v[154:157], v[166:169], v[10:13]
	v_mfma_i32_16x16x64_i8 v[54:57], v[130:133], v[186:189], v[54:57]
	v_mfma_i32_16x16x64_i8 v[50:53], v[134:137], v[186:189], v[50:53]
	v_mfma_i32_16x16x64_i8 v[38:41], v[130:133], v[178:181], v[38:41]
	v_mfma_i32_16x16x64_i8 v[34:37], v[134:137], v[178:181], v[34:37]
	v_mfma_i32_16x16x64_i8 v[22:25], v[130:133], v[170:173], v[22:25]
	v_mfma_i32_16x16x64_i8 v[18:21], v[134:137], v[170:173], v[18:21]
	v_mfma_i32_16x16x64_i8 v[6:9], v[130:133], v[162:165], v[6:9]
	v_mfma_i32_16x16x64_i8 v[2:5], v[134:137], v[162:165], v[2:5]
	v_mfma_i32_16x16x64_i8 v[54:57], v[142:145], v[190:193], v[54:57]
	v_mfma_i32_16x16x64_i8 v[50:53], v[138:141], v[190:193], v[50:53]
	v_mfma_i32_16x16x64_i8 v[38:41], v[142:145], v[182:185], v[38:41]
	v_mfma_i32_16x16x64_i8 v[34:37], v[138:141], v[182:185], v[34:37]
	v_mfma_i32_16x16x64_i8 v[22:25], v[142:145], v[174:177], v[22:25]
	v_mfma_i32_16x16x64_i8 v[18:21], v[138:141], v[174:177], v[18:21]
	v_mfma_i32_16x16x64_i8 v[6:9], v[142:145], v[166:169], v[6:9]
	v_mfma_i32_16x16x64_i8 v[2:5], v[138:141], v[166:169], v[2:5]
	s_barrier
	s_add_i32 s31, 0, 0x18000
	s_add_i32 s62, 0, 0x1c000
	v_add_u32_e32 v134, s31, v215
	v_add_u32_e32 v142, s31, v217
	v_add_u32_e32 v150, s62, v215
	v_add_u32_e32 v158, s62, v217
	ds_read_b128 v[130:133], v134
	ds_read_b128 v[134:137], v134 offset:2048
	ds_read_b128 v[138:141], v142
	ds_read_b128 v[142:145], v142 offset:2048
	ds_read_b128 v[146:149], v150
	ds_read_b128 v[150:153], v150 offset:2048
	ds_read_b128 v[154:157], v158
	ds_read_b128 v[158:161], v158 offset:2048
	s_add_u32 s26, s26, 0x40000
	s_addc_u32 s27, s27, 0
	s_mov_b32 m0, s46
	v_lshl_add_u64 v[244:245], s[26:27], 0, v[196:197]
	ds_read_b128 v[162:165], v219 offset:32768
	ds_read_b128 v[166:169], v219 offset:33792
	ds_read_b128 v[170:173], v219 offset:34816
	ds_read_b128 v[174:177], v219 offset:35840
	ds_read_b128 v[178:181], v219 offset:36864
	ds_read_b128 v[182:185], v219 offset:37888
	ds_read_b128 v[186:189], v219 offset:38912
	ds_read_b128 v[190:193], v219 offset:39936
	global_load_lds_dwordx4 v[244:245], off
	v_lshl_add_u64 v[244:245], s[26:27], 0, v[198:199]
	s_mov_b32 m0, s47
	s_nop 0
	global_load_lds_dwordx4 v[244:245], off
	s_waitcnt vmcnt(8)
	s_waitcnt lgkmcnt(0)
	s_barrier
	s_waitcnt lgkmcnt(0)
	v_mfma_i32_16x16x64_i8 v[126:129], v[130:133], v[162:165], v[126:129]
	v_mfma_i32_16x16x64_i8 v[122:125], v[134:137], v[162:165], v[122:125]
	v_mfma_i32_16x16x64_i8 v[110:113], v[130:133], v[170:173], v[110:113]
	v_mfma_i32_16x16x64_i8 v[106:109], v[134:137], v[170:173], v[106:109]
	v_mfma_i32_16x16x64_i8 v[94:97], v[130:133], v[178:181], v[94:97]
	v_mfma_i32_16x16x64_i8 v[90:93], v[134:137], v[178:181], v[90:93]
	v_mfma_i32_16x16x64_i8 v[78:81], v[130:133], v[186:189], v[78:81]
	v_mfma_i32_16x16x64_i8 v[74:77], v[134:137], v[186:189], v[74:77]
	v_mfma_i32_16x16x64_i8 v[126:129], v[138:141], v[166:169], v[126:129]
	v_mfma_i32_16x16x64_i8 v[122:125], v[142:145], v[166:169], v[122:125]
	v_mfma_i32_16x16x64_i8 v[110:113], v[138:141], v[174:177], v[110:113]
	v_mfma_i32_16x16x64_i8 v[106:109], v[142:145], v[174:177], v[106:109]
	v_mfma_i32_16x16x64_i8 v[94:97], v[138:141], v[182:185], v[94:97]
	v_mfma_i32_16x16x64_i8 v[90:93], v[142:145], v[182:185], v[90:93]
	v_mfma_i32_16x16x64_i8 v[78:81], v[138:141], v[190:193], v[78:81]
	v_mfma_i32_16x16x64_i8 v[74:77], v[142:145], v[190:193], v[74:77]
	v_mfma_i32_16x16x64_i8 v[118:121], v[146:149], v[162:165], v[118:121]
	v_mfma_i32_16x16x64_i8 v[114:117], v[150:153], v[162:165], v[114:117]
	v_mfma_i32_16x16x64_i8 v[102:105], v[146:149], v[170:173], v[102:105]
	v_mfma_i32_16x16x64_i8 v[98:101], v[150:153], v[170:173], v[98:101]
	v_mfma_i32_16x16x64_i8 v[86:89], v[146:149], v[178:181], v[86:89]
	v_mfma_i32_16x16x64_i8 v[82:85], v[150:153], v[178:181], v[82:85]
	v_mfma_i32_16x16x64_i8 v[70:73], v[146:149], v[186:189], v[70:73]
	v_mfma_i32_16x16x64_i8 v[66:69], v[150:153], v[186:189], v[66:69]
	v_mfma_i32_16x16x64_i8 v[118:121], v[154:157], v[166:169], v[118:121]
	v_mfma_i32_16x16x64_i8 v[114:117], v[158:161], v[166:169], v[114:117]
	v_mfma_i32_16x16x64_i8 v[102:105], v[154:157], v[174:177], v[102:105]
	v_mfma_i32_16x16x64_i8 v[98:101], v[158:161], v[174:177], v[98:101]
	v_mfma_i32_16x16x64_i8 v[86:89], v[154:157], v[182:185], v[86:89]
	v_mfma_i32_16x16x64_i8 v[82:85], v[158:161], v[182:185], v[82:85]
	v_mfma_i32_16x16x64_i8 v[70:73], v[154:157], v[190:193], v[70:73]
	v_mfma_i32_16x16x64_i8 v[66:69], v[158:161], v[190:193], v[66:69]
	s_barrier
	s_add_i32 s26, s31, s34
	v_lshl_add_u64 v[244:245], s[28:29], 0, v[200:201]
	s_mov_b32 m0, s26
	ds_read_b128 v[162:165], v219 offset:49152
	ds_read_b128 v[166:169], v219 offset:50176
	ds_read_b128 v[170:173], v219 offset:51200
	ds_read_b128 v[174:177], v219 offset:52224
	ds_read_b128 v[178:181], v219 offset:53248
	ds_read_b128 v[182:185], v219 offset:54272
	ds_read_b128 v[186:189], v219 offset:55296
	ds_read_b128 v[190:193], v219 offset:56320
	global_load_lds_dwordx4 v[244:245], off
	s_add_i32 m0, s26, 0x2000
	s_add_u32 s24, s24, 0x9000
	v_lshl_add_u64 v[244:245], s[28:29], 0, v[202:203]
	s_addc_u32 s25, s25, 0
	s_add_i32 s26, s62, s34
	global_load_lds_dwordx4 v[244:245], off
	v_lshl_add_u64 v[244:245], s[24:25], 0, v[200:201]
	s_mov_b32 m0, s26
	v_lshl_add_u64 v[240:241], v[240:241], 0, s[2:3]
	global_load_lds_dwordx4 v[244:245], off
	v_lshl_add_u64 v[244:245], s[24:25], 0, v[202:203]
	s_add_i32 m0, s26, 0x2000
	s_nop 0
	global_load_lds_dwordx4 v[244:245], off
	s_mov_b32 m0, s49
	s_nop 0
	global_load_lds_dwordx4 v[240:241], off
	v_lshl_add_u64 v[240:241], v[242:243], 0, s[2:3]
	s_mov_b32 m0, s50
	s_nop 0
	global_load_lds_dwordx4 v[240:241], off
	s_waitcnt vmcnt(8)
	s_waitcnt lgkmcnt(0)
	s_barrier
	s_waitcnt lgkmcnt(0)
	v_mfma_i32_16x16x64_i8 v[62:65], v[130:133], v[162:165], v[62:65]
	v_mfma_i32_16x16x64_i8 v[58:61], v[134:137], v[162:165], v[58:61]
	v_mfma_i32_16x16x64_i8 v[46:49], v[130:133], v[170:173], v[46:49]
	v_mfma_i32_16x16x64_i8 v[42:45], v[134:137], v[170:173], v[42:45]
	v_mfma_i32_16x16x64_i8 v[30:33], v[130:133], v[178:181], v[30:33]
	v_mfma_i32_16x16x64_i8 v[26:29], v[134:137], v[178:181], v[26:29]
	v_mfma_i32_16x16x64_i8 v[14:17], v[130:133], v[186:189], v[14:17]
	v_mfma_i32_16x16x64_i8 v[10:13], v[134:137], v[186:189], v[10:13]
	v_mfma_i32_16x16x64_i8 v[62:65], v[138:141], v[166:169], v[62:65]
	v_mfma_i32_16x16x64_i8 v[58:61], v[142:145], v[166:169], v[58:61]
	v_mfma_i32_16x16x64_i8 v[46:49], v[138:141], v[174:177], v[46:49]
	v_mfma_i32_16x16x64_i8 v[42:45], v[142:145], v[174:177], v[42:45]
	v_mfma_i32_16x16x64_i8 v[30:33], v[138:141], v[182:185], v[30:33]
	v_mfma_i32_16x16x64_i8 v[26:29], v[142:145], v[182:185], v[26:29]
	v_mfma_i32_16x16x64_i8 v[14:17], v[138:141], v[190:193], v[14:17]
	v_mfma_i32_16x16x64_i8 v[10:13], v[142:145], v[190:193], v[10:13]
	v_mfma_i32_16x16x64_i8 v[54:57], v[146:149], v[162:165], v[54:57]
	v_mfma_i32_16x16x64_i8 v[50:53], v[150:153], v[162:165], v[50:53]
	v_mfma_i32_16x16x64_i8 v[38:41], v[146:149], v[170:173], v[38:41]
	v_mfma_i32_16x16x64_i8 v[34:37], v[150:153], v[170:173], v[34:37]
	v_mfma_i32_16x16x64_i8 v[22:25], v[146:149], v[178:181], v[22:25]
	v_mfma_i32_16x16x64_i8 v[18:21], v[150:153], v[178:181], v[18:21]
	v_mfma_i32_16x16x64_i8 v[6:9], v[146:149], v[186:189], v[6:9]
	v_mfma_i32_16x16x64_i8 v[2:5], v[150:153], v[186:189], v[2:5]
	v_mfma_i32_16x16x64_i8 v[54:57], v[154:157], v[166:169], v[54:57]
	v_mfma_i32_16x16x64_i8 v[50:53], v[158:161], v[166:169], v[50:53]
	v_mfma_i32_16x16x64_i8 v[38:41], v[154:157], v[174:177], v[38:41]
	v_mfma_i32_16x16x64_i8 v[34:37], v[158:161], v[174:177], v[34:37]
	v_mfma_i32_16x16x64_i8 v[22:25], v[154:157], v[182:185], v[22:25]
	v_mfma_i32_16x16x64_i8 v[18:21], v[158:161], v[182:185], v[18:21]
	v_mfma_i32_16x16x64_i8 v[6:9], v[154:157], v[190:193], v[6:9]
	v_mfma_i32_16x16x64_i8 v[2:5], v[158:161], v[190:193], v[2:5]
	s_barrier
	s_add_u32 s60, s60, 0x10000
	s_addc_u32 s61, s61, 0
	s_add_u32 s22, s22, 0x100
	s_addc_u32 s23, s23, 0
	s_cmp_gt_u32 s59, 13
	s_mov_b32 s59, s30
	s_cbranch_scc1 .LBB0_1193

.LBB0_1189:
	s_add_u32 s24, s20, s22
	s_addc_u32 s25, s21, s23
	s_add_u32 s24, s24, 0x100
	s_addc_u32 s25, s25, 0
	s_waitcnt lgkmcnt(0)
	s_cmpk_eq_i32 s22, 0x700
	s_cselect_b32 s27, s11, s25
	s_cselect_b32 s26, s56, s24
	s_cselect_b32 s25, s9, s61
	s_cselect_b32 s24, s57, s60
	s_barrier
	s_waitcnt lgkmcnt(0)
	v_mfma_i32_16x16x64_i8 v[126:129], v[146:149], v[186:189], v[126:129]
	v_mfma_i32_16x16x64_i8 v[122:125], v[150:153], v[186:189], v[122:125]
	v_mfma_i32_16x16x64_i8 v[110:113], v[146:149], v[178:181], v[110:113]
	v_mfma_i32_16x16x64_i8 v[106:109], v[150:153], v[178:181], v[106:109]
	v_mfma_i32_16x16x64_i8 v[94:97], v[146:149], v[170:173], v[94:97]
	v_mfma_i32_16x16x64_i8 v[90:93], v[150:153], v[170:173], v[90:93]
	v_mfma_i32_16x16x64_i8 v[78:81], v[146:149], v[162:165], v[78:81]
	v_mfma_i32_16x16x64_i8 v[74:77], v[150:153], v[162:165], v[74:77]
	v_mfma_i32_16x16x64_i8 v[126:129], v[158:161], v[190:193], v[126:129]
	v_mfma_i32_16x16x64_i8 v[122:125], v[154:157], v[190:193], v[122:125]
	v_mfma_i32_16x16x64_i8 v[110:113], v[158:161], v[182:185], v[110:113]
	v_mfma_i32_16x16x64_i8 v[106:109], v[154:157], v[182:185], v[106:109]
	v_mfma_i32_16x16x64_i8 v[94:97], v[158:161], v[174:177], v[94:97]
	v_mfma_i32_16x16x64_i8 v[90:93], v[154:157], v[174:177], v[90:93]
	v_mfma_i32_16x16x64_i8 v[78:81], v[158:161], v[166:169], v[78:81]
	v_mfma_i32_16x16x64_i8 v[74:77], v[154:157], v[166:169], v[74:77]
	v_mfma_i32_16x16x64_i8 v[118:121], v[130:133], v[186:189], v[118:121]
	v_mfma_i32_16x16x64_i8 v[114:117], v[134:137], v[186:189], v[114:117]
	v_mfma_i32_16x16x64_i8 v[102:105], v[130:133], v[178:181], v[102:105]
	v_mfma_i32_16x16x64_i8 v[98:101], v[134:137], v[178:181], v[98:101]
	v_mfma_i32_16x16x64_i8 v[86:89], v[130:133], v[170:173], v[86:89]
	v_mfma_i32_16x16x64_i8 v[82:85], v[134:137], v[170:173], v[82:85]
	v_mfma_i32_16x16x64_i8 v[70:73], v[130:133], v[162:165], v[70:73]
	v_mfma_i32_16x16x64_i8 v[66:69], v[134:137], v[162:165], v[66:69]
	v_mfma_i32_16x16x64_i8 v[118:121], v[142:145], v[190:193], v[118:121]
	v_mfma_i32_16x16x64_i8 v[114:117], v[138:141], v[190:193], v[114:117]
	v_mfma_i32_16x16x64_i8 v[102:105], v[142:145], v[182:185], v[102:105]
	v_mfma_i32_16x16x64_i8 v[98:101], v[138:141], v[182:185], v[98:101]
	v_mfma_i32_16x16x64_i8 v[86:89], v[142:145], v[174:177], v[86:89]
	v_mfma_i32_16x16x64_i8 v[82:85], v[138:141], v[174:177], v[82:85]
	v_mfma_i32_16x16x64_i8 v[70:73], v[142:145], v[166:169], v[70:73]
	v_mfma_i32_16x16x64_i8 v[66:69], v[138:141], v[166:169], v[66:69]
	s_barrier
	s_mov_b32 m0, s38
	v_lshl_add_u64 v[240:241], s[24:25], 0, v[200:201]
	s_add_u32 s30, s24, 0x1000
	ds_read_b128 v[186:189], v219 offset:16384
	ds_read_b128 v[190:193], v219 offset:17408
	ds_read_b128 v[178:181], v219 offset:18432
	ds_read_b128 v[182:185], v219 offset:19456
	ds_read_b128 v[170:173], v219 offset:20480
	ds_read_b128 v[174:177], v219 offset:21504
	ds_read_b128 v[162:165], v219 offset:22528
	ds_read_b128 v[166:169], v219 offset:23552
	global_load_lds_dwordx4 v[240:241], off
	v_lshl_add_u64 v[240:241], s[24:25], 0, v[202:203]
	s_mov_b32 m0, s39
	s_addc_u32 s31, s25, 0
	global_load_lds_dwordx4 v[240:241], off
	v_lshl_add_u64 v[240:241], s[30:31], 0, v[200:201]
	s_mov_b32 m0, s40
	v_lshl_add_u64 v[242:243], s[26:27], 0, v[198:199]
	global_load_lds_dwordx4 v[240:241], off
	v_lshl_add_u64 v[240:241], s[30:31], 0, v[202:203]
	s_mov_b32 m0, s41
	s_mov_b64 s[30:31], -1
	global_load_lds_dwordx4 v[240:241], off
	v_lshl_add_u64 v[240:241], s[26:27], 0, v[196:197]
	s_mov_b32 m0, s37
	s_and_b64 vcc, exec, s[28:29]
	global_load_lds_dwordx4 v[240:241], off
	s_mov_b32 m0, s45
	s_nop 0
	global_load_lds_dwordx4 v[242:243], off
	s_cbranch_vccz .LBB0_1191
	s_waitcnt vmcnt(8)
	s_mov_b64 s[30:31], 0

.LBB0_1504:
	s_waitcnt lgkmcnt(0)
	s_add_i32 s34, s59, 2
	s_add_u32 s30, s26, 0x8000
	s_addc_u32 s31, s27, 0
	s_barrier
	s_waitcnt lgkmcnt(0)
	v_mfma_i32_16x16x64_i8 v[62:65], v[146:149], v[186:189], v[62:65]
	v_mfma_i32_16x16x64_i8 v[58:61], v[150:153], v[186:189], v[58:61]
	v_mfma_i32_16x16x64_i8 v[46:49], v[146:149], v[178:181], v[46:49]
	v_mfma_i32_16x16x64_i8 v[42:45], v[150:153], v[178:181], v[42:45]
	v_mfma_i32_16x16x64_i8 v[30:33], v[146:149], v[170:173], v[30:33]
	v_mfma_i32_16x16x64_i8 v[26:29], v[150:153], v[170:173], v[26:29]
	v_mfma_i32_16x16x64_i8 v[14:17], v[146:149], v[162:165], v[14:17]
	v_mfma_i32_16x16x64_i8 v[10:13], v[150:153], v[162:165], v[10:13]
	v_mfma_i32_16x16x64_i8 v[62:65], v[158:161], v[190:193], v[62:65]
	v_mfma_i32_16x16x64_i8 v[58:61], v[154:157], v[190:193], v[58:61]
	v_mfma_i32_16x16x64_i8 v[46:49], v[158:161], v[182:185], v[46:49]
	v_mfma_i32_16x16x64_i8 v[42:45], v[154:157], v[182:185], v[42:45]
	v_mfma_i32_16x16x64_i8 v[30:33], v[158:161], v[174:177], v[30:33]
	v_mfma_i32_16x16x64_i8 v[26:29], v[154:157], v[174:177], v[26:29]
	v_mfma_i32_16x16x64_i8 v[14:17], v[158:161], v[166:169], v[14:17]
	v_mfma_i32_16x16x64_i8 v[10:13], v[154:157], v[166:169], v[10:13]
	v_mfma_i32_16x16x64_i8 v[54:57], v[130:133], v[186:189], v[54:57]
	v_mfma_i32_16x16x64_i8 v[50:53], v[134:137], v[186:189], v[50:53]
	v_mfma_i32_16x16x64_i8 v[38:41], v[130:133], v[178:181], v[38:41]
	v_mfma_i32_16x16x64_i8 v[34:37], v[134:137], v[178:181], v[34:37]
	v_mfma_i32_16x16x64_i8 v[22:25], v[130:133], v[170:173], v[22:25]
	v_mfma_i32_16x16x64_i8 v[18:21], v[134:137], v[170:173], v[18:21]
	v_mfma_i32_16x16x64_i8 v[6:9], v[130:133], v[162:165], v[6:9]
	v_mfma_i32_16x16x64_i8 v[2:5], v[134:137], v[162:165], v[2:5]
	v_mfma_i32_16x16x64_i8 v[54:57], v[142:145], v[190:193], v[54:57]
	v_mfma_i32_16x16x64_i8 v[50:53], v[138:141], v[190:193], v[50:53]
	v_mfma_i32_16x16x64_i8 v[38:41], v[142:145], v[182:185], v[38:41]
	v_mfma_i32_16x16x64_i8 v[34:37], v[138:141], v[182:185], v[34:37]
	v_mfma_i32_16x16x64_i8 v[22:25], v[142:145], v[174:177], v[22:25]
	v_mfma_i32_16x16x64_i8 v[18:21], v[138:141], v[174:177], v[18:21]
	v_mfma_i32_16x16x64_i8 v[6:9], v[142:145], v[166:169], v[6:9]
	v_mfma_i32_16x16x64_i8 v[2:5], v[138:141], v[166:169], v[2:5]
	s_barrier
	s_add_i32 s35, 0, 0x18000
	s_add_i32 s62, 0, 0x1c000
	v_add_u32_e32 v134, s35, v211
	v_add_u32_e32 v142, s35, v213
	v_add_u32_e32 v150, s62, v211
	v_add_u32_e32 v158, s62, v213
	ds_read_b128 v[130:133], v134
	ds_read_b128 v[134:137], v134 offset:2048
	ds_read_b128 v[138:141], v142
	ds_read_b128 v[142:145], v142 offset:2048
	ds_read_b128 v[146:149], v150
	ds_read_b128 v[150:153], v150 offset:2048
	ds_read_b128 v[154:157], v158
	ds_read_b128 v[158:161], v158 offset:2048
	s_add_u32 s28, s28, 0x40000
	s_addc_u32 s29, s29, 0
	s_mov_b32 m0, s49
	v_lshl_add_u64 v[246:247], s[28:29], 0, v[196:197]
	ds_read_b128 v[162:165], v207 offset:32768
	ds_read_b128 v[166:169], v207 offset:33792
	ds_read_b128 v[170:173], v207 offset:34816
	ds_read_b128 v[174:177], v207 offset:35840
	ds_read_b128 v[178:181], v207 offset:36864
	ds_read_b128 v[182:185], v207 offset:37888
	ds_read_b128 v[186:189], v207 offset:38912
	ds_read_b128 v[190:193], v207 offset:39936
	global_load_lds_dwordx4 v[246:247], off
	v_lshl_add_u64 v[246:247], s[28:29], 0, v[198:199]
	s_mov_b32 m0, s50
	s_nop 0
	global_load_lds_dwordx4 v[246:247], off
	s_waitcnt vmcnt(8)
	s_waitcnt lgkmcnt(0)
	s_barrier
	s_waitcnt lgkmcnt(0)
	v_mfma_i32_16x16x64_i8 v[126:129], v[130:133], v[162:165], v[126:129]
	v_mfma_i32_16x16x64_i8 v[122:125], v[134:137], v[162:165], v[122:125]
	v_mfma_i32_16x16x64_i8 v[110:113], v[130:133], v[170:173], v[110:113]
	v_mfma_i32_16x16x64_i8 v[106:109], v[134:137], v[170:173], v[106:109]
	v_mfma_i32_16x16x64_i8 v[94:97], v[130:133], v[178:181], v[94:97]
	v_mfma_i32_16x16x64_i8 v[90:93], v[134:137], v[178:181], v[90:93]
	v_mfma_i32_16x16x64_i8 v[78:81], v[130:133], v[186:189], v[78:81]
	v_mfma_i32_16x16x64_i8 v[74:77], v[134:137], v[186:189], v[74:77]
	v_mfma_i32_16x16x64_i8 v[126:129], v[138:141], v[166:169], v[126:129]
	v_mfma_i32_16x16x64_i8 v[122:125], v[142:145], v[166:169], v[122:125]
	v_mfma_i32_16x16x64_i8 v[110:113], v[138:141], v[174:177], v[110:113]
	v_mfma_i32_16x16x64_i8 v[106:109], v[142:145], v[174:177], v[106:109]
	v_mfma_i32_16x16x64_i8 v[94:97], v[138:141], v[182:185], v[94:97]
	v_mfma_i32_16x16x64_i8 v[90:93], v[142:145], v[182:185], v[90:93]
	v_mfma_i32_16x16x64_i8 v[78:81], v[138:141], v[190:193], v[78:81]
	v_mfma_i32_16x16x64_i8 v[74:77], v[142:145], v[190:193], v[74:77]
	v_mfma_i32_16x16x64_i8 v[118:121], v[146:149], v[162:165], v[118:121]
	v_mfma_i32_16x16x64_i8 v[114:117], v[150:153], v[162:165], v[114:117]
	v_mfma_i32_16x16x64_i8 v[102:105], v[146:149], v[170:173], v[102:105]
	v_mfma_i32_16x16x64_i8 v[98:101], v[150:153], v[170:173], v[98:101]
	v_mfma_i32_16x16x64_i8 v[86:89], v[146:149], v[178:181], v[86:89]
	v_mfma_i32_16x16x64_i8 v[82:85], v[150:153], v[178:181], v[82:85]
	v_mfma_i32_16x16x64_i8 v[70:73], v[146:149], v[186:189], v[70:73]
	v_mfma_i32_16x16x64_i8 v[66:69], v[150:153], v[186:189], v[66:69]
	v_mfma_i32_16x16x64_i8 v[118:121], v[154:157], v[166:169], v[118:121]
	v_mfma_i32_16x16x64_i8 v[114:117], v[158:161], v[166:169], v[114:117]
	v_mfma_i32_16x16x64_i8 v[102:105], v[154:157], v[174:177], v[102:105]
	v_mfma_i32_16x16x64_i8 v[98:101], v[158:161], v[174:177], v[98:101]
	v_mfma_i32_16x16x64_i8 v[86:89], v[154:157], v[182:185], v[86:89]
	v_mfma_i32_16x16x64_i8 v[82:85], v[158:161], v[182:185], v[82:85]
	v_mfma_i32_16x16x64_i8 v[70:73], v[154:157], v[190:193], v[70:73]
	v_mfma_i32_16x16x64_i8 v[66:69], v[158:161], v[190:193], v[66:69]
	s_barrier
	s_add_i32 s28, s35, s38
	v_lshl_add_u64 v[246:247], s[30:31], 0, v[200:201]
	s_mov_b32 m0, s28
	ds_read_b128 v[162:165], v207 offset:49152
	ds_read_b128 v[166:169], v207 offset:50176
	ds_read_b128 v[170:173], v207 offset:51200
	ds_read_b128 v[174:177], v207 offset:52224
	ds_read_b128 v[178:181], v207 offset:53248
	ds_read_b128 v[182:185], v207 offset:54272
	ds_read_b128 v[186:189], v207 offset:55296
	ds_read_b128 v[190:193], v207 offset:56320
	global_load_lds_dwordx4 v[246:247], off
	s_add_i32 m0, s28, 0x2000
	s_add_u32 s26, s26, 0x9000
	v_lshl_add_u64 v[246:247], s[30:31], 0, v[202:203]
	s_addc_u32 s27, s27, 0
	s_add_i32 s28, s62, s38
	global_load_lds_dwordx4 v[246:247], off
	v_lshl_add_u64 v[246:247], s[26:27], 0, v[200:201]
	s_mov_b32 m0, s28
	v_lshl_add_u64 v[242:243], v[242:243], 0, s[2:3]
	global_load_lds_dwordx4 v[246:247], off
	v_lshl_add_u64 v[246:247], s[26:27], 0, v[202:203]
	s_add_i32 m0, s28, 0x2000
	s_nop 0
	global_load_lds_dwordx4 v[246:247], off
	s_mov_b32 m0, s52
	s_nop 0
	global_load_lds_dwordx4 v[242:243], off
	v_lshl_add_u64 v[242:243], v[244:245], 0, s[2:3]
	s_mov_b32 m0, s53
	s_nop 0
	global_load_lds_dwordx4 v[242:243], off
	s_waitcnt vmcnt(8)
	s_waitcnt lgkmcnt(0)
	s_barrier
	s_waitcnt lgkmcnt(0)
	v_mfma_i32_16x16x64_i8 v[62:65], v[130:133], v[162:165], v[62:65]
	v_mfma_i32_16x16x64_i8 v[58:61], v[134:137], v[162:165], v[58:61]
	v_mfma_i32_16x16x64_i8 v[46:49], v[130:133], v[170:173], v[46:49]
	v_mfma_i32_16x16x64_i8 v[42:45], v[134:137], v[170:173], v[42:45]
	v_mfma_i32_16x16x64_i8 v[30:33], v[130:133], v[178:181], v[30:33]
	v_mfma_i32_16x16x64_i8 v[26:29], v[134:137], v[178:181], v[26:29]
	v_mfma_i32_16x16x64_i8 v[14:17], v[130:133], v[186:189], v[14:17]
	v_mfma_i32_16x16x64_i8 v[10:13], v[134:137], v[186:189], v[10:13]
	v_mfma_i32_16x16x64_i8 v[62:65], v[138:141], v[166:169], v[62:65]
	v_mfma_i32_16x16x64_i8 v[58:61], v[142:145], v[166:169], v[58:61]
	v_mfma_i32_16x16x64_i8 v[46:49], v[138:141], v[174:177], v[46:49]
	v_mfma_i32_16x16x64_i8 v[42:45], v[142:145], v[174:177], v[42:45]
	v_mfma_i32_16x16x64_i8 v[30:33], v[138:141], v[182:185], v[30:33]
	v_mfma_i32_16x16x64_i8 v[26:29], v[142:145], v[182:185], v[26:29]
	v_mfma_i32_16x16x64_i8 v[14:17], v[138:141], v[190:193], v[14:17]
	v_mfma_i32_16x16x64_i8 v[10:13], v[142:145], v[190:193], v[10:13]
	v_mfma_i32_16x16x64_i8 v[54:57], v[146:149], v[162:165], v[54:57]
	v_mfma_i32_16x16x64_i8 v[50:53], v[150:153], v[162:165], v[50:53]
	v_mfma_i32_16x16x64_i8 v[38:41], v[146:149], v[170:173], v[38:41]
	v_mfma_i32_16x16x64_i8 v[34:37], v[150:153], v[170:173], v[34:37]
	v_mfma_i32_16x16x64_i8 v[22:25], v[146:149], v[178:181], v[22:25]
	v_mfma_i32_16x16x64_i8 v[18:21], v[150:153], v[178:181], v[18:21]
	v_mfma_i32_16x16x64_i8 v[6:9], v[146:149], v[186:189], v[6:9]
	v_mfma_i32_16x16x64_i8 v[2:5], v[150:153], v[186:189], v[2:5]
	v_mfma_i32_16x16x64_i8 v[54:57], v[154:157], v[166:169], v[54:57]
	v_mfma_i32_16x16x64_i8 v[50:53], v[158:161], v[166:169], v[50:53]
	v_mfma_i32_16x16x64_i8 v[38:41], v[154:157], v[174:177], v[38:41]
	v_mfma_i32_16x16x64_i8 v[34:37], v[158:161], v[174:177], v[34:37]
	v_mfma_i32_16x16x64_i8 v[22:25], v[154:157], v[182:185], v[22:25]
	v_mfma_i32_16x16x64_i8 v[18:21], v[158:161], v[182:185], v[18:21]
	v_mfma_i32_16x16x64_i8 v[6:9], v[154:157], v[190:193], v[6:9]
	v_mfma_i32_16x16x64_i8 v[2:5], v[158:161], v[190:193], v[2:5]
	s_barrier
	s_add_u32 s60, s60, 0x10000
	s_addc_u32 s61, s61, 0
	s_add_u32 s24, s24, 0x100
	s_addc_u32 s25, s25, 0
	s_cmp_gt_u32 s59, 13
	s_mov_b32 s59, s34
	s_cbranch_scc1 .LBB0_1513

.LBB0_1509:
	s_add_u32 s26, s22, s24
	s_addc_u32 s27, s23, s25
	s_add_u32 s26, s26, 0x100
	s_addc_u32 s27, s27, 0
	s_waitcnt lgkmcnt(0)
	s_cmpk_eq_i32 s24, 0x700
	s_cselect_b32 s29, s11, s27
	s_cselect_b32 s28, s19, s26
	s_cselect_b32 s27, s9, s61
	s_cselect_b32 s26, s21, s60
	s_barrier
	s_waitcnt lgkmcnt(0)
	v_mfma_i32_16x16x64_i8 v[126:129], v[146:149], v[186:189], v[126:129]
	v_mfma_i32_16x16x64_i8 v[122:125], v[150:153], v[186:189], v[122:125]
	v_mfma_i32_16x16x64_i8 v[110:113], v[146:149], v[178:181], v[110:113]
	v_mfma_i32_16x16x64_i8 v[106:109], v[150:153], v[178:181], v[106:109]
	v_mfma_i32_16x16x64_i8 v[94:97], v[146:149], v[170:173], v[94:97]
	v_mfma_i32_16x16x64_i8 v[90:93], v[150:153], v[170:173], v[90:93]
	v_mfma_i32_16x16x64_i8 v[78:81], v[146:149], v[162:165], v[78:81]
	v_mfma_i32_16x16x64_i8 v[74:77], v[150:153], v[162:165], v[74:77]
	v_mfma_i32_16x16x64_i8 v[126:129], v[158:161], v[190:193], v[126:129]
	v_mfma_i32_16x16x64_i8 v[122:125], v[154:157], v[190:193], v[122:125]
	v_mfma_i32_16x16x64_i8 v[110:113], v[158:161], v[182:185], v[110:113]
	v_mfma_i32_16x16x64_i8 v[106:109], v[154:157], v[182:185], v[106:109]
	v_mfma_i32_16x16x64_i8 v[94:97], v[158:161], v[174:177], v[94:97]
	v_mfma_i32_16x16x64_i8 v[90:93], v[154:157], v[174:177], v[90:93]
	v_mfma_i32_16x16x64_i8 v[78:81], v[158:161], v[166:169], v[78:81]
	v_mfma_i32_16x16x64_i8 v[74:77], v[154:157], v[166:169], v[74:77]
	v_mfma_i32_16x16x64_i8 v[118:121], v[130:133], v[186:189], v[118:121]
	v_mfma_i32_16x16x64_i8 v[114:117], v[134:137], v[186:189], v[114:117]
	v_mfma_i32_16x16x64_i8 v[102:105], v[130:133], v[178:181], v[102:105]
	v_mfma_i32_16x16x64_i8 v[98:101], v[134:137], v[178:181], v[98:101]
	v_mfma_i32_16x16x64_i8 v[86:89], v[130:133], v[170:173], v[86:89]
	v_mfma_i32_16x16x64_i8 v[82:85], v[134:137], v[170:173], v[82:85]
	v_mfma_i32_16x16x64_i8 v[70:73], v[130:133], v[162:165], v[70:73]
	v_mfma_i32_16x16x64_i8 v[66:69], v[134:137], v[162:165], v[66:69]
	v_mfma_i32_16x16x64_i8 v[118:121], v[142:145], v[190:193], v[118:121]
	v_mfma_i32_16x16x64_i8 v[114:117], v[138:141], v[190:193], v[114:117]
	v_mfma_i32_16x16x64_i8 v[102:105], v[142:145], v[182:185], v[102:105]
	v_mfma_i32_16x16x64_i8 v[98:101], v[138:141], v[182:185], v[98:101]
	v_mfma_i32_16x16x64_i8 v[86:89], v[142:145], v[174:177], v[86:89]
	v_mfma_i32_16x16x64_i8 v[82:85], v[138:141], v[174:177], v[82:85]
	v_mfma_i32_16x16x64_i8 v[70:73], v[142:145], v[166:169], v[70:73]
	v_mfma_i32_16x16x64_i8 v[66:69], v[138:141], v[166:169], v[66:69]
	s_barrier
	s_mov_b32 m0, s41
	v_lshl_add_u64 v[242:243], s[26:27], 0, v[200:201]
	s_add_u32 s34, s26, 0x1000
	ds_read_b128 v[186:189], v207 offset:16384
	ds_read_b128 v[190:193], v207 offset:17408
	ds_read_b128 v[178:181], v207 offset:18432
	ds_read_b128 v[182:185], v207 offset:19456
	ds_read_b128 v[170:173], v207 offset:20480
	ds_read_b128 v[174:177], v207 offset:21504
	ds_read_b128 v[162:165], v207 offset:22528
	ds_read_b128 v[166:169], v207 offset:23552
	global_load_lds_dwordx4 v[242:243], off
	v_lshl_add_u64 v[242:243], s[26:27], 0, v[202:203]
	s_mov_b32 m0, s45
	s_addc_u32 s35, s27, 0
	global_load_lds_dwordx4 v[242:243], off
	v_lshl_add_u64 v[242:243], s[34:35], 0, v[200:201]
	s_mov_b32 m0, s46
	v_lshl_add_u64 v[244:245], s[28:29], 0, v[198:199]
	global_load_lds_dwordx4 v[242:243], off
	v_lshl_add_u64 v[242:243], s[34:35], 0, v[202:203]
	s_mov_b32 m0, s47
	s_mov_b64 s[34:35], -1
	global_load_lds_dwordx4 v[242:243], off
	v_lshl_add_u64 v[242:243], s[28:29], 0, v[196:197]
	s_mov_b32 m0, s40
	s_and_b64 vcc, exec, s[30:31]
	global_load_lds_dwordx4 v[242:243], off
	s_mov_b32 m0, s48
	s_nop 0
	global_load_lds_dwordx4 v[244:245], off
	s_cbranch_vccz .LBB0_1511
	s_waitcnt vmcnt(8)
	s_mov_b64 s[34:35], 0

.LBB0_1587:
	s_add_i32 s53, s50, 2
	s_add_u32 s24, s22, 0x8000
	s_waitcnt lgkmcnt(0)
	s_addc_u32 s25, s23, 0
	s_add_u32 s26, s20, 0x8000
	s_addc_u32 s27, s21, 0
	s_barrier
	s_waitcnt lgkmcnt(0)
	v_mfma_scale_f32_16x16x128_f8f6f4 v[126:129], v[26:33], v[58:65], v[126:129], v230, v230 op_sel_hi:[0,0,0]
	v_mfma_scale_f32_16x16x128_f8f6f4 v[122:125], v[18:25], v[58:65], v[122:125], v230, v230 op_sel_hi:[0,0,0]
	v_mfma_scale_f32_16x16x128_f8f6f4 v[110:113], v[26:33], v[50:57], v[110:113], v230, v230 op_sel_hi:[0,0,0]
	v_mfma_scale_f32_16x16x128_f8f6f4 v[106:109], v[18:25], v[50:57], v[106:109], v230, v230 op_sel_hi:[0,0,0]
	v_mfma_scale_f32_16x16x128_f8f6f4 v[94:97], v[26:33], v[42:49], v[94:97], v230, v230 op_sel_hi:[0,0,0]
	v_mfma_scale_f32_16x16x128_f8f6f4 v[90:93], v[18:25], v[42:49], v[90:93], v230, v230 op_sel_hi:[0,0,0]
	v_mfma_scale_f32_16x16x128_f8f6f4 v[78:81], v[26:33], v[34:41], v[78:81], v230, v230 op_sel_hi:[0,0,0]
	v_mfma_scale_f32_16x16x128_f8f6f4 v[74:77], v[18:25], v[34:41], v[74:77], v230, v230 op_sel_hi:[0,0,0]
	v_mfma_scale_f32_16x16x128_f8f6f4 v[118:121], v[10:17], v[58:65], v[118:121], v230, v230 op_sel_hi:[0,0,0]
	v_mfma_scale_f32_16x16x128_f8f6f4 v[114:117], v[2:9], v[58:65], v[114:117], v230, v230 op_sel_hi:[0,0,0]
	v_mfma_scale_f32_16x16x128_f8f6f4 v[102:105], v[10:17], v[50:57], v[102:105], v230, v230 op_sel_hi:[0,0,0]
	v_mfma_scale_f32_16x16x128_f8f6f4 v[98:101], v[2:9], v[50:57], v[98:101], v230, v230 op_sel_hi:[0,0,0]
	v_mfma_scale_f32_16x16x128_f8f6f4 v[86:89], v[10:17], v[42:49], v[86:89], v230, v230 op_sel_hi:[0,0,0]
	v_mfma_scale_f32_16x16x128_f8f6f4 v[82:85], v[2:9], v[42:49], v[82:85], v230, v230 op_sel_hi:[0,0,0]
	v_mfma_scale_f32_16x16x128_f8f6f4 v[70:73], v[10:17], v[34:41], v[70:73], v230, v230 op_sel_hi:[0,0,0]
	v_mfma_scale_f32_16x16x128_f8f6f4 v[66:69], v[2:9], v[34:41], v[66:69], v230, v230 op_sel_hi:[0,0,0]
	s_barrier
	s_add_i32 s54, 0, 0x18000
	s_add_i32 s55, 0, 0x1c000
	v_add_u32_e32 v6, s54, v218
	v_add_u32_e32 v14, s54, v219
	v_add_u32_e32 v22, s55, v218
	v_add_u32_e32 v30, s55, v219
	ds_read_b128 v[2:5], v6
	ds_read_b128 v[10:13], v6 offset:2048
	ds_read_b128 v[6:9], v14
	ds_read_b128 v[14:17], v14 offset:2048
	ds_read_b128 v[18:21], v22
	ds_read_b128 v[26:29], v22 offset:2048
	ds_read_b128 v[22:25], v30
	ds_read_b128 v[30:33], v30 offset:2048
	s_add_u32 s22, s22, 0x1000
	s_addc_u32 s23, s23, 0
	s_mov_b32 m0, s36
	v_lshl_add_u64 v[232:233], s[22:23], 0, v[194:195]
	ds_read_b128 v[34:37], v228 offset:32768
	ds_read_b128 v[42:45], v228 offset:34816
	ds_read_b128 v[38:41], v229 offset:32768
	ds_read_b128 v[46:49], v229 offset:34816
	ds_read_b128 v[50:53], v228 offset:36864
	ds_read_b128 v[58:61], v228 offset:38912
	ds_read_b128 v[54:57], v229 offset:36864
	ds_read_b128 v[62:65], v229 offset:38912
	global_load_lds_dwordx4 v[232:233], off
	v_lshl_add_u64 v[232:233], s[22:23], 0, v[198:199]
	s_mov_b32 m0, s37
	s_nop 0
	global_load_lds_dwordx4 v[232:233], off
	s_waitcnt vmcnt(8)
	s_waitcnt lgkmcnt(0)
	s_barrier
	s_waitcnt lgkmcnt(0)
	v_mfma_scale_f32_16x16x128_f8f6f4 v[190:193], v[2:9], v[34:41], v[190:193], v230, v230 op_sel_hi:[0,0,0]
	v_mfma_scale_f32_16x16x128_f8f6f4 v[186:189], v[10:17], v[34:41], v[186:189], v230, v230 op_sel_hi:[0,0,0]
	v_mfma_scale_f32_16x16x128_f8f6f4 v[174:177], v[2:9], v[42:49], v[174:177], v230, v230 op_sel_hi:[0,0,0]
	v_mfma_scale_f32_16x16x128_f8f6f4 v[170:173], v[10:17], v[42:49], v[170:173], v230, v230 op_sel_hi:[0,0,0]
	v_mfma_scale_f32_16x16x128_f8f6f4 v[158:161], v[2:9], v[50:57], v[158:161], v230, v230 op_sel_hi:[0,0,0]
	v_mfma_scale_f32_16x16x128_f8f6f4 v[154:157], v[10:17], v[50:57], v[154:157], v230, v230 op_sel_hi:[0,0,0]
	v_mfma_scale_f32_16x16x128_f8f6f4 v[142:145], v[2:9], v[58:65], v[142:145], v230, v230 op_sel_hi:[0,0,0]
	v_mfma_scale_f32_16x16x128_f8f6f4 v[138:141], v[10:17], v[58:65], v[138:141], v230, v230 op_sel_hi:[0,0,0]
	v_mfma_scale_f32_16x16x128_f8f6f4 v[182:185], v[18:25], v[34:41], v[182:185], v230, v230 op_sel_hi:[0,0,0]
	v_mfma_scale_f32_16x16x128_f8f6f4 v[178:181], v[26:33], v[34:41], v[178:181], v230, v230 op_sel_hi:[0,0,0]
	v_mfma_scale_f32_16x16x128_f8f6f4 v[166:169], v[18:25], v[42:49], v[166:169], v230, v230 op_sel_hi:[0,0,0]
	v_mfma_scale_f32_16x16x128_f8f6f4 v[162:165], v[26:33], v[42:49], v[162:165], v230, v230 op_sel_hi:[0,0,0]
	v_mfma_scale_f32_16x16x128_f8f6f4 v[150:153], v[18:25], v[50:57], v[150:153], v230, v230 op_sel_hi:[0,0,0]
	v_mfma_scale_f32_16x16x128_f8f6f4 v[146:149], v[26:33], v[50:57], v[146:149], v230, v230 op_sel_hi:[0,0,0]
	v_mfma_scale_f32_16x16x128_f8f6f4 v[134:137], v[18:25], v[58:65], v[134:137], v230, v230 op_sel_hi:[0,0,0]
	v_mfma_scale_f32_16x16x128_f8f6f4 v[130:133], v[26:33], v[58:65], v[130:133], v230, v230 op_sel_hi:[0,0,0]
	s_barrier
	s_add_i32 s22, s54, s11
	v_lshl_add_u64 v[232:233], s[26:27], 0, v[196:197]
	s_mov_b32 m0, s22
	ds_read_b128 v[34:37], v228 offset:49152
	ds_read_b128 v[42:45], v228 offset:51200
	ds_read_b128 v[38:41], v229 offset:49152
	ds_read_b128 v[46:49], v229 offset:51200
	ds_read_b128 v[50:53], v228 offset:53248
	ds_read_b128 v[58:61], v228 offset:55296
	ds_read_b128 v[54:57], v229 offset:53248
	ds_read_b128 v[62:65], v229 offset:55296
	global_load_lds_dwordx4 v[232:233], off
	s_add_i32 m0, s22, 0x2000
	s_add_u32 s20, s20, 0x9000
	v_lshl_add_u64 v[232:233], s[26:27], 0, v[200:201]
	s_addc_u32 s21, s21, 0
	s_add_i32 s22, s55, s11
	global_load_lds_dwordx4 v[232:233], off
	v_lshl_add_u64 v[232:233], s[20:21], 0, v[196:197]
	s_mov_b32 m0, s22
	s_nop 0
	global_load_lds_dwordx4 v[232:233], off
	v_lshl_add_u64 v[232:233], s[20:21], 0, v[200:201]
	s_add_i32 m0, s22, 0x2000
	s_nop 0
	global_load_lds_dwordx4 v[232:233], off
	v_lshl_add_u64 v[232:233], s[24:25], 0, v[194:195]
	s_mov_b32 m0, s38
	s_nop 0
	global_load_lds_dwordx4 v[232:233], off
	v_lshl_add_u64 v[232:233], s[24:25], 0, v[198:199]
	s_mov_b32 m0, s39
	s_nop 0
	global_load_lds_dwordx4 v[232:233], off
	s_waitcnt vmcnt(8)
	s_waitcnt lgkmcnt(0)
	s_barrier
	s_waitcnt lgkmcnt(0)
	v_mfma_scale_f32_16x16x128_f8f6f4 v[126:129], v[2:9], v[34:41], v[126:129], v230, v230 op_sel_hi:[0,0,0]
	v_mfma_scale_f32_16x16x128_f8f6f4 v[122:125], v[10:17], v[34:41], v[122:125], v230, v230 op_sel_hi:[0,0,0]
	v_mfma_scale_f32_16x16x128_f8f6f4 v[110:113], v[2:9], v[42:49], v[110:113], v230, v230 op_sel_hi:[0,0,0]
	v_mfma_scale_f32_16x16x128_f8f6f4 v[106:109], v[10:17], v[42:49], v[106:109], v230, v230 op_sel_hi:[0,0,0]
	v_mfma_scale_f32_16x16x128_f8f6f4 v[94:97], v[2:9], v[50:57], v[94:97], v230, v230 op_sel_hi:[0,0,0]
	v_mfma_scale_f32_16x16x128_f8f6f4 v[90:93], v[10:17], v[50:57], v[90:93], v230, v230 op_sel_hi:[0,0,0]
	v_mfma_scale_f32_16x16x128_f8f6f4 v[78:81], v[2:9], v[58:65], v[78:81], v230, v230 op_sel_hi:[0,0,0]
	v_mfma_scale_f32_16x16x128_f8f6f4 v[74:77], v[10:17], v[58:65], v[74:77], v230, v230 op_sel_hi:[0,0,0]
	v_mfma_scale_f32_16x16x128_f8f6f4 v[118:121], v[18:25], v[34:41], v[118:121], v230, v230 op_sel_hi:[0,0,0]
	v_mfma_scale_f32_16x16x128_f8f6f4 v[114:117], v[26:33], v[34:41], v[114:117], v230, v230 op_sel_hi:[0,0,0]
	v_mfma_scale_f32_16x16x128_f8f6f4 v[102:105], v[18:25], v[42:49], v[102:105], v230, v230 op_sel_hi:[0,0,0]
	v_mfma_scale_f32_16x16x128_f8f6f4 v[98:101], v[26:33], v[42:49], v[98:101], v230, v230 op_sel_hi:[0,0,0]
	v_mfma_scale_f32_16x16x128_f8f6f4 v[86:89], v[18:25], v[50:57], v[86:89], v230, v230 op_sel_hi:[0,0,0]
	v_mfma_scale_f32_16x16x128_f8f6f4 v[82:85], v[26:33], v[50:57], v[82:85], v230, v230 op_sel_hi:[0,0,0]
	v_mfma_scale_f32_16x16x128_f8f6f4 v[70:73], v[18:25], v[58:65], v[70:73], v230, v230 op_sel_hi:[0,0,0]
	v_mfma_scale_f32_16x16x128_f8f6f4 v[66:69], v[26:33], v[58:65], v[66:69], v230, v230 op_sel_hi:[0,0,0]
	s_barrier
	s_add_u32 s18, s18, 0x10000
	s_addc_u32 s19, s19, 0
	s_cmp_gt_u32 s50, 41
	s_mov_b32 s50, s53
	s_cbranch_scc1 .LBB0_1596

.LBB0_1592:
	s_add_u32 s20, s16, s18
	s_addc_u32 s21, s17, s19
	s_add_u32 s20, s20, 0x10000
	s_addc_u32 s21, s21, 0
	s_add_u32 s26, s51, s18
	s_addc_u32 s27, s52, s19
	s_waitcnt lgkmcnt(0)
	s_cmp_eq_u32 s18, 0x150000
	s_cselect_b32 s23, s13, s21
	s_cselect_b32 s22, s12, s20
	s_cselect_b32 s21, s15, s27
	s_cselect_b32 s20, s14, s26
	s_barrier
	s_waitcnt lgkmcnt(0)
	v_mfma_scale_f32_16x16x128_f8f6f4 v[190:193], v[26:33], v[58:65], v[190:193], v230, v230 op_sel_hi:[0,0,0]
	v_mfma_scale_f32_16x16x128_f8f6f4 v[186:189], v[18:25], v[58:65], v[186:189], v230, v230 op_sel_hi:[0,0,0]
	v_mfma_scale_f32_16x16x128_f8f6f4 v[174:177], v[26:33], v[50:57], v[174:177], v230, v230 op_sel_hi:[0,0,0]
	v_mfma_scale_f32_16x16x128_f8f6f4 v[170:173], v[18:25], v[50:57], v[170:173], v230, v230 op_sel_hi:[0,0,0]
	v_mfma_scale_f32_16x16x128_f8f6f4 v[158:161], v[26:33], v[42:49], v[158:161], v230, v230 op_sel_hi:[0,0,0]
	v_mfma_scale_f32_16x16x128_f8f6f4 v[154:157], v[18:25], v[42:49], v[154:157], v230, v230 op_sel_hi:[0,0,0]
	v_mfma_scale_f32_16x16x128_f8f6f4 v[142:145], v[26:33], v[34:41], v[142:145], v230, v230 op_sel_hi:[0,0,0]
	v_mfma_scale_f32_16x16x128_f8f6f4 v[138:141], v[18:25], v[34:41], v[138:141], v230, v230 op_sel_hi:[0,0,0]
	v_mfma_scale_f32_16x16x128_f8f6f4 v[182:185], v[10:17], v[58:65], v[182:185], v230, v230 op_sel_hi:[0,0,0]
	v_mfma_scale_f32_16x16x128_f8f6f4 v[178:181], v[2:9], v[58:65], v[178:181], v230, v230 op_sel_hi:[0,0,0]
	v_mfma_scale_f32_16x16x128_f8f6f4 v[166:169], v[10:17], v[50:57], v[166:169], v230, v230 op_sel_hi:[0,0,0]
	v_mfma_scale_f32_16x16x128_f8f6f4 v[162:165], v[2:9], v[50:57], v[162:165], v230, v230 op_sel_hi:[0,0,0]
	v_mfma_scale_f32_16x16x128_f8f6f4 v[150:153], v[10:17], v[42:49], v[150:153], v230, v230 op_sel_hi:[0,0,0]
	v_mfma_scale_f32_16x16x128_f8f6f4 v[146:149], v[2:9], v[42:49], v[146:149], v230, v230 op_sel_hi:[0,0,0]
	v_mfma_scale_f32_16x16x128_f8f6f4 v[134:137], v[10:17], v[34:41], v[134:137], v230, v230 op_sel_hi:[0,0,0]
	v_mfma_scale_f32_16x16x128_f8f6f4 v[130:133], v[2:9], v[34:41], v[130:133], v230, v230 op_sel_hi:[0,0,0]
	s_barrier
	s_mov_b32 m0, s29
	v_lshl_add_u64 v[232:233], s[20:21], 0, v[196:197]
	s_add_u32 s26, s20, 0x1000
	ds_read_b128 v[58:61], v228 offset:16384
	ds_read_b128 v[50:53], v228 offset:18432
	ds_read_b128 v[62:65], v229 offset:16384
	ds_read_b128 v[54:57], v229 offset:18432
	ds_read_b128 v[42:45], v228 offset:20480
	ds_read_b128 v[34:37], v228 offset:22528
	ds_read_b128 v[46:49], v229 offset:20480
	ds_read_b128 v[38:41], v229 offset:22528
	global_load_lds_dwordx4 v[232:233], off
	v_lshl_add_u64 v[232:233], s[20:21], 0, v[200:201]
	s_mov_b32 m0, s30
	s_addc_u32 s27, s21, 0
	global_load_lds_dwordx4 v[232:233], off
	v_lshl_add_u64 v[232:233], s[26:27], 0, v[196:197]
	s_mov_b32 m0, s31
	s_and_b64 vcc, exec, s[24:25]
	global_load_lds_dwordx4 v[232:233], off
	v_lshl_add_u64 v[232:233], s[26:27], 0, v[200:201]
	s_mov_b32 m0, s34
	s_mov_b64 s[26:27], -1
	global_load_lds_dwordx4 v[232:233], off
	v_lshl_add_u64 v[232:233], s[22:23], 0, v[194:195]
	s_mov_b32 m0, s28
	s_nop 0
	global_load_lds_dwordx4 v[232:233], off
	v_lshl_add_u64 v[232:233], s[22:23], 0, v[198:199]
	s_mov_b32 m0, s35
	s_nop 0
	global_load_lds_dwordx4 v[232:233], off
	s_cbranch_vccz .LBB0_1594
	s_waitcnt vmcnt(8)
	s_mov_b64 s[26:27], 0

.LBB0_1940:
	s_add_i32 s53, s50, 2
	s_add_u32 s22, s20, 0x8000
	s_waitcnt lgkmcnt(0)
	s_addc_u32 s23, s21, 0
	s_add_u32 s24, s18, 0x8000
	s_addc_u32 s25, s19, 0
	s_barrier
	s_waitcnt lgkmcnt(0)
	v_mfma_scale_f32_16x16x128_f8f6f4 v[126:129], v[26:33], v[58:65], v[126:129], v221, v221 op_sel_hi:[0,0,0]
	v_mfma_scale_f32_16x16x128_f8f6f4 v[122:125], v[18:25], v[58:65], v[122:125], v221, v221 op_sel_hi:[0,0,0]
	v_mfma_scale_f32_16x16x128_f8f6f4 v[110:113], v[26:33], v[50:57], v[110:113], v221, v221 op_sel_hi:[0,0,0]
	v_mfma_scale_f32_16x16x128_f8f6f4 v[106:109], v[18:25], v[50:57], v[106:109], v221, v221 op_sel_hi:[0,0,0]
	v_mfma_scale_f32_16x16x128_f8f6f4 v[94:97], v[26:33], v[42:49], v[94:97], v221, v221 op_sel_hi:[0,0,0]
	v_mfma_scale_f32_16x16x128_f8f6f4 v[90:93], v[18:25], v[42:49], v[90:93], v221, v221 op_sel_hi:[0,0,0]
	v_mfma_scale_f32_16x16x128_f8f6f4 v[78:81], v[26:33], v[34:41], v[78:81], v221, v221 op_sel_hi:[0,0,0]
	v_mfma_scale_f32_16x16x128_f8f6f4 v[74:77], v[18:25], v[34:41], v[74:77], v221, v221 op_sel_hi:[0,0,0]
	v_mfma_scale_f32_16x16x128_f8f6f4 v[118:121], v[10:17], v[58:65], v[118:121], v221, v221 op_sel_hi:[0,0,0]
	v_mfma_scale_f32_16x16x128_f8f6f4 v[114:117], v[2:9], v[58:65], v[114:117], v221, v221 op_sel_hi:[0,0,0]
	v_mfma_scale_f32_16x16x128_f8f6f4 v[102:105], v[10:17], v[50:57], v[102:105], v221, v221 op_sel_hi:[0,0,0]
	v_mfma_scale_f32_16x16x128_f8f6f4 v[98:101], v[2:9], v[50:57], v[98:101], v221, v221 op_sel_hi:[0,0,0]
	v_mfma_scale_f32_16x16x128_f8f6f4 v[86:89], v[10:17], v[42:49], v[86:89], v221, v221 op_sel_hi:[0,0,0]
	v_mfma_scale_f32_16x16x128_f8f6f4 v[82:85], v[2:9], v[42:49], v[82:85], v221, v221 op_sel_hi:[0,0,0]
	v_mfma_scale_f32_16x16x128_f8f6f4 v[70:73], v[10:17], v[34:41], v[70:73], v221, v221 op_sel_hi:[0,0,0]
	v_mfma_scale_f32_16x16x128_f8f6f4 v[66:69], v[2:9], v[34:41], v[66:69], v221, v221 op_sel_hi:[0,0,0]
	s_barrier
	s_add_i32 s54, 0, 0x18000
	s_add_i32 s55, 0, 0x1c000
	v_add_u32_e32 v6, s54, v212
	v_add_u32_e32 v14, s54, v213
	v_add_u32_e32 v22, s55, v212
	v_add_u32_e32 v30, s55, v213
	ds_read_b128 v[2:5], v6
	ds_read_b128 v[10:13], v6 offset:2048
	ds_read_b128 v[6:9], v14
	ds_read_b128 v[14:17], v14 offset:2048
	ds_read_b128 v[18:21], v22
	ds_read_b128 v[26:29], v22 offset:2048
	ds_read_b128 v[22:25], v30
	ds_read_b128 v[30:33], v30 offset:2048
	s_add_u32 s20, s20, 0x1000
	s_addc_u32 s21, s21, 0
	s_mov_b32 m0, s36
	v_lshl_add_u64 v[228:229], s[20:21], 0, v[194:195]
	ds_read_b128 v[34:37], v219 offset:32768
	ds_read_b128 v[42:45], v219 offset:34816
	ds_read_b128 v[38:41], v220 offset:32768
	ds_read_b128 v[46:49], v220 offset:34816
	ds_read_b128 v[50:53], v219 offset:36864
	ds_read_b128 v[58:61], v219 offset:38912
	ds_read_b128 v[54:57], v220 offset:36864
	ds_read_b128 v[62:65], v220 offset:38912
	global_load_lds_dwordx4 v[228:229], off
	v_lshl_add_u64 v[228:229], s[20:21], 0, v[198:199]
	s_mov_b32 m0, s37
	s_nop 0
	global_load_lds_dwordx4 v[228:229], off
	s_waitcnt vmcnt(8)
	s_waitcnt lgkmcnt(0)
	s_barrier
	s_waitcnt lgkmcnt(0)
	v_mfma_scale_f32_16x16x128_f8f6f4 v[190:193], v[2:9], v[34:41], v[190:193], v221, v221 op_sel_hi:[0,0,0]
	v_mfma_scale_f32_16x16x128_f8f6f4 v[186:189], v[10:17], v[34:41], v[186:189], v221, v221 op_sel_hi:[0,0,0]
	v_mfma_scale_f32_16x16x128_f8f6f4 v[174:177], v[2:9], v[42:49], v[174:177], v221, v221 op_sel_hi:[0,0,0]
	v_mfma_scale_f32_16x16x128_f8f6f4 v[170:173], v[10:17], v[42:49], v[170:173], v221, v221 op_sel_hi:[0,0,0]
	v_mfma_scale_f32_16x16x128_f8f6f4 v[158:161], v[2:9], v[50:57], v[158:161], v221, v221 op_sel_hi:[0,0,0]
	v_mfma_scale_f32_16x16x128_f8f6f4 v[154:157], v[10:17], v[50:57], v[154:157], v221, v221 op_sel_hi:[0,0,0]
	v_mfma_scale_f32_16x16x128_f8f6f4 v[142:145], v[2:9], v[58:65], v[142:145], v221, v221 op_sel_hi:[0,0,0]
	v_mfma_scale_f32_16x16x128_f8f6f4 v[138:141], v[10:17], v[58:65], v[138:141], v221, v221 op_sel_hi:[0,0,0]
	v_mfma_scale_f32_16x16x128_f8f6f4 v[182:185], v[18:25], v[34:41], v[182:185], v221, v221 op_sel_hi:[0,0,0]
	v_mfma_scale_f32_16x16x128_f8f6f4 v[178:181], v[26:33], v[34:41], v[178:181], v221, v221 op_sel_hi:[0,0,0]
	v_mfma_scale_f32_16x16x128_f8f6f4 v[166:169], v[18:25], v[42:49], v[166:169], v221, v221 op_sel_hi:[0,0,0]
	v_mfma_scale_f32_16x16x128_f8f6f4 v[162:165], v[26:33], v[42:49], v[162:165], v221, v221 op_sel_hi:[0,0,0]
	v_mfma_scale_f32_16x16x128_f8f6f4 v[150:153], v[18:25], v[50:57], v[150:153], v221, v221 op_sel_hi:[0,0,0]
	v_mfma_scale_f32_16x16x128_f8f6f4 v[146:149], v[26:33], v[50:57], v[146:149], v221, v221 op_sel_hi:[0,0,0]
	v_mfma_scale_f32_16x16x128_f8f6f4 v[134:137], v[18:25], v[58:65], v[134:137], v221, v221 op_sel_hi:[0,0,0]
	v_mfma_scale_f32_16x16x128_f8f6f4 v[130:133], v[26:33], v[58:65], v[130:133], v221, v221 op_sel_hi:[0,0,0]
	s_barrier
	s_add_i32 s20, s54, s27
	v_lshl_add_u64 v[228:229], s[24:25], 0, v[196:197]
	s_mov_b32 m0, s20
	ds_read_b128 v[34:37], v219 offset:49152
	ds_read_b128 v[42:45], v219 offset:51200
	ds_read_b128 v[38:41], v220 offset:49152
	ds_read_b128 v[46:49], v220 offset:51200
	ds_read_b128 v[50:53], v219 offset:53248
	ds_read_b128 v[58:61], v219 offset:55296
	ds_read_b128 v[54:57], v220 offset:53248
	ds_read_b128 v[62:65], v220 offset:55296
	global_load_lds_dwordx4 v[228:229], off
	s_add_i32 m0, s20, 0x2000
	s_add_u32 s18, s18, 0x9000
	v_lshl_add_u64 v[228:229], s[24:25], 0, v[200:201]
	s_addc_u32 s19, s19, 0
	s_add_i32 s20, s55, s27
	global_load_lds_dwordx4 v[228:229], off
	v_lshl_add_u64 v[228:229], s[18:19], 0, v[196:197]
	s_mov_b32 m0, s20
	s_nop 0
	global_load_lds_dwordx4 v[228:229], off
	v_lshl_add_u64 v[228:229], s[18:19], 0, v[200:201]
	s_add_i32 m0, s20, 0x2000
	s_nop 0
	global_load_lds_dwordx4 v[228:229], off
	v_lshl_add_u64 v[228:229], s[22:23], 0, v[194:195]
	s_mov_b32 m0, s38
	s_nop 0
	global_load_lds_dwordx4 v[228:229], off
	v_lshl_add_u64 v[228:229], s[22:23], 0, v[198:199]
	s_mov_b32 m0, s39
	s_nop 0
	global_load_lds_dwordx4 v[228:229], off
	s_waitcnt vmcnt(8)
	s_waitcnt lgkmcnt(0)
	s_barrier
	s_waitcnt lgkmcnt(0)
	v_mfma_scale_f32_16x16x128_f8f6f4 v[126:129], v[2:9], v[34:41], v[126:129], v221, v221 op_sel_hi:[0,0,0]
	v_mfma_scale_f32_16x16x128_f8f6f4 v[122:125], v[10:17], v[34:41], v[122:125], v221, v221 op_sel_hi:[0,0,0]
	v_mfma_scale_f32_16x16x128_f8f6f4 v[110:113], v[2:9], v[42:49], v[110:113], v221, v221 op_sel_hi:[0,0,0]
	v_mfma_scale_f32_16x16x128_f8f6f4 v[106:109], v[10:17], v[42:49], v[106:109], v221, v221 op_sel_hi:[0,0,0]
	v_mfma_scale_f32_16x16x128_f8f6f4 v[94:97], v[2:9], v[50:57], v[94:97], v221, v221 op_sel_hi:[0,0,0]
	v_mfma_scale_f32_16x16x128_f8f6f4 v[90:93], v[10:17], v[50:57], v[90:93], v221, v221 op_sel_hi:[0,0,0]
	v_mfma_scale_f32_16x16x128_f8f6f4 v[78:81], v[2:9], v[58:65], v[78:81], v221, v221 op_sel_hi:[0,0,0]
	v_mfma_scale_f32_16x16x128_f8f6f4 v[74:77], v[10:17], v[58:65], v[74:77], v221, v221 op_sel_hi:[0,0,0]
	v_mfma_scale_f32_16x16x128_f8f6f4 v[118:121], v[18:25], v[34:41], v[118:121], v221, v221 op_sel_hi:[0,0,0]
	v_mfma_scale_f32_16x16x128_f8f6f4 v[114:117], v[26:33], v[34:41], v[114:117], v221, v221 op_sel_hi:[0,0,0]
	v_mfma_scale_f32_16x16x128_f8f6f4 v[102:105], v[18:25], v[42:49], v[102:105], v221, v221 op_sel_hi:[0,0,0]
	v_mfma_scale_f32_16x16x128_f8f6f4 v[98:101], v[26:33], v[42:49], v[98:101], v221, v221 op_sel_hi:[0,0,0]
	v_mfma_scale_f32_16x16x128_f8f6f4 v[86:89], v[18:25], v[50:57], v[86:89], v221, v221 op_sel_hi:[0,0,0]
	v_mfma_scale_f32_16x16x128_f8f6f4 v[82:85], v[26:33], v[50:57], v[82:85], v221, v221 op_sel_hi:[0,0,0]
	v_mfma_scale_f32_16x16x128_f8f6f4 v[70:73], v[18:25], v[58:65], v[70:73], v221, v221 op_sel_hi:[0,0,0]
	v_mfma_scale_f32_16x16x128_f8f6f4 v[66:69], v[26:33], v[58:65], v[66:69], v221, v221 op_sel_hi:[0,0,0]
	s_barrier
	s_add_u32 s16, s16, 0x10000
	s_addc_u32 s17, s17, 0
	s_cmp_gt_u32 s50, 41
	s_mov_b32 s50, s53
	s_cbranch_scc1 .LBB0_1949

.LBB0_1945:
	s_add_u32 s18, s14, s16
	s_addc_u32 s19, s15, s17
	s_add_u32 s18, s18, 0x10000
	s_addc_u32 s19, s19, 0
	s_add_u32 s24, s51, s16
	s_addc_u32 s25, s52, s17
	s_waitcnt lgkmcnt(0)
	s_cmp_eq_u32 s16, 0x150000
	s_cselect_b32 s21, s11, s19
	s_cselect_b32 s20, s10, s18
	s_cselect_b32 s19, s13, s25
	s_cselect_b32 s18, s12, s24
	s_barrier
	s_waitcnt lgkmcnt(0)
	v_mfma_scale_f32_16x16x128_f8f6f4 v[190:193], v[26:33], v[58:65], v[190:193], v221, v221 op_sel_hi:[0,0,0]
	v_mfma_scale_f32_16x16x128_f8f6f4 v[186:189], v[18:25], v[58:65], v[186:189], v221, v221 op_sel_hi:[0,0,0]
	v_mfma_scale_f32_16x16x128_f8f6f4 v[174:177], v[26:33], v[50:57], v[174:177], v221, v221 op_sel_hi:[0,0,0]
	v_mfma_scale_f32_16x16x128_f8f6f4 v[170:173], v[18:25], v[50:57], v[170:173], v221, v221 op_sel_hi:[0,0,0]
	v_mfma_scale_f32_16x16x128_f8f6f4 v[158:161], v[26:33], v[42:49], v[158:161], v221, v221 op_sel_hi:[0,0,0]
	v_mfma_scale_f32_16x16x128_f8f6f4 v[154:157], v[18:25], v[42:49], v[154:157], v221, v221 op_sel_hi:[0,0,0]
	v_mfma_scale_f32_16x16x128_f8f6f4 v[142:145], v[26:33], v[34:41], v[142:145], v221, v221 op_sel_hi:[0,0,0]
	v_mfma_scale_f32_16x16x128_f8f6f4 v[138:141], v[18:25], v[34:41], v[138:141], v221, v221 op_sel_hi:[0,0,0]
	v_mfma_scale_f32_16x16x128_f8f6f4 v[182:185], v[10:17], v[58:65], v[182:185], v221, v221 op_sel_hi:[0,0,0]
	v_mfma_scale_f32_16x16x128_f8f6f4 v[178:181], v[2:9], v[58:65], v[178:181], v221, v221 op_sel_hi:[0,0,0]
	v_mfma_scale_f32_16x16x128_f8f6f4 v[166:169], v[10:17], v[50:57], v[166:169], v221, v221 op_sel_hi:[0,0,0]
	v_mfma_scale_f32_16x16x128_f8f6f4 v[162:165], v[2:9], v[50:57], v[162:165], v221, v221 op_sel_hi:[0,0,0]
	v_mfma_scale_f32_16x16x128_f8f6f4 v[150:153], v[10:17], v[42:49], v[150:153], v221, v221 op_sel_hi:[0,0,0]
	v_mfma_scale_f32_16x16x128_f8f6f4 v[146:149], v[2:9], v[42:49], v[146:149], v221, v221 op_sel_hi:[0,0,0]
	v_mfma_scale_f32_16x16x128_f8f6f4 v[134:137], v[10:17], v[34:41], v[134:137], v221, v221 op_sel_hi:[0,0,0]
	v_mfma_scale_f32_16x16x128_f8f6f4 v[130:133], v[2:9], v[34:41], v[130:133], v221, v221 op_sel_hi:[0,0,0]
	s_barrier
	s_mov_b32 m0, s29
	v_lshl_add_u64 v[228:229], s[18:19], 0, v[196:197]
	s_add_u32 s24, s18, 0x1000
	ds_read_b128 v[58:61], v219 offset:16384
	ds_read_b128 v[50:53], v219 offset:18432
	ds_read_b128 v[62:65], v220 offset:16384
	ds_read_b128 v[54:57], v220 offset:18432
	ds_read_b128 v[42:45], v219 offset:20480
	ds_read_b128 v[34:37], v219 offset:22528
	ds_read_b128 v[46:49], v220 offset:20480
	ds_read_b128 v[38:41], v220 offset:22528
	global_load_lds_dwordx4 v[228:229], off
	v_lshl_add_u64 v[228:229], s[18:19], 0, v[200:201]
	s_mov_b32 m0, s30
	s_addc_u32 s25, s19, 0
	global_load_lds_dwordx4 v[228:229], off
	v_lshl_add_u64 v[228:229], s[24:25], 0, v[196:197]
	s_mov_b32 m0, s31
	s_and_b64 vcc, exec, s[22:23]
	global_load_lds_dwordx4 v[228:229], off
	v_lshl_add_u64 v[228:229], s[24:25], 0, v[200:201]
	s_mov_b32 m0, s34
	s_mov_b64 s[24:25], -1
	global_load_lds_dwordx4 v[228:229], off
	v_lshl_add_u64 v[228:229], s[20:21], 0, v[194:195]
	s_mov_b32 m0, s28
	s_nop 0
	global_load_lds_dwordx4 v[228:229], off
	v_lshl_add_u64 v[228:229], s[20:21], 0, v[198:199]
	s_mov_b32 m0, s35
	s_nop 0
	global_load_lds_dwordx4 v[228:229], off
	s_cbranch_vccz .LBB0_1947
	s_waitcnt vmcnt(8)
	s_mov_b64 s[24:25], 0

.LBB0_2078:
	s_waitcnt lgkmcnt(0)
	s_add_i32 s42, s68, 2
	s_add_u32 s40, s36, 0x8000
	s_addc_u32 s41, s37, 0
	s_barrier
	s_waitcnt lgkmcnt(0)
	v_mfma_i32_16x16x64_i8 v[62:65], v[146:149], v[186:189], v[62:65]
	v_mfma_i32_16x16x64_i8 v[58:61], v[150:153], v[186:189], v[58:61]
	v_mfma_i32_16x16x64_i8 v[46:49], v[146:149], v[178:181], v[46:49]
	v_mfma_i32_16x16x64_i8 v[42:45], v[150:153], v[178:181], v[42:45]
	v_mfma_i32_16x16x64_i8 v[30:33], v[146:149], v[170:173], v[30:33]
	v_mfma_i32_16x16x64_i8 v[26:29], v[150:153], v[170:173], v[26:29]
	v_mfma_i32_16x16x64_i8 v[14:17], v[146:149], v[162:165], v[14:17]
	v_mfma_i32_16x16x64_i8 v[10:13], v[150:153], v[162:165], v[10:13]
	v_mfma_i32_16x16x64_i8 v[62:65], v[158:161], v[190:193], v[62:65]
	v_mfma_i32_16x16x64_i8 v[58:61], v[154:157], v[190:193], v[58:61]
	v_mfma_i32_16x16x64_i8 v[46:49], v[158:161], v[182:185], v[46:49]
	v_mfma_i32_16x16x64_i8 v[42:45], v[154:157], v[182:185], v[42:45]
	v_mfma_i32_16x16x64_i8 v[30:33], v[158:161], v[174:177], v[30:33]
	v_mfma_i32_16x16x64_i8 v[26:29], v[154:157], v[174:177], v[26:29]
	v_mfma_i32_16x16x64_i8 v[14:17], v[158:161], v[166:169], v[14:17]
	v_mfma_i32_16x16x64_i8 v[10:13], v[154:157], v[166:169], v[10:13]
	v_mfma_i32_16x16x64_i8 v[54:57], v[122:125], v[186:189], v[54:57]
	v_mfma_i32_16x16x64_i8 v[50:53], v[126:129], v[186:189], v[50:53]
	v_mfma_i32_16x16x64_i8 v[38:41], v[122:125], v[178:181], v[38:41]
	v_mfma_i32_16x16x64_i8 v[34:37], v[126:129], v[178:181], v[34:37]
	v_mfma_i32_16x16x64_i8 v[22:25], v[122:125], v[170:173], v[22:25]
	v_mfma_i32_16x16x64_i8 v[18:21], v[126:129], v[170:173], v[18:21]
	v_mfma_i32_16x16x64_i8 v[6:9], v[122:125], v[162:165], v[6:9]
	v_mfma_i32_16x16x64_i8 v[2:5], v[126:129], v[162:165], v[2:5]
	v_mfma_i32_16x16x64_i8 v[54:57], v[142:145], v[190:193], v[54:57]
	v_mfma_i32_16x16x64_i8 v[50:53], v[138:141], v[190:193], v[50:53]
	v_mfma_i32_16x16x64_i8 v[38:41], v[142:145], v[182:185], v[38:41]
	v_mfma_i32_16x16x64_i8 v[34:37], v[138:141], v[182:185], v[34:37]
	v_mfma_i32_16x16x64_i8 v[22:25], v[142:145], v[174:177], v[22:25]
	v_mfma_i32_16x16x64_i8 v[18:21], v[138:141], v[174:177], v[18:21]
	v_mfma_i32_16x16x64_i8 v[6:9], v[142:145], v[166:169], v[6:9]
	v_mfma_i32_16x16x64_i8 v[2:5], v[138:141], v[166:169], v[2:5]
	s_barrier
	s_add_i32 s43, 0, 0x18000
	s_add_i32 s71, 0, 0x1c000
	v_add_u32_e32 v126, s43, v1
	v_add_u32_e32 v142, s43, v234
	v_add_u32_e32 v150, s71, v1
	v_add_u32_e32 v158, s71, v234
	ds_read_b128 v[122:125], v126
	ds_read_b128 v[126:129], v126 offset:2048
	ds_read_b128 v[138:141], v142
	ds_read_b128 v[142:145], v142 offset:2048
	ds_read_b128 v[146:149], v150
	ds_read_b128 v[150:153], v150 offset:2048
	ds_read_b128 v[154:157], v158
	ds_read_b128 v[158:161], v158 offset:2048
	s_add_u32 s38, s38, 0x40000
	s_addc_u32 s39, s39, 0
	s_mov_b32 m0, s50
	v_lshl_add_u64 v[240:241], s[38:39], 0, v[194:195]
	ds_read_b128 v[162:165], v237 offset:32768
	ds_read_b128 v[166:169], v237 offset:33792
	ds_read_b128 v[170:173], v237 offset:34816
	ds_read_b128 v[174:177], v237 offset:35840
	ds_read_b128 v[178:181], v237 offset:36864
	ds_read_b128 v[182:185], v237 offset:37888
	ds_read_b128 v[186:189], v237 offset:38912
	ds_read_b128 v[190:193], v237 offset:39936
	global_load_lds_dwordx4 v[240:241], off
	v_lshl_add_u64 v[240:241], s[38:39], 0, v[198:199]
	s_mov_b32 m0, s51
	s_nop 0
	global_load_lds_dwordx4 v[240:241], off
	s_waitcnt vmcnt(8)
	s_waitcnt lgkmcnt(0)
	s_barrier
	s_waitcnt lgkmcnt(0)
	v_mfma_i32_16x16x64_i8 v[134:137], v[122:125], v[162:165], v[134:137]
	v_mfma_i32_16x16x64_i8 v[130:133], v[126:129], v[162:165], v[130:133]
	v_mfma_i32_16x16x64_i8 v[110:113], v[122:125], v[170:173], v[110:113]
	v_mfma_i32_16x16x64_i8 v[106:109], v[126:129], v[170:173], v[106:109]
	v_mfma_i32_16x16x64_i8 v[94:97], v[122:125], v[178:181], v[94:97]
	v_mfma_i32_16x16x64_i8 v[90:93], v[126:129], v[178:181], v[90:93]
	v_mfma_i32_16x16x64_i8 v[78:81], v[122:125], v[186:189], v[78:81]
	v_mfma_i32_16x16x64_i8 v[74:77], v[126:129], v[186:189], v[74:77]
	v_mfma_i32_16x16x64_i8 v[134:137], v[138:141], v[166:169], v[134:137]
	v_mfma_i32_16x16x64_i8 v[130:133], v[142:145], v[166:169], v[130:133]
	v_mfma_i32_16x16x64_i8 v[110:113], v[138:141], v[174:177], v[110:113]
	v_mfma_i32_16x16x64_i8 v[106:109], v[142:145], v[174:177], v[106:109]
	v_mfma_i32_16x16x64_i8 v[94:97], v[138:141], v[182:185], v[94:97]
	v_mfma_i32_16x16x64_i8 v[90:93], v[142:145], v[182:185], v[90:93]
	v_mfma_i32_16x16x64_i8 v[78:81], v[138:141], v[190:193], v[78:81]
	v_mfma_i32_16x16x64_i8 v[74:77], v[142:145], v[190:193], v[74:77]
	v_mfma_i32_16x16x64_i8 v[118:121], v[146:149], v[162:165], v[118:121]
	v_mfma_i32_16x16x64_i8 v[114:117], v[150:153], v[162:165], v[114:117]
	v_mfma_i32_16x16x64_i8 v[102:105], v[146:149], v[170:173], v[102:105]
	v_mfma_i32_16x16x64_i8 v[98:101], v[150:153], v[170:173], v[98:101]
	v_mfma_i32_16x16x64_i8 v[86:89], v[146:149], v[178:181], v[86:89]
	v_mfma_i32_16x16x64_i8 v[82:85], v[150:153], v[178:181], v[82:85]
	v_mfma_i32_16x16x64_i8 v[70:73], v[146:149], v[186:189], v[70:73]
	v_mfma_i32_16x16x64_i8 v[66:69], v[150:153], v[186:189], v[66:69]
	v_mfma_i32_16x16x64_i8 v[118:121], v[154:157], v[166:169], v[118:121]
	v_mfma_i32_16x16x64_i8 v[114:117], v[158:161], v[166:169], v[114:117]
	v_mfma_i32_16x16x64_i8 v[102:105], v[154:157], v[174:177], v[102:105]
	v_mfma_i32_16x16x64_i8 v[98:101], v[158:161], v[174:177], v[98:101]
	v_mfma_i32_16x16x64_i8 v[86:89], v[154:157], v[182:185], v[86:89]
	v_mfma_i32_16x16x64_i8 v[82:85], v[158:161], v[182:185], v[82:85]
	v_mfma_i32_16x16x64_i8 v[70:73], v[154:157], v[190:193], v[70:73]
	v_mfma_i32_16x16x64_i8 v[66:69], v[158:161], v[190:193], v[66:69]
	s_barrier
	s_add_i32 s38, s43, s44
	v_lshl_add_u64 v[240:241], s[40:41], 0, v[196:197]
	s_mov_b32 m0, s38
	ds_read_b128 v[162:165], v237 offset:49152
	ds_read_b128 v[166:169], v237 offset:50176
	ds_read_b128 v[170:173], v237 offset:51200
	ds_read_b128 v[174:177], v237 offset:52224
	ds_read_b128 v[178:181], v237 offset:53248
	ds_read_b128 v[182:185], v237 offset:54272
	ds_read_b128 v[186:189], v237 offset:55296
	ds_read_b128 v[190:193], v237 offset:56320
	global_load_lds_dwordx4 v[240:241], off
	s_add_i32 m0, s38, 0x2000
	s_add_u32 s36, s36, 0x9000
	v_lshl_add_u64 v[240:241], s[40:41], 0, v[200:201]
	s_addc_u32 s37, s37, 0
	s_add_i32 s38, s71, s44
	global_load_lds_dwordx4 v[240:241], off
	v_lshl_add_u64 v[240:241], s[36:37], 0, v[196:197]
	s_mov_b32 m0, s38
	v_lshl_add_u64 v[214:215], v[214:215], 0, s[12:13]
	global_load_lds_dwordx4 v[240:241], off
	v_lshl_add_u64 v[240:241], s[36:37], 0, v[200:201]
	s_add_i32 m0, s38, 0x2000
	s_nop 0
	global_load_lds_dwordx4 v[240:241], off
	s_mov_b32 m0, s54
	s_nop 0
	global_load_lds_dwordx4 v[214:215], off
	v_lshl_add_u64 v[214:215], v[216:217], 0, s[12:13]
	s_mov_b32 m0, s55
	s_nop 0
	global_load_lds_dwordx4 v[214:215], off
	s_waitcnt vmcnt(8)
	s_waitcnt lgkmcnt(0)
	s_barrier
	s_waitcnt lgkmcnt(0)
	v_mfma_i32_16x16x64_i8 v[62:65], v[122:125], v[162:165], v[62:65]
	v_mfma_i32_16x16x64_i8 v[58:61], v[126:129], v[162:165], v[58:61]
	v_mfma_i32_16x16x64_i8 v[46:49], v[122:125], v[170:173], v[46:49]
	v_mfma_i32_16x16x64_i8 v[42:45], v[126:129], v[170:173], v[42:45]
	v_mfma_i32_16x16x64_i8 v[30:33], v[122:125], v[178:181], v[30:33]
	v_mfma_i32_16x16x64_i8 v[26:29], v[126:129], v[178:181], v[26:29]
	v_mfma_i32_16x16x64_i8 v[14:17], v[122:125], v[186:189], v[14:17]
	v_mfma_i32_16x16x64_i8 v[10:13], v[126:129], v[186:189], v[10:13]
	v_mfma_i32_16x16x64_i8 v[62:65], v[138:141], v[166:169], v[62:65]
	v_mfma_i32_16x16x64_i8 v[58:61], v[142:145], v[166:169], v[58:61]
	v_mfma_i32_16x16x64_i8 v[46:49], v[138:141], v[174:177], v[46:49]
	v_mfma_i32_16x16x64_i8 v[42:45], v[142:145], v[174:177], v[42:45]
	v_mfma_i32_16x16x64_i8 v[30:33], v[138:141], v[182:185], v[30:33]
	v_mfma_i32_16x16x64_i8 v[26:29], v[142:145], v[182:185], v[26:29]
	v_mfma_i32_16x16x64_i8 v[14:17], v[138:141], v[190:193], v[14:17]
	v_mfma_i32_16x16x64_i8 v[10:13], v[142:145], v[190:193], v[10:13]
	v_mfma_i32_16x16x64_i8 v[54:57], v[146:149], v[162:165], v[54:57]
	v_mfma_i32_16x16x64_i8 v[50:53], v[150:153], v[162:165], v[50:53]
	v_mfma_i32_16x16x64_i8 v[38:41], v[146:149], v[170:173], v[38:41]
	v_mfma_i32_16x16x64_i8 v[34:37], v[150:153], v[170:173], v[34:37]
	v_mfma_i32_16x16x64_i8 v[22:25], v[146:149], v[178:181], v[22:25]
	v_mfma_i32_16x16x64_i8 v[18:21], v[150:153], v[178:181], v[18:21]
	v_mfma_i32_16x16x64_i8 v[6:9], v[146:149], v[186:189], v[6:9]
	v_mfma_i32_16x16x64_i8 v[2:5], v[150:153], v[186:189], v[2:5]
	v_mfma_i32_16x16x64_i8 v[54:57], v[154:157], v[166:169], v[54:57]
	v_mfma_i32_16x16x64_i8 v[50:53], v[158:161], v[166:169], v[50:53]
	v_mfma_i32_16x16x64_i8 v[38:41], v[154:157], v[174:177], v[38:41]
	v_mfma_i32_16x16x64_i8 v[34:37], v[158:161], v[174:177], v[34:37]
	v_mfma_i32_16x16x64_i8 v[22:25], v[154:157], v[182:185], v[22:25]
	v_mfma_i32_16x16x64_i8 v[18:21], v[158:161], v[182:185], v[18:21]
	v_mfma_i32_16x16x64_i8 v[6:9], v[154:157], v[190:193], v[6:9]
	v_mfma_i32_16x16x64_i8 v[2:5], v[158:161], v[190:193], v[2:5]
	s_barrier
	s_add_u32 s69, s69, 0x10000
	s_addc_u32 s70, s70, 0
	s_add_u32 s34, s34, 0x100
	s_addc_u32 s35, s35, 0
	s_cmp_gt_u32 s68, 13
	s_mov_b32 s68, s42
	s_cbranch_scc1 .LBB0_2087

.LBB0_2083:
	s_add_u32 s36, s0, s34
	s_addc_u32 s37, s1, s35
	s_add_u32 s36, s36, 0x100
	s_addc_u32 s37, s37, 0
	s_waitcnt lgkmcnt(0)
	s_cmpk_eq_i32 s34, 0x700
	s_cselect_b32 s39, s2, s37
	s_cselect_b32 s38, s21, s36
	s_cselect_b32 s37, s19, s70
	s_cselect_b32 s36, s66, s69
	s_barrier
	s_waitcnt lgkmcnt(0)
	v_mfma_i32_16x16x64_i8 v[134:137], v[146:149], v[186:189], v[134:137]
	v_mfma_i32_16x16x64_i8 v[130:133], v[150:153], v[186:189], v[130:133]
	v_mfma_i32_16x16x64_i8 v[110:113], v[146:149], v[178:181], v[110:113]
	v_mfma_i32_16x16x64_i8 v[106:109], v[150:153], v[178:181], v[106:109]
	v_mfma_i32_16x16x64_i8 v[94:97], v[146:149], v[170:173], v[94:97]
	v_mfma_i32_16x16x64_i8 v[90:93], v[150:153], v[170:173], v[90:93]
	v_mfma_i32_16x16x64_i8 v[78:81], v[146:149], v[162:165], v[78:81]
	v_mfma_i32_16x16x64_i8 v[74:77], v[150:153], v[162:165], v[74:77]
	v_mfma_i32_16x16x64_i8 v[134:137], v[158:161], v[190:193], v[134:137]
	v_mfma_i32_16x16x64_i8 v[130:133], v[154:157], v[190:193], v[130:133]
	v_mfma_i32_16x16x64_i8 v[110:113], v[158:161], v[182:185], v[110:113]
	v_mfma_i32_16x16x64_i8 v[106:109], v[154:157], v[182:185], v[106:109]
	v_mfma_i32_16x16x64_i8 v[94:97], v[158:161], v[174:177], v[94:97]
	v_mfma_i32_16x16x64_i8 v[90:93], v[154:157], v[174:177], v[90:93]
	v_mfma_i32_16x16x64_i8 v[78:81], v[158:161], v[166:169], v[78:81]
	v_mfma_i32_16x16x64_i8 v[74:77], v[154:157], v[166:169], v[74:77]
	v_mfma_i32_16x16x64_i8 v[118:121], v[122:125], v[186:189], v[118:121]
	v_mfma_i32_16x16x64_i8 v[114:117], v[126:129], v[186:189], v[114:117]
	v_mfma_i32_16x16x64_i8 v[102:105], v[122:125], v[178:181], v[102:105]
	v_mfma_i32_16x16x64_i8 v[98:101], v[126:129], v[178:181], v[98:101]
	v_mfma_i32_16x16x64_i8 v[86:89], v[122:125], v[170:173], v[86:89]
	v_mfma_i32_16x16x64_i8 v[82:85], v[126:129], v[170:173], v[82:85]
	v_mfma_i32_16x16x64_i8 v[70:73], v[122:125], v[162:165], v[70:73]
	v_mfma_i32_16x16x64_i8 v[66:69], v[126:129], v[162:165], v[66:69]
	v_mfma_i32_16x16x64_i8 v[118:121], v[142:145], v[190:193], v[118:121]
	v_mfma_i32_16x16x64_i8 v[114:117], v[138:141], v[190:193], v[114:117]
	v_mfma_i32_16x16x64_i8 v[102:105], v[142:145], v[182:185], v[102:105]
	v_mfma_i32_16x16x64_i8 v[98:101], v[138:141], v[182:185], v[98:101]
	v_mfma_i32_16x16x64_i8 v[86:89], v[142:145], v[174:177], v[86:89]
	v_mfma_i32_16x16x64_i8 v[82:85], v[138:141], v[174:177], v[82:85]
	v_mfma_i32_16x16x64_i8 v[70:73], v[142:145], v[166:169], v[70:73]
	v_mfma_i32_16x16x64_i8 v[66:69], v[138:141], v[166:169], v[66:69]
	s_barrier
	s_mov_b32 m0, s31
	v_lshl_add_u64 v[214:215], s[36:37], 0, v[196:197]
	s_add_u32 s42, s36, 0x1000
	ds_read_b128 v[186:189], v237 offset:16384
	ds_read_b128 v[190:193], v237 offset:17408
	ds_read_b128 v[178:181], v237 offset:18432
	ds_read_b128 v[182:185], v237 offset:19456
	ds_read_b128 v[170:173], v237 offset:20480
	ds_read_b128 v[174:177], v237 offset:21504
	ds_read_b128 v[162:165], v237 offset:22528
	ds_read_b128 v[166:169], v237 offset:23552
	global_load_lds_dwordx4 v[214:215], off
	v_lshl_add_u64 v[214:215], s[36:37], 0, v[200:201]
	s_mov_b32 m0, s45
	s_addc_u32 s43, s37, 0
	global_load_lds_dwordx4 v[214:215], off
	v_lshl_add_u64 v[214:215], s[42:43], 0, v[196:197]
	s_mov_b32 m0, s46
	v_lshl_add_u64 v[216:217], s[38:39], 0, v[198:199]
	global_load_lds_dwordx4 v[214:215], off
	v_lshl_add_u64 v[214:215], s[42:43], 0, v[200:201]
	s_mov_b32 m0, s47
	s_mov_b64 s[42:43], -1
	global_load_lds_dwordx4 v[214:215], off
	v_lshl_add_u64 v[214:215], s[38:39], 0, v[194:195]
	s_mov_b32 m0, s29
	s_and_b64 vcc, exec, s[40:41]
	global_load_lds_dwordx4 v[214:215], off
	s_mov_b32 m0, s49
	s_nop 0
	global_load_lds_dwordx4 v[216:217], off
	s_cbranch_vccz .LBB0_2085
	s_waitcnt vmcnt(8)
	s_mov_b64 s[42:43], 0

.LBB0_2501:
	s_waitcnt lgkmcnt(0)
	s_add_i32 s42, s68, 2
	s_add_u32 s40, s36, 0x8000
	s_addc_u32 s41, s37, 0
	s_barrier
	s_waitcnt lgkmcnt(0)
	v_mfma_i32_16x16x64_i8 v[62:65], v[146:149], v[186:189], v[62:65]
	v_mfma_i32_16x16x64_i8 v[58:61], v[150:153], v[186:189], v[58:61]
	v_mfma_i32_16x16x64_i8 v[46:49], v[146:149], v[178:181], v[46:49]
	v_mfma_i32_16x16x64_i8 v[42:45], v[150:153], v[178:181], v[42:45]
	v_mfma_i32_16x16x64_i8 v[30:33], v[146:149], v[170:173], v[30:33]
	v_mfma_i32_16x16x64_i8 v[26:29], v[150:153], v[170:173], v[26:29]
	v_mfma_i32_16x16x64_i8 v[14:17], v[146:149], v[162:165], v[14:17]
	v_mfma_i32_16x16x64_i8 v[10:13], v[150:153], v[162:165], v[10:13]
	v_mfma_i32_16x16x64_i8 v[62:65], v[158:161], v[190:193], v[62:65]
	v_mfma_i32_16x16x64_i8 v[58:61], v[154:157], v[190:193], v[58:61]
	v_mfma_i32_16x16x64_i8 v[46:49], v[158:161], v[182:185], v[46:49]
	v_mfma_i32_16x16x64_i8 v[42:45], v[154:157], v[182:185], v[42:45]
	v_mfma_i32_16x16x64_i8 v[30:33], v[158:161], v[174:177], v[30:33]
	v_mfma_i32_16x16x64_i8 v[26:29], v[154:157], v[174:177], v[26:29]
	v_mfma_i32_16x16x64_i8 v[14:17], v[158:161], v[166:169], v[14:17]
	v_mfma_i32_16x16x64_i8 v[10:13], v[154:157], v[166:169], v[10:13]
	v_mfma_i32_16x16x64_i8 v[54:57], v[122:125], v[186:189], v[54:57]
	v_mfma_i32_16x16x64_i8 v[50:53], v[126:129], v[186:189], v[50:53]
	v_mfma_i32_16x16x64_i8 v[38:41], v[122:125], v[178:181], v[38:41]
	v_mfma_i32_16x16x64_i8 v[34:37], v[126:129], v[178:181], v[34:37]
	v_mfma_i32_16x16x64_i8 v[22:25], v[122:125], v[170:173], v[22:25]
	v_mfma_i32_16x16x64_i8 v[18:21], v[126:129], v[170:173], v[18:21]
	v_mfma_i32_16x16x64_i8 v[6:9], v[122:125], v[162:165], v[6:9]
	v_mfma_i32_16x16x64_i8 v[2:5], v[126:129], v[162:165], v[2:5]
	v_mfma_i32_16x16x64_i8 v[54:57], v[142:145], v[190:193], v[54:57]
	v_mfma_i32_16x16x64_i8 v[50:53], v[138:141], v[190:193], v[50:53]
	v_mfma_i32_16x16x64_i8 v[38:41], v[142:145], v[182:185], v[38:41]
	v_mfma_i32_16x16x64_i8 v[34:37], v[138:141], v[182:185], v[34:37]
	v_mfma_i32_16x16x64_i8 v[22:25], v[142:145], v[174:177], v[22:25]
	v_mfma_i32_16x16x64_i8 v[18:21], v[138:141], v[174:177], v[18:21]
	v_mfma_i32_16x16x64_i8 v[6:9], v[142:145], v[166:169], v[6:9]
	v_mfma_i32_16x16x64_i8 v[2:5], v[138:141], v[166:169], v[2:5]
	s_barrier
	s_add_i32 s43, 0, 0x18000
	s_add_i32 s71, 0, 0x1c000
	v_add_u32_e32 v126, s43, v1
	v_add_u32_e32 v142, s43, v232
	v_add_u32_e32 v150, s71, v1
	v_add_u32_e32 v158, s71, v232
	ds_read_b128 v[122:125], v126
	ds_read_b128 v[126:129], v126 offset:2048
	ds_read_b128 v[138:141], v142
	ds_read_b128 v[142:145], v142 offset:2048
	ds_read_b128 v[146:149], v150
	ds_read_b128 v[150:153], v150 offset:2048
	ds_read_b128 v[154:157], v158
	ds_read_b128 v[158:161], v158 offset:2048
	s_add_u32 s38, s38, 0x40000
	s_addc_u32 s39, s39, 0
	s_mov_b32 m0, s52
	v_lshl_add_u64 v[236:237], s[38:39], 0, v[194:195]
	ds_read_b128 v[162:165], v233 offset:32768
	ds_read_b128 v[166:169], v233 offset:33792
	ds_read_b128 v[170:173], v233 offset:34816
	ds_read_b128 v[174:177], v233 offset:35840
	ds_read_b128 v[178:181], v233 offset:36864
	ds_read_b128 v[182:185], v233 offset:37888
	ds_read_b128 v[186:189], v233 offset:38912
	ds_read_b128 v[190:193], v233 offset:39936
	global_load_lds_dwordx4 v[236:237], off
	v_lshl_add_u64 v[236:237], s[38:39], 0, v[198:199]
	s_mov_b32 m0, s53
	s_nop 0
	global_load_lds_dwordx4 v[236:237], off
	s_waitcnt vmcnt(8)
	s_waitcnt lgkmcnt(0)
	s_barrier
	s_waitcnt lgkmcnt(0)
	v_mfma_i32_16x16x64_i8 v[134:137], v[122:125], v[162:165], v[134:137]
	v_mfma_i32_16x16x64_i8 v[130:133], v[126:129], v[162:165], v[130:133]
	v_mfma_i32_16x16x64_i8 v[110:113], v[122:125], v[170:173], v[110:113]
	v_mfma_i32_16x16x64_i8 v[106:109], v[126:129], v[170:173], v[106:109]
	v_mfma_i32_16x16x64_i8 v[94:97], v[122:125], v[178:181], v[94:97]
	v_mfma_i32_16x16x64_i8 v[90:93], v[126:129], v[178:181], v[90:93]
	v_mfma_i32_16x16x64_i8 v[78:81], v[122:125], v[186:189], v[78:81]
	v_mfma_i32_16x16x64_i8 v[74:77], v[126:129], v[186:189], v[74:77]
	v_mfma_i32_16x16x64_i8 v[134:137], v[138:141], v[166:169], v[134:137]
	v_mfma_i32_16x16x64_i8 v[130:133], v[142:145], v[166:169], v[130:133]
	v_mfma_i32_16x16x64_i8 v[110:113], v[138:141], v[174:177], v[110:113]
	v_mfma_i32_16x16x64_i8 v[106:109], v[142:145], v[174:177], v[106:109]
	v_mfma_i32_16x16x64_i8 v[94:97], v[138:141], v[182:185], v[94:97]
	v_mfma_i32_16x16x64_i8 v[90:93], v[142:145], v[182:185], v[90:93]
	v_mfma_i32_16x16x64_i8 v[78:81], v[138:141], v[190:193], v[78:81]
	v_mfma_i32_16x16x64_i8 v[74:77], v[142:145], v[190:193], v[74:77]
	v_mfma_i32_16x16x64_i8 v[118:121], v[146:149], v[162:165], v[118:121]
	v_mfma_i32_16x16x64_i8 v[114:117], v[150:153], v[162:165], v[114:117]
	v_mfma_i32_16x16x64_i8 v[102:105], v[146:149], v[170:173], v[102:105]
	v_mfma_i32_16x16x64_i8 v[98:101], v[150:153], v[170:173], v[98:101]
	v_mfma_i32_16x16x64_i8 v[86:89], v[146:149], v[178:181], v[86:89]
	v_mfma_i32_16x16x64_i8 v[82:85], v[150:153], v[178:181], v[82:85]
	v_mfma_i32_16x16x64_i8 v[70:73], v[146:149], v[186:189], v[70:73]
	v_mfma_i32_16x16x64_i8 v[66:69], v[150:153], v[186:189], v[66:69]
	v_mfma_i32_16x16x64_i8 v[118:121], v[154:157], v[166:169], v[118:121]
	v_mfma_i32_16x16x64_i8 v[114:117], v[158:161], v[166:169], v[114:117]
	v_mfma_i32_16x16x64_i8 v[102:105], v[154:157], v[174:177], v[102:105]
	v_mfma_i32_16x16x64_i8 v[98:101], v[158:161], v[174:177], v[98:101]
	v_mfma_i32_16x16x64_i8 v[86:89], v[154:157], v[182:185], v[86:89]
	v_mfma_i32_16x16x64_i8 v[82:85], v[158:161], v[182:185], v[82:85]
	v_mfma_i32_16x16x64_i8 v[70:73], v[154:157], v[190:193], v[70:73]
	v_mfma_i32_16x16x64_i8 v[66:69], v[158:161], v[190:193], v[66:69]
	s_barrier
	s_add_i32 s38, s43, s46
	v_lshl_add_u64 v[236:237], s[40:41], 0, v[196:197]
	s_mov_b32 m0, s38
	ds_read_b128 v[162:165], v233 offset:49152
	ds_read_b128 v[166:169], v233 offset:50176
	ds_read_b128 v[170:173], v233 offset:51200
	ds_read_b128 v[174:177], v233 offset:52224
	ds_read_b128 v[178:181], v233 offset:53248
	ds_read_b128 v[182:185], v233 offset:54272
	ds_read_b128 v[186:189], v233 offset:55296
	ds_read_b128 v[190:193], v233 offset:56320
	global_load_lds_dwordx4 v[236:237], off
	s_add_i32 m0, s38, 0x2000
	s_add_u32 s36, s36, 0x9000
	v_lshl_add_u64 v[236:237], s[40:41], 0, v[200:201]
	s_addc_u32 s37, s37, 0
	s_add_i32 s38, s71, s46
	global_load_lds_dwordx4 v[236:237], off
	v_lshl_add_u64 v[236:237], s[36:37], 0, v[196:197]
	s_mov_b32 m0, s38
	v_lshl_add_u64 v[214:215], v[214:215], 0, s[12:13]
	global_load_lds_dwordx4 v[236:237], off
	v_lshl_add_u64 v[236:237], s[36:37], 0, v[200:201]
	s_add_i32 m0, s38, 0x2000
	s_nop 0
	global_load_lds_dwordx4 v[236:237], off
	s_mov_b32 m0, s56
	s_nop 0
	global_load_lds_dwordx4 v[214:215], off
	v_lshl_add_u64 v[214:215], v[216:217], 0, s[12:13]
	s_mov_b32 m0, s57
	s_nop 0
	global_load_lds_dwordx4 v[214:215], off
	s_waitcnt vmcnt(8)
	s_waitcnt lgkmcnt(0)
	s_barrier
	s_waitcnt lgkmcnt(0)
	v_mfma_i32_16x16x64_i8 v[62:65], v[122:125], v[162:165], v[62:65]
	v_mfma_i32_16x16x64_i8 v[58:61], v[126:129], v[162:165], v[58:61]
	v_mfma_i32_16x16x64_i8 v[46:49], v[122:125], v[170:173], v[46:49]
	v_mfma_i32_16x16x64_i8 v[42:45], v[126:129], v[170:173], v[42:45]
	v_mfma_i32_16x16x64_i8 v[30:33], v[122:125], v[178:181], v[30:33]
	v_mfma_i32_16x16x64_i8 v[26:29], v[126:129], v[178:181], v[26:29]
	v_mfma_i32_16x16x64_i8 v[14:17], v[122:125], v[186:189], v[14:17]
	v_mfma_i32_16x16x64_i8 v[10:13], v[126:129], v[186:189], v[10:13]
	v_mfma_i32_16x16x64_i8 v[62:65], v[138:141], v[166:169], v[62:65]
	v_mfma_i32_16x16x64_i8 v[58:61], v[142:145], v[166:169], v[58:61]
	v_mfma_i32_16x16x64_i8 v[46:49], v[138:141], v[174:177], v[46:49]
	v_mfma_i32_16x16x64_i8 v[42:45], v[142:145], v[174:177], v[42:45]
	v_mfma_i32_16x16x64_i8 v[30:33], v[138:141], v[182:185], v[30:33]
	v_mfma_i32_16x16x64_i8 v[26:29], v[142:145], v[182:185], v[26:29]
	v_mfma_i32_16x16x64_i8 v[14:17], v[138:141], v[190:193], v[14:17]
	v_mfma_i32_16x16x64_i8 v[10:13], v[142:145], v[190:193], v[10:13]
	v_mfma_i32_16x16x64_i8 v[54:57], v[146:149], v[162:165], v[54:57]
	v_mfma_i32_16x16x64_i8 v[50:53], v[150:153], v[162:165], v[50:53]
	v_mfma_i32_16x16x64_i8 v[38:41], v[146:149], v[170:173], v[38:41]
	v_mfma_i32_16x16x64_i8 v[34:37], v[150:153], v[170:173], v[34:37]
	v_mfma_i32_16x16x64_i8 v[22:25], v[146:149], v[178:181], v[22:25]
	v_mfma_i32_16x16x64_i8 v[18:21], v[150:153], v[178:181], v[18:21]
	v_mfma_i32_16x16x64_i8 v[6:9], v[146:149], v[186:189], v[6:9]
	v_mfma_i32_16x16x64_i8 v[2:5], v[150:153], v[186:189], v[2:5]
	v_mfma_i32_16x16x64_i8 v[54:57], v[154:157], v[166:169], v[54:57]
	v_mfma_i32_16x16x64_i8 v[50:53], v[158:161], v[166:169], v[50:53]
	v_mfma_i32_16x16x64_i8 v[38:41], v[154:157], v[174:177], v[38:41]
	v_mfma_i32_16x16x64_i8 v[34:37], v[158:161], v[174:177], v[34:37]
	v_mfma_i32_16x16x64_i8 v[22:25], v[154:157], v[182:185], v[22:25]
	v_mfma_i32_16x16x64_i8 v[18:21], v[158:161], v[182:185], v[18:21]
	v_mfma_i32_16x16x64_i8 v[6:9], v[154:157], v[190:193], v[6:9]
	v_mfma_i32_16x16x64_i8 v[2:5], v[158:161], v[190:193], v[2:5]
	s_barrier
	s_add_u32 s69, s69, 0x10000
	s_addc_u32 s70, s70, 0
	s_add_u32 s34, s34, 0x100
	s_addc_u32 s35, s35, 0
	s_cmp_gt_u32 s68, 13
	s_mov_b32 s68, s42
	s_cbranch_scc1 .LBB0_2510

.LBB0_2506:
	s_add_u32 s36, s0, s34
	s_addc_u32 s37, s1, s35
	s_add_u32 s36, s36, 0x100
	s_addc_u32 s37, s37, 0
	s_waitcnt lgkmcnt(0)
	s_cmpk_eq_i32 s34, 0x700
	s_cselect_b32 s39, s2, s37
	s_cselect_b32 s38, s21, s36
	s_cselect_b32 s37, s19, s70
	s_cselect_b32 s36, s66, s69
	s_barrier
	s_waitcnt lgkmcnt(0)
	v_mfma_i32_16x16x64_i8 v[134:137], v[146:149], v[186:189], v[134:137]
	v_mfma_i32_16x16x64_i8 v[130:133], v[150:153], v[186:189], v[130:133]
	v_mfma_i32_16x16x64_i8 v[110:113], v[146:149], v[178:181], v[110:113]
	v_mfma_i32_16x16x64_i8 v[106:109], v[150:153], v[178:181], v[106:109]
	v_mfma_i32_16x16x64_i8 v[94:97], v[146:149], v[170:173], v[94:97]
	v_mfma_i32_16x16x64_i8 v[90:93], v[150:153], v[170:173], v[90:93]
	v_mfma_i32_16x16x64_i8 v[78:81], v[146:149], v[162:165], v[78:81]
	v_mfma_i32_16x16x64_i8 v[74:77], v[150:153], v[162:165], v[74:77]
	v_mfma_i32_16x16x64_i8 v[134:137], v[158:161], v[190:193], v[134:137]
	v_mfma_i32_16x16x64_i8 v[130:133], v[154:157], v[190:193], v[130:133]
	v_mfma_i32_16x16x64_i8 v[110:113], v[158:161], v[182:185], v[110:113]
	v_mfma_i32_16x16x64_i8 v[106:109], v[154:157], v[182:185], v[106:109]
	v_mfma_i32_16x16x64_i8 v[94:97], v[158:161], v[174:177], v[94:97]
	v_mfma_i32_16x16x64_i8 v[90:93], v[154:157], v[174:177], v[90:93]
	v_mfma_i32_16x16x64_i8 v[78:81], v[158:161], v[166:169], v[78:81]
	v_mfma_i32_16x16x64_i8 v[74:77], v[154:157], v[166:169], v[74:77]
	v_mfma_i32_16x16x64_i8 v[118:121], v[122:125], v[186:189], v[118:121]
	v_mfma_i32_16x16x64_i8 v[114:117], v[126:129], v[186:189], v[114:117]
	v_mfma_i32_16x16x64_i8 v[102:105], v[122:125], v[178:181], v[102:105]
	v_mfma_i32_16x16x64_i8 v[98:101], v[126:129], v[178:181], v[98:101]
	v_mfma_i32_16x16x64_i8 v[86:89], v[122:125], v[170:173], v[86:89]
	v_mfma_i32_16x16x64_i8 v[82:85], v[126:129], v[170:173], v[82:85]
	v_mfma_i32_16x16x64_i8 v[70:73], v[122:125], v[162:165], v[70:73]
	v_mfma_i32_16x16x64_i8 v[66:69], v[126:129], v[162:165], v[66:69]
	v_mfma_i32_16x16x64_i8 v[118:121], v[142:145], v[190:193], v[118:121]
	v_mfma_i32_16x16x64_i8 v[114:117], v[138:141], v[190:193], v[114:117]
	v_mfma_i32_16x16x64_i8 v[102:105], v[142:145], v[182:185], v[102:105]
	v_mfma_i32_16x16x64_i8 v[98:101], v[138:141], v[182:185], v[98:101]
	v_mfma_i32_16x16x64_i8 v[86:89], v[142:145], v[174:177], v[86:89]
	v_mfma_i32_16x16x64_i8 v[82:85], v[138:141], v[174:177], v[82:85]
	v_mfma_i32_16x16x64_i8 v[70:73], v[142:145], v[166:169], v[70:73]
	v_mfma_i32_16x16x64_i8 v[66:69], v[138:141], v[166:169], v[66:69]
	s_barrier
	s_mov_b32 m0, s31
	v_lshl_add_u64 v[214:215], s[36:37], 0, v[196:197]
	s_add_u32 s42, s36, 0x1000
	ds_read_b128 v[186:189], v233 offset:16384
	ds_read_b128 v[190:193], v233 offset:17408
	ds_read_b128 v[178:181], v233 offset:18432
	ds_read_b128 v[182:185], v233 offset:19456
	ds_read_b128 v[170:173], v233 offset:20480
	ds_read_b128 v[174:177], v233 offset:21504
	ds_read_b128 v[162:165], v233 offset:22528
	ds_read_b128 v[166:169], v233 offset:23552
	global_load_lds_dwordx4 v[214:215], off
	v_lshl_add_u64 v[214:215], s[36:37], 0, v[200:201]
	s_mov_b32 m0, s47
	s_addc_u32 s43, s37, 0
	global_load_lds_dwordx4 v[214:215], off
	v_lshl_add_u64 v[214:215], s[42:43], 0, v[196:197]
	s_mov_b32 m0, s49
	v_lshl_add_u64 v[216:217], s[38:39], 0, v[198:199]
	global_load_lds_dwordx4 v[214:215], off
	v_lshl_add_u64 v[214:215], s[42:43], 0, v[200:201]
	s_mov_b32 m0, s50
	s_mov_b64 s[42:43], -1
	global_load_lds_dwordx4 v[214:215], off
	v_lshl_add_u64 v[214:215], s[38:39], 0, v[194:195]
	s_mov_b32 m0, s29
	s_and_b64 vcc, exec, s[40:41]
	global_load_lds_dwordx4 v[214:215], off
	s_mov_b32 m0, s51
	s_nop 0
	global_load_lds_dwordx4 v[216:217], off
	s_cbranch_vccz .LBB0_2508
	s_waitcnt vmcnt(8)
	s_mov_b64 s[42:43], 0

.LBB0_3526:
	s_waitcnt lgkmcnt(0)
	s_add_i32 s40, s67, 2
	s_add_u32 s38, s34, 0x8000
	s_addc_u32 s39, s35, 0
	s_barrier
	s_waitcnt lgkmcnt(0)
	v_mfma_scale_f32_16x16x128_f8f6f4 v[126:129], v[26:33], v[58:65], v[126:129], v230, v230 op_sel_hi:[0,0,0]
	v_mfma_scale_f32_16x16x128_f8f6f4 v[122:125], v[18:25], v[58:65], v[122:125], v230, v230 op_sel_hi:[0,0,0]
	v_mfma_scale_f32_16x16x128_f8f6f4 v[110:113], v[26:33], v[50:57], v[110:113], v230, v230 op_sel_hi:[0,0,0]
	v_mfma_scale_f32_16x16x128_f8f6f4 v[106:109], v[18:25], v[50:57], v[106:109], v230, v230 op_sel_hi:[0,0,0]
	v_mfma_scale_f32_16x16x128_f8f6f4 v[94:97], v[26:33], v[42:49], v[94:97], v230, v230 op_sel_hi:[0,0,0]
	v_mfma_scale_f32_16x16x128_f8f6f4 v[90:93], v[18:25], v[42:49], v[90:93], v230, v230 op_sel_hi:[0,0,0]
	v_mfma_scale_f32_16x16x128_f8f6f4 v[78:81], v[26:33], v[34:41], v[78:81], v230, v230 op_sel_hi:[0,0,0]
	v_mfma_scale_f32_16x16x128_f8f6f4 v[74:77], v[18:25], v[34:41], v[74:77], v230, v230 op_sel_hi:[0,0,0]
	v_mfma_scale_f32_16x16x128_f8f6f4 v[118:121], v[10:17], v[58:65], v[118:121], v230, v230 op_sel_hi:[0,0,0]
	v_mfma_scale_f32_16x16x128_f8f6f4 v[114:117], v[2:9], v[58:65], v[114:117], v230, v230 op_sel_hi:[0,0,0]
	v_mfma_scale_f32_16x16x128_f8f6f4 v[102:105], v[10:17], v[50:57], v[102:105], v230, v230 op_sel_hi:[0,0,0]
	v_mfma_scale_f32_16x16x128_f8f6f4 v[98:101], v[2:9], v[50:57], v[98:101], v230, v230 op_sel_hi:[0,0,0]
	v_mfma_scale_f32_16x16x128_f8f6f4 v[86:89], v[10:17], v[42:49], v[86:89], v230, v230 op_sel_hi:[0,0,0]
	v_mfma_scale_f32_16x16x128_f8f6f4 v[82:85], v[2:9], v[42:49], v[82:85], v230, v230 op_sel_hi:[0,0,0]
	v_mfma_scale_f32_16x16x128_f8f6f4 v[70:73], v[10:17], v[34:41], v[70:73], v230, v230 op_sel_hi:[0,0,0]
	v_mfma_scale_f32_16x16x128_f8f6f4 v[66:69], v[2:9], v[34:41], v[66:69], v230, v230 op_sel_hi:[0,0,0]
	s_barrier
	s_add_i32 s41, 0, 0x18000
	s_add_i32 s70, 0, 0x1c000
	v_add_u32_e32 v6, s41, v218
	v_add_u32_e32 v14, s41, v219
	v_add_u32_e32 v22, s70, v218
	v_add_u32_e32 v30, s70, v219
	ds_read_b128 v[2:5], v6
	ds_read_b128 v[10:13], v6 offset:2048
	ds_read_b128 v[6:9], v14
	ds_read_b128 v[14:17], v14 offset:2048
	ds_read_b128 v[18:21], v22
	ds_read_b128 v[26:29], v22 offset:2048
	ds_read_b128 v[22:25], v30
	ds_read_b128 v[30:33], v30 offset:2048
	s_add_u32 s36, s36, 0x40000
	s_addc_u32 s37, s37, 0
	s_mov_b32 m0, s51
	v_lshl_add_u64 v[232:233], s[36:37], 0, v[194:195]
	ds_read_b128 v[34:37], v228 offset:32768
	ds_read_b128 v[42:45], v228 offset:34816
	ds_read_b128 v[38:41], v229 offset:32768
	ds_read_b128 v[46:49], v229 offset:34816
	ds_read_b128 v[50:53], v228 offset:36864
	ds_read_b128 v[58:61], v228 offset:38912
	ds_read_b128 v[54:57], v229 offset:36864
	ds_read_b128 v[62:65], v229 offset:38912
	global_load_lds_dwordx4 v[232:233], off
	v_lshl_add_u64 v[232:233], s[36:37], 0, v[198:199]
	s_mov_b32 m0, s52
	s_nop 0
	global_load_lds_dwordx4 v[232:233], off
	s_waitcnt vmcnt(8)
	s_waitcnt lgkmcnt(0)
	s_barrier
	s_waitcnt lgkmcnt(0)
	v_mfma_scale_f32_16x16x128_f8f6f4 v[190:193], v[2:9], v[34:41], v[190:193], v230, v230 op_sel_hi:[0,0,0]
	v_mfma_scale_f32_16x16x128_f8f6f4 v[186:189], v[10:17], v[34:41], v[186:189], v230, v230 op_sel_hi:[0,0,0]
	v_mfma_scale_f32_16x16x128_f8f6f4 v[174:177], v[2:9], v[42:49], v[174:177], v230, v230 op_sel_hi:[0,0,0]
	v_mfma_scale_f32_16x16x128_f8f6f4 v[170:173], v[10:17], v[42:49], v[170:173], v230, v230 op_sel_hi:[0,0,0]
	v_mfma_scale_f32_16x16x128_f8f6f4 v[158:161], v[2:9], v[50:57], v[158:161], v230, v230 op_sel_hi:[0,0,0]
	v_mfma_scale_f32_16x16x128_f8f6f4 v[154:157], v[10:17], v[50:57], v[154:157], v230, v230 op_sel_hi:[0,0,0]
	v_mfma_scale_f32_16x16x128_f8f6f4 v[142:145], v[2:9], v[58:65], v[142:145], v230, v230 op_sel_hi:[0,0,0]
	v_mfma_scale_f32_16x16x128_f8f6f4 v[138:141], v[10:17], v[58:65], v[138:141], v230, v230 op_sel_hi:[0,0,0]
	v_mfma_scale_f32_16x16x128_f8f6f4 v[182:185], v[18:25], v[34:41], v[182:185], v230, v230 op_sel_hi:[0,0,0]
	v_mfma_scale_f32_16x16x128_f8f6f4 v[178:181], v[26:33], v[34:41], v[178:181], v230, v230 op_sel_hi:[0,0,0]
	v_mfma_scale_f32_16x16x128_f8f6f4 v[166:169], v[18:25], v[42:49], v[166:169], v230, v230 op_sel_hi:[0,0,0]
	v_mfma_scale_f32_16x16x128_f8f6f4 v[162:165], v[26:33], v[42:49], v[162:165], v230, v230 op_sel_hi:[0,0,0]
	v_mfma_scale_f32_16x16x128_f8f6f4 v[150:153], v[18:25], v[50:57], v[150:153], v230, v230 op_sel_hi:[0,0,0]
	v_mfma_scale_f32_16x16x128_f8f6f4 v[146:149], v[26:33], v[50:57], v[146:149], v230, v230 op_sel_hi:[0,0,0]
	v_mfma_scale_f32_16x16x128_f8f6f4 v[134:137], v[18:25], v[58:65], v[134:137], v230, v230 op_sel_hi:[0,0,0]
	v_mfma_scale_f32_16x16x128_f8f6f4 v[130:133], v[26:33], v[58:65], v[130:133], v230, v230 op_sel_hi:[0,0,0]
	s_barrier
	s_add_i32 s36, s41, s45
	v_lshl_add_u64 v[232:233], s[38:39], 0, v[196:197]
	s_mov_b32 m0, s36
	ds_read_b128 v[34:37], v228 offset:49152
	ds_read_b128 v[42:45], v228 offset:51200
	ds_read_b128 v[38:41], v229 offset:49152
	ds_read_b128 v[46:49], v229 offset:51200
	ds_read_b128 v[50:53], v228 offset:53248
	ds_read_b128 v[58:61], v228 offset:55296
	ds_read_b128 v[54:57], v229 offset:53248
	ds_read_b128 v[62:65], v229 offset:55296
	global_load_lds_dwordx4 v[232:233], off
	s_add_i32 m0, s36, 0x2000
	s_add_u32 s34, s34, 0x9000
	v_lshl_add_u64 v[232:233], s[38:39], 0, v[200:201]
	s_addc_u32 s35, s35, 0
	s_add_i32 s36, s70, s45
	global_load_lds_dwordx4 v[232:233], off
	v_lshl_add_u64 v[232:233], s[34:35], 0, v[196:197]
	s_mov_b32 m0, s36
	v_lshl_add_u64 v[214:215], v[214:215], 0, s[4:5]
	global_load_lds_dwordx4 v[232:233], off
	v_lshl_add_u64 v[232:233], s[34:35], 0, v[200:201]
	s_add_i32 m0, s36, 0x2000
	s_nop 0
	global_load_lds_dwordx4 v[232:233], off
	s_mov_b32 m0, s55
	s_nop 0
	global_load_lds_dwordx4 v[214:215], off
	v_lshl_add_u64 v[214:215], v[216:217], 0, s[4:5]
	s_mov_b32 m0, s56
	s_nop 0
	global_load_lds_dwordx4 v[214:215], off
	s_waitcnt vmcnt(8)
	s_waitcnt lgkmcnt(0)
	s_barrier
	s_waitcnt lgkmcnt(0)
	v_mfma_scale_f32_16x16x128_f8f6f4 v[126:129], v[2:9], v[34:41], v[126:129], v230, v230 op_sel_hi:[0,0,0]
	v_mfma_scale_f32_16x16x128_f8f6f4 v[122:125], v[10:17], v[34:41], v[122:125], v230, v230 op_sel_hi:[0,0,0]
	v_mfma_scale_f32_16x16x128_f8f6f4 v[110:113], v[2:9], v[42:49], v[110:113], v230, v230 op_sel_hi:[0,0,0]
	v_mfma_scale_f32_16x16x128_f8f6f4 v[106:109], v[10:17], v[42:49], v[106:109], v230, v230 op_sel_hi:[0,0,0]
	v_mfma_scale_f32_16x16x128_f8f6f4 v[94:97], v[2:9], v[50:57], v[94:97], v230, v230 op_sel_hi:[0,0,0]
	v_mfma_scale_f32_16x16x128_f8f6f4 v[90:93], v[10:17], v[50:57], v[90:93], v230, v230 op_sel_hi:[0,0,0]
	v_mfma_scale_f32_16x16x128_f8f6f4 v[78:81], v[2:9], v[58:65], v[78:81], v230, v230 op_sel_hi:[0,0,0]
	v_mfma_scale_f32_16x16x128_f8f6f4 v[74:77], v[10:17], v[58:65], v[74:77], v230, v230 op_sel_hi:[0,0,0]
	v_mfma_scale_f32_16x16x128_f8f6f4 v[118:121], v[18:25], v[34:41], v[118:121], v230, v230 op_sel_hi:[0,0,0]
	v_mfma_scale_f32_16x16x128_f8f6f4 v[114:117], v[26:33], v[34:41], v[114:117], v230, v230 op_sel_hi:[0,0,0]
	v_mfma_scale_f32_16x16x128_f8f6f4 v[102:105], v[18:25], v[42:49], v[102:105], v230, v230 op_sel_hi:[0,0,0]
	v_mfma_scale_f32_16x16x128_f8f6f4 v[98:101], v[26:33], v[42:49], v[98:101], v230, v230 op_sel_hi:[0,0,0]
	v_mfma_scale_f32_16x16x128_f8f6f4 v[86:89], v[18:25], v[50:57], v[86:89], v230, v230 op_sel_hi:[0,0,0]
	v_mfma_scale_f32_16x16x128_f8f6f4 v[82:85], v[26:33], v[50:57], v[82:85], v230, v230 op_sel_hi:[0,0,0]
	v_mfma_scale_f32_16x16x128_f8f6f4 v[70:73], v[18:25], v[58:65], v[70:73], v230, v230 op_sel_hi:[0,0,0]
	v_mfma_scale_f32_16x16x128_f8f6f4 v[66:69], v[26:33], v[58:65], v[66:69], v230, v230 op_sel_hi:[0,0,0]
	s_barrier
	s_add_u32 s68, s68, 0x10000
	s_addc_u32 s69, s69, 0
	s_add_u32 s30, s30, 0x100
	s_addc_u32 s31, s31, 0
	s_cmp_gt_u32 s67, 13
	s_mov_b32 s67, s40
	s_cbranch_scc1 .LBB0_3535

.LBB0_3531:
	s_add_u32 s34, s28, s30
	s_addc_u32 s35, s29, s31
	s_add_u32 s34, s34, 0x100
	s_addc_u32 s35, s35, 0
	s_waitcnt lgkmcnt(0)
	s_cmpk_eq_i32 s30, 0x700
	s_cselect_b32 s37, s21, s35
	s_cselect_b32 s36, s64, s34
	s_cselect_b32 s35, s19, s69
	s_cselect_b32 s34, s65, s68
	s_barrier
	s_waitcnt lgkmcnt(0)
	v_mfma_scale_f32_16x16x128_f8f6f4 v[190:193], v[26:33], v[58:65], v[190:193], v230, v230 op_sel_hi:[0,0,0]
	v_mfma_scale_f32_16x16x128_f8f6f4 v[186:189], v[18:25], v[58:65], v[186:189], v230, v230 op_sel_hi:[0,0,0]
	v_mfma_scale_f32_16x16x128_f8f6f4 v[174:177], v[26:33], v[50:57], v[174:177], v230, v230 op_sel_hi:[0,0,0]
	v_mfma_scale_f32_16x16x128_f8f6f4 v[170:173], v[18:25], v[50:57], v[170:173], v230, v230 op_sel_hi:[0,0,0]
	v_mfma_scale_f32_16x16x128_f8f6f4 v[158:161], v[26:33], v[42:49], v[158:161], v230, v230 op_sel_hi:[0,0,0]
	v_mfma_scale_f32_16x16x128_f8f6f4 v[154:157], v[18:25], v[42:49], v[154:157], v230, v230 op_sel_hi:[0,0,0]
	v_mfma_scale_f32_16x16x128_f8f6f4 v[142:145], v[26:33], v[34:41], v[142:145], v230, v230 op_sel_hi:[0,0,0]
	v_mfma_scale_f32_16x16x128_f8f6f4 v[138:141], v[18:25], v[34:41], v[138:141], v230, v230 op_sel_hi:[0,0,0]
	v_mfma_scale_f32_16x16x128_f8f6f4 v[182:185], v[10:17], v[58:65], v[182:185], v230, v230 op_sel_hi:[0,0,0]
	v_mfma_scale_f32_16x16x128_f8f6f4 v[178:181], v[2:9], v[58:65], v[178:181], v230, v230 op_sel_hi:[0,0,0]
	v_mfma_scale_f32_16x16x128_f8f6f4 v[166:169], v[10:17], v[50:57], v[166:169], v230, v230 op_sel_hi:[0,0,0]
	v_mfma_scale_f32_16x16x128_f8f6f4 v[162:165], v[2:9], v[50:57], v[162:165], v230, v230 op_sel_hi:[0,0,0]
	v_mfma_scale_f32_16x16x128_f8f6f4 v[150:153], v[10:17], v[42:49], v[150:153], v230, v230 op_sel_hi:[0,0,0]
	v_mfma_scale_f32_16x16x128_f8f6f4 v[146:149], v[2:9], v[42:49], v[146:149], v230, v230 op_sel_hi:[0,0,0]
	v_mfma_scale_f32_16x16x128_f8f6f4 v[134:137], v[10:17], v[34:41], v[134:137], v230, v230 op_sel_hi:[0,0,0]
	v_mfma_scale_f32_16x16x128_f8f6f4 v[130:133], v[2:9], v[34:41], v[130:133], v230, v230 op_sel_hi:[0,0,0]
	s_barrier
	s_mov_b32 m0, s46
	v_lshl_add_u64 v[214:215], s[34:35], 0, v[196:197]
	s_add_u32 s40, s34, 0x1000
	ds_read_b128 v[58:61], v228 offset:16384
	ds_read_b128 v[50:53], v228 offset:18432
	ds_read_b128 v[62:65], v229 offset:16384
	ds_read_b128 v[54:57], v229 offset:18432
	ds_read_b128 v[42:45], v228 offset:20480
	ds_read_b128 v[34:37], v228 offset:22528
	ds_read_b128 v[46:49], v229 offset:20480
	ds_read_b128 v[38:41], v229 offset:22528
	global_load_lds_dwordx4 v[214:215], off
	v_lshl_add_u64 v[214:215], s[34:35], 0, v[200:201]
	s_mov_b32 m0, s47
	s_addc_u32 s41, s35, 0
	global_load_lds_dwordx4 v[214:215], off
	v_lshl_add_u64 v[214:215], s[40:41], 0, v[196:197]
	s_mov_b32 m0, s48
	v_lshl_add_u64 v[216:217], s[36:37], 0, v[198:199]
	global_load_lds_dwordx4 v[214:215], off
	v_lshl_add_u64 v[214:215], s[40:41], 0, v[200:201]
	s_mov_b32 m0, s49
	s_mov_b64 s[40:41], -1
	global_load_lds_dwordx4 v[214:215], off
	v_lshl_add_u64 v[214:215], s[36:37], 0, v[194:195]
	s_mov_b32 m0, s27
	s_and_b64 vcc, exec, s[38:39]
	global_load_lds_dwordx4 v[214:215], off
	s_mov_b32 m0, s50
	s_nop 0
	global_load_lds_dwordx4 v[216:217], off
	s_cbranch_vccz .LBB0_3533
	s_waitcnt vmcnt(8)
	s_mov_b64 s[40:41], 0

.LBB0_3830:
	s_waitcnt lgkmcnt(0)
	s_add_i32 s36, s68, 2
	s_add_u32 s34, s28, 0x8000
	s_addc_u32 s35, s29, 0
	s_barrier
	s_waitcnt lgkmcnt(0)
	v_mfma_i32_16x16x64_i8 v[62:65], v[146:149], v[186:189], v[62:65]
	v_mfma_i32_16x16x64_i8 v[58:61], v[150:153], v[186:189], v[58:61]
	v_mfma_i32_16x16x64_i8 v[46:49], v[146:149], v[178:181], v[46:49]
	v_mfma_i32_16x16x64_i8 v[42:45], v[150:153], v[178:181], v[42:45]
	v_mfma_i32_16x16x64_i8 v[30:33], v[146:149], v[170:173], v[30:33]
	v_mfma_i32_16x16x64_i8 v[26:29], v[150:153], v[170:173], v[26:29]
	v_mfma_i32_16x16x64_i8 v[14:17], v[146:149], v[162:165], v[14:17]
	v_mfma_i32_16x16x64_i8 v[10:13], v[150:153], v[162:165], v[10:13]
	v_mfma_i32_16x16x64_i8 v[62:65], v[158:161], v[190:193], v[62:65]
	v_mfma_i32_16x16x64_i8 v[58:61], v[154:157], v[190:193], v[58:61]
	v_mfma_i32_16x16x64_i8 v[46:49], v[158:161], v[182:185], v[46:49]
	v_mfma_i32_16x16x64_i8 v[42:45], v[154:157], v[182:185], v[42:45]
	v_mfma_i32_16x16x64_i8 v[30:33], v[158:161], v[174:177], v[30:33]
	v_mfma_i32_16x16x64_i8 v[26:29], v[154:157], v[174:177], v[26:29]
	v_mfma_i32_16x16x64_i8 v[14:17], v[158:161], v[166:169], v[14:17]
	v_mfma_i32_16x16x64_i8 v[10:13], v[154:157], v[166:169], v[10:13]
	v_mfma_i32_16x16x64_i8 v[54:57], v[130:133], v[186:189], v[54:57]
	v_mfma_i32_16x16x64_i8 v[50:53], v[134:137], v[186:189], v[50:53]
	v_mfma_i32_16x16x64_i8 v[38:41], v[130:133], v[178:181], v[38:41]
	v_mfma_i32_16x16x64_i8 v[34:37], v[134:137], v[178:181], v[34:37]
	v_mfma_i32_16x16x64_i8 v[22:25], v[130:133], v[170:173], v[22:25]
	v_mfma_i32_16x16x64_i8 v[18:21], v[134:137], v[170:173], v[18:21]
	v_mfma_i32_16x16x64_i8 v[6:9], v[130:133], v[162:165], v[6:9]
	v_mfma_i32_16x16x64_i8 v[2:5], v[134:137], v[162:165], v[2:5]
	v_mfma_i32_16x16x64_i8 v[54:57], v[142:145], v[190:193], v[54:57]
	v_mfma_i32_16x16x64_i8 v[50:53], v[138:141], v[190:193], v[50:53]
	v_mfma_i32_16x16x64_i8 v[38:41], v[142:145], v[182:185], v[38:41]
	v_mfma_i32_16x16x64_i8 v[34:37], v[138:141], v[182:185], v[34:37]
	v_mfma_i32_16x16x64_i8 v[22:25], v[142:145], v[174:177], v[22:25]
	v_mfma_i32_16x16x64_i8 v[18:21], v[138:141], v[174:177], v[18:21]
	v_mfma_i32_16x16x64_i8 v[6:9], v[142:145], v[166:169], v[6:9]
	v_mfma_i32_16x16x64_i8 v[2:5], v[138:141], v[166:169], v[2:5]
	s_barrier
	s_add_i32 s37, 0, 0x18000
	s_add_i32 s71, 0, 0x1c000
	v_add_u32_e32 v134, s37, v229
	v_add_u32_e32 v142, s37, v231
	v_add_u32_e32 v150, s71, v229
	v_add_u32_e32 v158, s71, v231
	ds_read_b128 v[130:133], v134
	ds_read_b128 v[134:137], v134 offset:2048
	ds_read_b128 v[138:141], v142
	ds_read_b128 v[142:145], v142 offset:2048
	ds_read_b128 v[146:149], v150
	ds_read_b128 v[150:153], v150 offset:2048
	ds_read_b128 v[154:157], v158
	ds_read_b128 v[158:161], v158 offset:2048
	s_add_u32 s30, s30, 0x40000
	s_addc_u32 s31, s31, 0
	s_mov_b32 m0, s53
	v_lshl_add_u64 v[246:247], s[30:31], 0, v[202:203]
	ds_read_b128 v[162:165], v233 offset:32768
	ds_read_b128 v[166:169], v233 offset:33792
	ds_read_b128 v[170:173], v233 offset:34816
	ds_read_b128 v[174:177], v233 offset:35840
	ds_read_b128 v[178:181], v233 offset:36864
	ds_read_b128 v[182:185], v233 offset:37888
	ds_read_b128 v[186:189], v233 offset:38912
	ds_read_b128 v[190:193], v233 offset:39936
	global_load_lds_dwordx4 v[246:247], off
	v_lshl_add_u64 v[246:247], s[30:31], 0, v[198:199]
	s_mov_b32 m0, s54
	s_nop 0
	global_load_lds_dwordx4 v[246:247], off
	s_waitcnt vmcnt(8)
	s_waitcnt lgkmcnt(0)
	s_barrier
	s_waitcnt lgkmcnt(0)
	v_mfma_i32_16x16x64_i8 v[126:129], v[130:133], v[162:165], v[126:129]
	v_mfma_i32_16x16x64_i8 v[122:125], v[134:137], v[162:165], v[122:125]
	v_mfma_i32_16x16x64_i8 v[110:113], v[130:133], v[170:173], v[110:113]
	v_mfma_i32_16x16x64_i8 v[106:109], v[134:137], v[170:173], v[106:109]
	v_mfma_i32_16x16x64_i8 v[94:97], v[130:133], v[178:181], v[94:97]
	v_mfma_i32_16x16x64_i8 v[90:93], v[134:137], v[178:181], v[90:93]
	v_mfma_i32_16x16x64_i8 v[78:81], v[130:133], v[186:189], v[78:81]
	v_mfma_i32_16x16x64_i8 v[74:77], v[134:137], v[186:189], v[74:77]
	v_mfma_i32_16x16x64_i8 v[126:129], v[138:141], v[166:169], v[126:129]
	v_mfma_i32_16x16x64_i8 v[122:125], v[142:145], v[166:169], v[122:125]
	v_mfma_i32_16x16x64_i8 v[110:113], v[138:141], v[174:177], v[110:113]
	v_mfma_i32_16x16x64_i8 v[106:109], v[142:145], v[174:177], v[106:109]
	v_mfma_i32_16x16x64_i8 v[94:97], v[138:141], v[182:185], v[94:97]
	v_mfma_i32_16x16x64_i8 v[90:93], v[142:145], v[182:185], v[90:93]
	v_mfma_i32_16x16x64_i8 v[78:81], v[138:141], v[190:193], v[78:81]
	v_mfma_i32_16x16x64_i8 v[74:77], v[142:145], v[190:193], v[74:77]
	v_mfma_i32_16x16x64_i8 v[118:121], v[146:149], v[162:165], v[118:121]
	v_mfma_i32_16x16x64_i8 v[114:117], v[150:153], v[162:165], v[114:117]
	v_mfma_i32_16x16x64_i8 v[102:105], v[146:149], v[170:173], v[102:105]
	v_mfma_i32_16x16x64_i8 v[98:101], v[150:153], v[170:173], v[98:101]
	v_mfma_i32_16x16x64_i8 v[86:89], v[146:149], v[178:181], v[86:89]
	v_mfma_i32_16x16x64_i8 v[82:85], v[150:153], v[178:181], v[82:85]
	v_mfma_i32_16x16x64_i8 v[70:73], v[146:149], v[186:189], v[70:73]
	v_mfma_i32_16x16x64_i8 v[66:69], v[150:153], v[186:189], v[66:69]
	v_mfma_i32_16x16x64_i8 v[118:121], v[154:157], v[166:169], v[118:121]
	v_mfma_i32_16x16x64_i8 v[114:117], v[158:161], v[166:169], v[114:117]
	v_mfma_i32_16x16x64_i8 v[102:105], v[154:157], v[174:177], v[102:105]
	v_mfma_i32_16x16x64_i8 v[98:101], v[158:161], v[174:177], v[98:101]
	v_mfma_i32_16x16x64_i8 v[86:89], v[154:157], v[182:185], v[86:89]
	v_mfma_i32_16x16x64_i8 v[82:85], v[158:161], v[182:185], v[82:85]
	v_mfma_i32_16x16x64_i8 v[70:73], v[154:157], v[190:193], v[70:73]
	v_mfma_i32_16x16x64_i8 v[66:69], v[158:161], v[190:193], v[66:69]
	s_barrier
	s_add_i32 s30, s37, s43
	v_lshl_add_u64 v[246:247], s[34:35], 0, v[200:201]
	s_mov_b32 m0, s30
	ds_read_b128 v[162:165], v233 offset:49152
	ds_read_b128 v[166:169], v233 offset:50176
	ds_read_b128 v[170:173], v233 offset:51200
	ds_read_b128 v[174:177], v233 offset:52224
	ds_read_b128 v[178:181], v233 offset:53248
	ds_read_b128 v[182:185], v233 offset:54272
	ds_read_b128 v[186:189], v233 offset:55296
	ds_read_b128 v[190:193], v233 offset:56320
	global_load_lds_dwordx4 v[246:247], off
	s_add_i32 m0, s30, 0x2000
	s_add_u32 s28, s28, 0x9000
	v_lshl_add_u64 v[246:247], s[34:35], 0, v[196:197]
	s_addc_u32 s29, s29, 0
	s_add_i32 s30, s71, s43
	global_load_lds_dwordx4 v[246:247], off
	v_lshl_add_u64 v[246:247], s[28:29], 0, v[200:201]
	s_mov_b32 m0, s30
	v_lshl_add_u64 v[242:243], v[242:243], 0, s[10:11]
	global_load_lds_dwordx4 v[246:247], off
	v_lshl_add_u64 v[246:247], s[28:29], 0, v[196:197]
	s_add_i32 m0, s30, 0x2000
	s_nop 0
	global_load_lds_dwordx4 v[246:247], off
	s_mov_b32 m0, s58
	s_nop 0
	global_load_lds_dwordx4 v[242:243], off
	v_lshl_add_u64 v[242:243], v[244:245], 0, s[10:11]
	s_mov_b32 m0, s59
	s_nop 0
	global_load_lds_dwordx4 v[242:243], off
	s_waitcnt vmcnt(8)
	s_waitcnt lgkmcnt(0)
	s_barrier
	s_waitcnt lgkmcnt(0)
	v_mfma_i32_16x16x64_i8 v[62:65], v[130:133], v[162:165], v[62:65]
	v_mfma_i32_16x16x64_i8 v[58:61], v[134:137], v[162:165], v[58:61]
	v_mfma_i32_16x16x64_i8 v[46:49], v[130:133], v[170:173], v[46:49]
	v_mfma_i32_16x16x64_i8 v[42:45], v[134:137], v[170:173], v[42:45]
	v_mfma_i32_16x16x64_i8 v[30:33], v[130:133], v[178:181], v[30:33]
	v_mfma_i32_16x16x64_i8 v[26:29], v[134:137], v[178:181], v[26:29]
	v_mfma_i32_16x16x64_i8 v[14:17], v[130:133], v[186:189], v[14:17]
	v_mfma_i32_16x16x64_i8 v[10:13], v[134:137], v[186:189], v[10:13]
	v_mfma_i32_16x16x64_i8 v[62:65], v[138:141], v[166:169], v[62:65]
	v_mfma_i32_16x16x64_i8 v[58:61], v[142:145], v[166:169], v[58:61]
	v_mfma_i32_16x16x64_i8 v[46:49], v[138:141], v[174:177], v[46:49]
	v_mfma_i32_16x16x64_i8 v[42:45], v[142:145], v[174:177], v[42:45]
	v_mfma_i32_16x16x64_i8 v[30:33], v[138:141], v[182:185], v[30:33]
	v_mfma_i32_16x16x64_i8 v[26:29], v[142:145], v[182:185], v[26:29]
	v_mfma_i32_16x16x64_i8 v[14:17], v[138:141], v[190:193], v[14:17]
	v_mfma_i32_16x16x64_i8 v[10:13], v[142:145], v[190:193], v[10:13]
	v_mfma_i32_16x16x64_i8 v[54:57], v[146:149], v[162:165], v[54:57]
	v_mfma_i32_16x16x64_i8 v[50:53], v[150:153], v[162:165], v[50:53]
	v_mfma_i32_16x16x64_i8 v[38:41], v[146:149], v[170:173], v[38:41]
	v_mfma_i32_16x16x64_i8 v[34:37], v[150:153], v[170:173], v[34:37]
	v_mfma_i32_16x16x64_i8 v[22:25], v[146:149], v[178:181], v[22:25]
	v_mfma_i32_16x16x64_i8 v[18:21], v[150:153], v[178:181], v[18:21]
	v_mfma_i32_16x16x64_i8 v[6:9], v[146:149], v[186:189], v[6:9]
	v_mfma_i32_16x16x64_i8 v[2:5], v[150:153], v[186:189], v[2:5]
	v_mfma_i32_16x16x64_i8 v[54:57], v[154:157], v[166:169], v[54:57]
	v_mfma_i32_16x16x64_i8 v[50:53], v[158:161], v[166:169], v[50:53]
	v_mfma_i32_16x16x64_i8 v[38:41], v[154:157], v[174:177], v[38:41]
	v_mfma_i32_16x16x64_i8 v[34:37], v[158:161], v[174:177], v[34:37]
	v_mfma_i32_16x16x64_i8 v[22:25], v[154:157], v[182:185], v[22:25]
	v_mfma_i32_16x16x64_i8 v[18:21], v[158:161], v[182:185], v[18:21]
	v_mfma_i32_16x16x64_i8 v[6:9], v[154:157], v[190:193], v[6:9]
	v_mfma_i32_16x16x64_i8 v[2:5], v[158:161], v[190:193], v[2:5]
	s_barrier
	s_add_u32 s69, s69, 0x10000
	s_addc_u32 s70, s70, 0
	s_add_u32 s4, s4, 0x100
	s_addc_u32 s5, s5, 0
	s_cmp_gt_u32 s68, 13
	s_mov_b32 s68, s36
	s_cbranch_scc1 .LBB0_3839

.LBB0_3835:
	s_add_u32 s28, s26, s4
	s_addc_u32 s29, s27, s5
	s_add_u32 s28, s28, 0x100
	s_addc_u32 s29, s29, 0
	s_waitcnt lgkmcnt(0)
	s_cmpk_eq_i32 s4, 0x700
	s_cselect_b32 s31, s15, s29
	s_cselect_b32 s30, s17, s28
	s_cselect_b32 s29, s19, s70
	s_cselect_b32 s28, s18, s69
	s_barrier
	s_waitcnt lgkmcnt(0)
	v_mfma_i32_16x16x64_i8 v[126:129], v[146:149], v[186:189], v[126:129]
	v_mfma_i32_16x16x64_i8 v[122:125], v[150:153], v[186:189], v[122:125]
	v_mfma_i32_16x16x64_i8 v[110:113], v[146:149], v[178:181], v[110:113]
	v_mfma_i32_16x16x64_i8 v[106:109], v[150:153], v[178:181], v[106:109]
	v_mfma_i32_16x16x64_i8 v[94:97], v[146:149], v[170:173], v[94:97]
	v_mfma_i32_16x16x64_i8 v[90:93], v[150:153], v[170:173], v[90:93]
	v_mfma_i32_16x16x64_i8 v[78:81], v[146:149], v[162:165], v[78:81]
	v_mfma_i32_16x16x64_i8 v[74:77], v[150:153], v[162:165], v[74:77]
	v_mfma_i32_16x16x64_i8 v[126:129], v[158:161], v[190:193], v[126:129]
	v_mfma_i32_16x16x64_i8 v[122:125], v[154:157], v[190:193], v[122:125]
	v_mfma_i32_16x16x64_i8 v[110:113], v[158:161], v[182:185], v[110:113]
	v_mfma_i32_16x16x64_i8 v[106:109], v[154:157], v[182:185], v[106:109]
	v_mfma_i32_16x16x64_i8 v[94:97], v[158:161], v[174:177], v[94:97]
	v_mfma_i32_16x16x64_i8 v[90:93], v[154:157], v[174:177], v[90:93]
	v_mfma_i32_16x16x64_i8 v[78:81], v[158:161], v[166:169], v[78:81]
	v_mfma_i32_16x16x64_i8 v[74:77], v[154:157], v[166:169], v[74:77]
	v_mfma_i32_16x16x64_i8 v[118:121], v[130:133], v[186:189], v[118:121]
	v_mfma_i32_16x16x64_i8 v[114:117], v[134:137], v[186:189], v[114:117]
	v_mfma_i32_16x16x64_i8 v[102:105], v[130:133], v[178:181], v[102:105]
	v_mfma_i32_16x16x64_i8 v[98:101], v[134:137], v[178:181], v[98:101]
	v_mfma_i32_16x16x64_i8 v[86:89], v[130:133], v[170:173], v[86:89]
	v_mfma_i32_16x16x64_i8 v[82:85], v[134:137], v[170:173], v[82:85]
	v_mfma_i32_16x16x64_i8 v[70:73], v[130:133], v[162:165], v[70:73]
	v_mfma_i32_16x16x64_i8 v[66:69], v[134:137], v[162:165], v[66:69]
	v_mfma_i32_16x16x64_i8 v[118:121], v[142:145], v[190:193], v[118:121]
	v_mfma_i32_16x16x64_i8 v[114:117], v[138:141], v[190:193], v[114:117]
	v_mfma_i32_16x16x64_i8 v[102:105], v[142:145], v[182:185], v[102:105]
	v_mfma_i32_16x16x64_i8 v[98:101], v[138:141], v[182:185], v[98:101]
	v_mfma_i32_16x16x64_i8 v[86:89], v[142:145], v[174:177], v[86:89]
	v_mfma_i32_16x16x64_i8 v[82:85], v[138:141], v[174:177], v[82:85]
	v_mfma_i32_16x16x64_i8 v[70:73], v[142:145], v[166:169], v[70:73]
	v_mfma_i32_16x16x64_i8 v[66:69], v[138:141], v[166:169], v[66:69]
	s_barrier
	s_mov_b32 m0, s25
	v_lshl_add_u64 v[242:243], s[28:29], 0, v[200:201]
	s_add_u32 s36, s28, 0x1000
	ds_read_b128 v[186:189], v233 offset:16384
	ds_read_b128 v[190:193], v233 offset:17408
	ds_read_b128 v[178:181], v233 offset:18432
	ds_read_b128 v[182:185], v233 offset:19456
	ds_read_b128 v[170:173], v233 offset:20480
	ds_read_b128 v[174:177], v233 offset:21504
	ds_read_b128 v[162:165], v233 offset:22528
	ds_read_b128 v[166:169], v233 offset:23552
	global_load_lds_dwordx4 v[242:243], off
	v_lshl_add_u64 v[242:243], s[28:29], 0, v[196:197]
	s_mov_b32 m0, s46
	s_addc_u32 s37, s29, 0
	global_load_lds_dwordx4 v[242:243], off
	v_lshl_add_u64 v[242:243], s[36:37], 0, v[200:201]
	s_mov_b32 m0, s47
	v_lshl_add_u64 v[244:245], s[30:31], 0, v[198:199]
	global_load_lds_dwordx4 v[242:243], off
	v_lshl_add_u64 v[242:243], s[36:37], 0, v[196:197]
	s_mov_b32 m0, s51
	s_mov_b64 s[36:37], -1
	global_load_lds_dwordx4 v[242:243], off
	v_lshl_add_u64 v[242:243], s[30:31], 0, v[202:203]
	s_mov_b32 m0, s23
	s_and_b64 vcc, exec, s[34:35]
	global_load_lds_dwordx4 v[242:243], off
	s_mov_b32 m0, s52
	s_nop 0
	global_load_lds_dwordx4 v[244:245], off
	s_cbranch_vccz .LBB0_3837
	s_waitcnt vmcnt(8)
	s_mov_b64 s[36:37], 0

.LBB0_3925:
	s_add_i32 s75, s72, 2
	s_add_u32 s36, s34, 0x8000
	s_waitcnt lgkmcnt(0)
	s_addc_u32 s37, s35, 0
	s_add_u32 s38, s30, 0x8000
	s_addc_u32 s39, s31, 0
	s_barrier
	s_waitcnt lgkmcnt(0)
	v_mfma_scale_f32_16x16x128_f8f6f4 v[126:129], v[26:33], v[58:65], v[126:129], v232, v232 op_sel_hi:[0,0,0]
	v_mfma_scale_f32_16x16x128_f8f6f4 v[122:125], v[18:25], v[58:65], v[122:125], v232, v232 op_sel_hi:[0,0,0]
	v_mfma_scale_f32_16x16x128_f8f6f4 v[114:117], v[26:33], v[50:57], v[114:117], v232, v232 op_sel_hi:[0,0,0]
	v_mfma_scale_f32_16x16x128_f8f6f4 v[106:109], v[18:25], v[50:57], v[106:109], v232, v232 op_sel_hi:[0,0,0]
	v_mfma_scale_f32_16x16x128_f8f6f4 v[98:101], v[26:33], v[42:49], v[98:101], v232, v232 op_sel_hi:[0,0,0]
	v_mfma_scale_f32_16x16x128_f8f6f4 v[90:93], v[18:25], v[42:49], v[90:93], v232, v232 op_sel_hi:[0,0,0]
	v_mfma_scale_f32_16x16x128_f8f6f4 v[82:85], v[26:33], v[34:41], v[82:85], v232, v232 op_sel_hi:[0,0,0]
	v_mfma_scale_f32_16x16x128_f8f6f4 v[74:77], v[18:25], v[34:41], v[74:77], v232, v232 op_sel_hi:[0,0,0]
	v_mfma_scale_f32_16x16x128_f8f6f4 v[118:121], v[10:17], v[58:65], v[118:121], v232, v232 op_sel_hi:[0,0,0]
	v_mfma_scale_f32_16x16x128_f8f6f4 v[110:113], v[2:9], v[58:65], v[110:113], v232, v232 op_sel_hi:[0,0,0]
	v_mfma_scale_f32_16x16x128_f8f6f4 v[102:105], v[10:17], v[50:57], v[102:105], v232, v232 op_sel_hi:[0,0,0]
	v_mfma_scale_f32_16x16x128_f8f6f4 v[94:97], v[2:9], v[50:57], v[94:97], v232, v232 op_sel_hi:[0,0,0]
	v_mfma_scale_f32_16x16x128_f8f6f4 v[86:89], v[10:17], v[42:49], v[86:89], v232, v232 op_sel_hi:[0,0,0]
	v_mfma_scale_f32_16x16x128_f8f6f4 v[78:81], v[2:9], v[42:49], v[78:81], v232, v232 op_sel_hi:[0,0,0]
	v_mfma_scale_f32_16x16x128_f8f6f4 v[70:73], v[10:17], v[34:41], v[70:73], v232, v232 op_sel_hi:[0,0,0]
	v_mfma_scale_f32_16x16x128_f8f6f4 v[66:69], v[2:9], v[34:41], v[66:69], v232, v232 op_sel_hi:[0,0,0]
	s_barrier
	s_add_i32 s76, 0, 0x18000
	s_add_i32 s77, 0, 0x1c000
	v_add_u32_e32 v6, s76, v222
	v_add_u32_e32 v14, s76, v224
	v_add_u32_e32 v22, s77, v222
	v_add_u32_e32 v30, s77, v224
	ds_read_b128 v[2:5], v6
	ds_read_b128 v[10:13], v6 offset:2048
	ds_read_b128 v[6:9], v14
	ds_read_b128 v[14:17], v14 offset:2048
	ds_read_b128 v[18:21], v22
	ds_read_b128 v[26:29], v22 offset:2048
	ds_read_b128 v[22:25], v30
	ds_read_b128 v[30:33], v30 offset:2048
	s_add_u32 s34, s34, 0x1000
	s_addc_u32 s35, s35, 0
	s_mov_b32 m0, s55
	v_lshl_add_u64 v[234:235], s[34:35], 0, v[194:195]
	ds_read_b128 v[34:37], v230 offset:32768
	ds_read_b128 v[42:45], v230 offset:34816
	ds_read_b128 v[38:41], v231 offset:32768
	ds_read_b128 v[46:49], v231 offset:34816
	ds_read_b128 v[50:53], v230 offset:36864
	ds_read_b128 v[58:61], v230 offset:38912
	ds_read_b128 v[54:57], v231 offset:36864
	ds_read_b128 v[62:65], v231 offset:38912
	global_load_lds_dwordx4 v[234:235], off
	v_lshl_add_u64 v[234:235], s[34:35], 0, v[198:199]
	s_mov_b32 m0, s56
	s_nop 0
	global_load_lds_dwordx4 v[234:235], off
	s_waitcnt vmcnt(8)
	s_waitcnt lgkmcnt(0)
	s_barrier
	s_waitcnt lgkmcnt(0)
	v_mfma_scale_f32_16x16x128_f8f6f4 v[190:193], v[2:9], v[34:41], v[190:193], v232, v232 op_sel_hi:[0,0,0]
	v_mfma_scale_f32_16x16x128_f8f6f4 v[186:189], v[10:17], v[34:41], v[186:189], v232, v232 op_sel_hi:[0,0,0]
	v_mfma_scale_f32_16x16x128_f8f6f4 v[178:181], v[2:9], v[42:49], v[178:181], v232, v232 op_sel_hi:[0,0,0]
	v_mfma_scale_f32_16x16x128_f8f6f4 v[170:173], v[10:17], v[42:49], v[170:173], v232, v232 op_sel_hi:[0,0,0]
	v_mfma_scale_f32_16x16x128_f8f6f4 v[162:165], v[2:9], v[50:57], v[162:165], v232, v232 op_sel_hi:[0,0,0]
	v_mfma_scale_f32_16x16x128_f8f6f4 v[154:157], v[10:17], v[50:57], v[154:157], v232, v232 op_sel_hi:[0,0,0]
	v_mfma_scale_f32_16x16x128_f8f6f4 v[146:149], v[2:9], v[58:65], v[146:149], v232, v232 op_sel_hi:[0,0,0]
	v_mfma_scale_f32_16x16x128_f8f6f4 v[138:141], v[10:17], v[58:65], v[138:141], v232, v232 op_sel_hi:[0,0,0]
	v_mfma_scale_f32_16x16x128_f8f6f4 v[182:185], v[18:25], v[34:41], v[182:185], v232, v232 op_sel_hi:[0,0,0]
	v_mfma_scale_f32_16x16x128_f8f6f4 v[174:177], v[26:33], v[34:41], v[174:177], v232, v232 op_sel_hi:[0,0,0]
	v_mfma_scale_f32_16x16x128_f8f6f4 v[166:169], v[18:25], v[42:49], v[166:169], v232, v232 op_sel_hi:[0,0,0]
	v_mfma_scale_f32_16x16x128_f8f6f4 v[158:161], v[26:33], v[42:49], v[158:161], v232, v232 op_sel_hi:[0,0,0]
	v_mfma_scale_f32_16x16x128_f8f6f4 v[150:153], v[18:25], v[50:57], v[150:153], v232, v232 op_sel_hi:[0,0,0]
	v_mfma_scale_f32_16x16x128_f8f6f4 v[142:145], v[26:33], v[50:57], v[142:145], v232, v232 op_sel_hi:[0,0,0]
	v_mfma_scale_f32_16x16x128_f8f6f4 v[134:137], v[18:25], v[58:65], v[134:137], v232, v232 op_sel_hi:[0,0,0]
	v_mfma_scale_f32_16x16x128_f8f6f4 v[130:133], v[26:33], v[58:65], v[130:133], v232, v232 op_sel_hi:[0,0,0]
	s_barrier
	s_add_i32 s34, s76, s45
	v_lshl_add_u64 v[234:235], s[38:39], 0, v[196:197]
	s_mov_b32 m0, s34
	ds_read_b128 v[34:37], v230 offset:49152
	ds_read_b128 v[42:45], v230 offset:51200
	ds_read_b128 v[38:41], v231 offset:49152
	ds_read_b128 v[46:49], v231 offset:51200
	ds_read_b128 v[50:53], v230 offset:53248
	ds_read_b128 v[58:61], v230 offset:55296
	ds_read_b128 v[54:57], v231 offset:53248
	ds_read_b128 v[62:65], v231 offset:55296
	global_load_lds_dwordx4 v[234:235], off
	s_add_i32 m0, s34, 0x2000
	s_add_u32 s30, s30, 0x9000
	v_lshl_add_u64 v[234:235], s[38:39], 0, v[200:201]
	s_addc_u32 s31, s31, 0
	s_add_i32 s34, s77, s45
	global_load_lds_dwordx4 v[234:235], off
	v_lshl_add_u64 v[234:235], s[30:31], 0, v[196:197]
	s_mov_b32 m0, s34
	s_nop 0
	global_load_lds_dwordx4 v[234:235], off
	v_lshl_add_u64 v[234:235], s[30:31], 0, v[200:201]
	s_add_i32 m0, s34, 0x2000
	s_nop 0
	global_load_lds_dwordx4 v[234:235], off
	v_lshl_add_u64 v[234:235], s[36:37], 0, v[194:195]
	s_mov_b32 m0, s57
	s_nop 0
	global_load_lds_dwordx4 v[234:235], off
	v_lshl_add_u64 v[234:235], s[36:37], 0, v[198:199]
	s_mov_b32 m0, s58
	s_nop 0
	global_load_lds_dwordx4 v[234:235], off
	s_waitcnt vmcnt(8)
	s_waitcnt lgkmcnt(0)
	s_barrier
	s_waitcnt lgkmcnt(0)
	v_mfma_scale_f32_16x16x128_f8f6f4 v[126:129], v[2:9], v[34:41], v[126:129], v232, v232 op_sel_hi:[0,0,0]
	v_mfma_scale_f32_16x16x128_f8f6f4 v[122:125], v[10:17], v[34:41], v[122:125], v232, v232 op_sel_hi:[0,0,0]
	v_mfma_scale_f32_16x16x128_f8f6f4 v[114:117], v[2:9], v[42:49], v[114:117], v232, v232 op_sel_hi:[0,0,0]
	v_mfma_scale_f32_16x16x128_f8f6f4 v[106:109], v[10:17], v[42:49], v[106:109], v232, v232 op_sel_hi:[0,0,0]
	v_mfma_scale_f32_16x16x128_f8f6f4 v[98:101], v[2:9], v[50:57], v[98:101], v232, v232 op_sel_hi:[0,0,0]
	v_mfma_scale_f32_16x16x128_f8f6f4 v[90:93], v[10:17], v[50:57], v[90:93], v232, v232 op_sel_hi:[0,0,0]
	v_mfma_scale_f32_16x16x128_f8f6f4 v[82:85], v[2:9], v[58:65], v[82:85], v232, v232 op_sel_hi:[0,0,0]
	v_mfma_scale_f32_16x16x128_f8f6f4 v[74:77], v[10:17], v[58:65], v[74:77], v232, v232 op_sel_hi:[0,0,0]
	v_mfma_scale_f32_16x16x128_f8f6f4 v[118:121], v[18:25], v[34:41], v[118:121], v232, v232 op_sel_hi:[0,0,0]
	v_mfma_scale_f32_16x16x128_f8f6f4 v[110:113], v[26:33], v[34:41], v[110:113], v232, v232 op_sel_hi:[0,0,0]
	v_mfma_scale_f32_16x16x128_f8f6f4 v[102:105], v[18:25], v[42:49], v[102:105], v232, v232 op_sel_hi:[0,0,0]
	v_mfma_scale_f32_16x16x128_f8f6f4 v[94:97], v[26:33], v[42:49], v[94:97], v232, v232 op_sel_hi:[0,0,0]
	v_mfma_scale_f32_16x16x128_f8f6f4 v[86:89], v[18:25], v[50:57], v[86:89], v232, v232 op_sel_hi:[0,0,0]
	v_mfma_scale_f32_16x16x128_f8f6f4 v[78:81], v[26:33], v[50:57], v[78:81], v232, v232 op_sel_hi:[0,0,0]
	v_mfma_scale_f32_16x16x128_f8f6f4 v[70:73], v[18:25], v[58:65], v[70:73], v232, v232 op_sel_hi:[0,0,0]
	v_mfma_scale_f32_16x16x128_f8f6f4 v[66:69], v[26:33], v[58:65], v[66:69], v232, v232 op_sel_hi:[0,0,0]
	s_barrier
	s_add_u32 s28, s28, 0x10000
	s_addc_u32 s29, s29, 0
	s_cmp_gt_u32 s72, 53
	s_mov_b32 s72, s75
	s_cbranch_scc1 .LBB0_3934

.LBB0_3930:
	s_add_u32 s30, s26, s28
	s_addc_u32 s31, s27, s29
	s_add_u32 s30, s30, 0x10000
	s_addc_u32 s31, s31, 0
	s_add_u32 s38, s73, s28
	s_addc_u32 s39, s74, s29
	s_waitcnt lgkmcnt(0)
	s_cmp_eq_u32 s28, 0x1b0000
	s_cselect_b32 s35, s5, s31
	s_cselect_b32 s34, s4, s30
	s_cselect_b32 s31, s25, s39
	s_cselect_b32 s30, s24, s38
	s_barrier
	s_waitcnt lgkmcnt(0)
	v_mfma_scale_f32_16x16x128_f8f6f4 v[190:193], v[26:33], v[58:65], v[190:193], v232, v232 op_sel_hi:[0,0,0]
	v_mfma_scale_f32_16x16x128_f8f6f4 v[186:189], v[18:25], v[58:65], v[186:189], v232, v232 op_sel_hi:[0,0,0]
	v_mfma_scale_f32_16x16x128_f8f6f4 v[178:181], v[26:33], v[50:57], v[178:181], v232, v232 op_sel_hi:[0,0,0]
	v_mfma_scale_f32_16x16x128_f8f6f4 v[170:173], v[18:25], v[50:57], v[170:173], v232, v232 op_sel_hi:[0,0,0]
	v_mfma_scale_f32_16x16x128_f8f6f4 v[162:165], v[26:33], v[42:49], v[162:165], v232, v232 op_sel_hi:[0,0,0]
	v_mfma_scale_f32_16x16x128_f8f6f4 v[154:157], v[18:25], v[42:49], v[154:157], v232, v232 op_sel_hi:[0,0,0]
	v_mfma_scale_f32_16x16x128_f8f6f4 v[146:149], v[26:33], v[34:41], v[146:149], v232, v232 op_sel_hi:[0,0,0]
	v_mfma_scale_f32_16x16x128_f8f6f4 v[138:141], v[18:25], v[34:41], v[138:141], v232, v232 op_sel_hi:[0,0,0]
	v_mfma_scale_f32_16x16x128_f8f6f4 v[182:185], v[10:17], v[58:65], v[182:185], v232, v232 op_sel_hi:[0,0,0]
	v_mfma_scale_f32_16x16x128_f8f6f4 v[174:177], v[2:9], v[58:65], v[174:177], v232, v232 op_sel_hi:[0,0,0]
	v_mfma_scale_f32_16x16x128_f8f6f4 v[166:169], v[10:17], v[50:57], v[166:169], v232, v232 op_sel_hi:[0,0,0]
	v_mfma_scale_f32_16x16x128_f8f6f4 v[158:161], v[2:9], v[50:57], v[158:161], v232, v232 op_sel_hi:[0,0,0]
	v_mfma_scale_f32_16x16x128_f8f6f4 v[150:153], v[10:17], v[42:49], v[150:153], v232, v232 op_sel_hi:[0,0,0]
	v_mfma_scale_f32_16x16x128_f8f6f4 v[142:145], v[2:9], v[42:49], v[142:145], v232, v232 op_sel_hi:[0,0,0]
	v_mfma_scale_f32_16x16x128_f8f6f4 v[134:137], v[10:17], v[34:41], v[134:137], v232, v232 op_sel_hi:[0,0,0]
	v_mfma_scale_f32_16x16x128_f8f6f4 v[130:133], v[2:9], v[34:41], v[130:133], v232, v232 op_sel_hi:[0,0,0]
	s_barrier
	s_mov_b32 m0, s47
	v_lshl_add_u64 v[234:235], s[30:31], 0, v[196:197]
	s_add_u32 s38, s30, 0x1000
	ds_read_b128 v[58:61], v230 offset:16384
	ds_read_b128 v[50:53], v230 offset:18432
	ds_read_b128 v[62:65], v231 offset:16384
	ds_read_b128 v[54:57], v231 offset:18432
	ds_read_b128 v[42:45], v230 offset:20480
	ds_read_b128 v[34:37], v230 offset:22528
	ds_read_b128 v[46:49], v231 offset:20480
	ds_read_b128 v[38:41], v231 offset:22528
	global_load_lds_dwordx4 v[234:235], off
	v_lshl_add_u64 v[234:235], s[30:31], 0, v[200:201]
	s_mov_b32 m0, s51
	s_addc_u32 s39, s31, 0
	global_load_lds_dwordx4 v[234:235], off
	v_lshl_add_u64 v[234:235], s[38:39], 0, v[196:197]
	s_mov_b32 m0, s52
	s_and_b64 vcc, exec, s[36:37]
	global_load_lds_dwordx4 v[234:235], off
	v_lshl_add_u64 v[234:235], s[38:39], 0, v[200:201]
	s_mov_b32 m0, s53
	s_mov_b64 s[38:39], -1
	global_load_lds_dwordx4 v[234:235], off
	v_lshl_add_u64 v[234:235], s[34:35], 0, v[194:195]
	s_mov_b32 m0, s46
	s_nop 0
	global_load_lds_dwordx4 v[234:235], off
	v_lshl_add_u64 v[234:235], s[34:35], 0, v[198:199]
	s_mov_b32 m0, s54
	s_nop 0
	global_load_lds_dwordx4 v[234:235], off
	s_cbranch_vccz .LBB0_3932
	s_waitcnt vmcnt(8)
	s_mov_b64 s[38:39], 0

.LBB0_3948:
	s_add_i32 s29, s29, 2
	s_add_u32 s14, s12, 0x8000
	s_waitcnt lgkmcnt(0)
	s_addc_u32 s15, s13, 0
	s_add_u32 s16, s10, 0x8000
	s_addc_u32 s17, s11, 0
	s_barrier
	s_waitcnt lgkmcnt(0)
	v_mfma_scale_f32_16x16x128_f8f6f4 v[126:129], v[26:33], v[58:65], v[126:129], v214, v214 op_sel_hi:[0,0,0]
	v_mfma_scale_f32_16x16x128_f8f6f4 v[122:125], v[18:25], v[58:65], v[122:125], v214, v214 op_sel_hi:[0,0,0]
	v_mfma_scale_f32_16x16x128_f8f6f4 v[118:121], v[26:33], v[50:57], v[118:121], v214, v214 op_sel_hi:[0,0,0]
	v_mfma_scale_f32_16x16x128_f8f6f4 v[114:117], v[18:25], v[50:57], v[114:117], v214, v214 op_sel_hi:[0,0,0]
	v_mfma_scale_f32_16x16x128_f8f6f4 v[110:113], v[26:33], v[42:49], v[110:113], v214, v214 op_sel_hi:[0,0,0]
	v_mfma_scale_f32_16x16x128_f8f6f4 v[106:109], v[18:25], v[42:49], v[106:109], v214, v214 op_sel_hi:[0,0,0]
	v_mfma_scale_f32_16x16x128_f8f6f4 v[98:101], v[26:33], v[34:41], v[98:101], v214, v214 op_sel_hi:[0,0,0]
	v_mfma_scale_f32_16x16x128_f8f6f4 v[90:93], v[18:25], v[34:41], v[90:93], v214, v214 op_sel_hi:[0,0,0]
	v_mfma_scale_f32_16x16x128_f8f6f4 v[102:105], v[10:17], v[58:65], v[102:105], v214, v214 op_sel_hi:[0,0,0]
	v_mfma_scale_f32_16x16x128_f8f6f4 v[94:97], v[2:9], v[58:65], v[94:97], v214, v214 op_sel_hi:[0,0,0]
	v_mfma_scale_f32_16x16x128_f8f6f4 v[86:89], v[10:17], v[50:57], v[86:89], v214, v214 op_sel_hi:[0,0,0]
	v_mfma_scale_f32_16x16x128_f8f6f4 v[82:85], v[2:9], v[50:57], v[82:85], v214, v214 op_sel_hi:[0,0,0]
	v_mfma_scale_f32_16x16x128_f8f6f4 v[78:81], v[10:17], v[42:49], v[78:81], v214, v214 op_sel_hi:[0,0,0]
	v_mfma_scale_f32_16x16x128_f8f6f4 v[74:77], v[2:9], v[42:49], v[74:77], v214, v214 op_sel_hi:[0,0,0]
	v_mfma_scale_f32_16x16x128_f8f6f4 v[70:73], v[10:17], v[34:41], v[70:73], v214, v214 op_sel_hi:[0,0,0]
	v_mfma_scale_f32_16x16x128_f8f6f4 v[66:69], v[2:9], v[34:41], v[66:69], v214, v214 op_sel_hi:[0,0,0]
	s_barrier
	v_add_u32_e32 v6, s38, v203
	v_add_u32_e32 v14, s38, v208
	v_add_u32_e32 v22, s39, v203
	v_add_u32_e32 v30, s39, v208
	ds_read_b128 v[2:5], v6
	ds_read_b128 v[10:13], v6 offset:2048
	ds_read_b128 v[6:9], v14
	ds_read_b128 v[14:17], v14 offset:2048
	ds_read_b128 v[18:21], v22
	ds_read_b128 v[26:29], v22 offset:2048
	ds_read_b128 v[22:25], v30
	ds_read_b128 v[30:33], v30 offset:2048
	s_add_u32 s12, s12, 0x1000
	s_addc_u32 s13, s13, 0
	s_mov_b32 m0, s27
	v_lshl_add_u64 v[216:217], s[12:13], 0, v[194:195]
	ds_read_b128 v[34:37], v212 offset:32768
	ds_read_b128 v[42:45], v212 offset:34816
	ds_read_b128 v[38:41], v213 offset:32768
	ds_read_b128 v[46:49], v213 offset:34816
	ds_read_b128 v[50:53], v212 offset:36864
	ds_read_b128 v[58:61], v212 offset:38912
	ds_read_b128 v[54:57], v213 offset:36864
	ds_read_b128 v[62:65], v213 offset:38912
	global_load_lds_dwordx4 v[216:217], off
	v_lshl_add_u64 v[216:217], s[12:13], 0, v[198:199]
	s_mov_b32 m0, s28
	s_nop 0
	global_load_lds_dwordx4 v[216:217], off
	s_waitcnt vmcnt(8)
	s_waitcnt lgkmcnt(0)
	s_barrier
	s_waitcnt lgkmcnt(0)
	v_mfma_scale_f32_16x16x128_f8f6f4 v[190:193], v[2:9], v[34:41], v[190:193], v214, v214 op_sel_hi:[0,0,0]
	v_mfma_scale_f32_16x16x128_f8f6f4 v[186:189], v[10:17], v[34:41], v[186:189], v214, v214 op_sel_hi:[0,0,0]
	v_mfma_scale_f32_16x16x128_f8f6f4 v[182:185], v[2:9], v[42:49], v[182:185], v214, v214 op_sel_hi:[0,0,0]
	v_mfma_scale_f32_16x16x128_f8f6f4 v[178:181], v[10:17], v[42:49], v[178:181], v214, v214 op_sel_hi:[0,0,0]
	v_mfma_scale_f32_16x16x128_f8f6f4 v[174:177], v[2:9], v[50:57], v[174:177], v214, v214 op_sel_hi:[0,0,0]
	v_mfma_scale_f32_16x16x128_f8f6f4 v[170:173], v[10:17], v[50:57], v[170:173], v214, v214 op_sel_hi:[0,0,0]
	v_mfma_scale_f32_16x16x128_f8f6f4 v[162:165], v[2:9], v[58:65], v[162:165], v214, v214 op_sel_hi:[0,0,0]
	v_mfma_scale_f32_16x16x128_f8f6f4 v[154:157], v[10:17], v[58:65], v[154:157], v214, v214 op_sel_hi:[0,0,0]
	v_mfma_scale_f32_16x16x128_f8f6f4 v[166:169], v[18:25], v[34:41], v[166:169], v214, v214 op_sel_hi:[0,0,0]
	v_mfma_scale_f32_16x16x128_f8f6f4 v[158:161], v[26:33], v[34:41], v[158:161], v214, v214 op_sel_hi:[0,0,0]
	v_mfma_scale_f32_16x16x128_f8f6f4 v[150:153], v[18:25], v[42:49], v[150:153], v214, v214 op_sel_hi:[0,0,0]
	v_mfma_scale_f32_16x16x128_f8f6f4 v[146:149], v[26:33], v[42:49], v[146:149], v214, v214 op_sel_hi:[0,0,0]
	v_mfma_scale_f32_16x16x128_f8f6f4 v[142:145], v[18:25], v[50:57], v[142:145], v214, v214 op_sel_hi:[0,0,0]
	v_mfma_scale_f32_16x16x128_f8f6f4 v[138:141], v[26:33], v[50:57], v[138:141], v214, v214 op_sel_hi:[0,0,0]
	v_mfma_scale_f32_16x16x128_f8f6f4 v[134:137], v[18:25], v[58:65], v[134:137], v214, v214 op_sel_hi:[0,0,0]
	v_mfma_scale_f32_16x16x128_f8f6f4 v[130:133], v[26:33], v[58:65], v[130:133], v214, v214 op_sel_hi:[0,0,0]
	s_barrier
	s_mov_b32 m0, s40
	v_lshl_add_u64 v[216:217], s[16:17], 0, v[196:197]
	s_add_u32 s10, s10, 0x9000
	ds_read_b128 v[34:37], v212 offset:49152
	ds_read_b128 v[42:45], v212 offset:51200
	ds_read_b128 v[38:41], v213 offset:49152
	ds_read_b128 v[46:49], v213 offset:51200
	ds_read_b128 v[50:53], v212 offset:53248
	ds_read_b128 v[58:61], v212 offset:55296
	ds_read_b128 v[54:57], v213 offset:53248
	ds_read_b128 v[62:65], v213 offset:55296
	global_load_lds_dwordx4 v[216:217], off
	v_lshl_add_u64 v[216:217], s[16:17], 0, v[200:201]
	s_mov_b32 m0, s41
	s_addc_u32 s11, s11, 0
	global_load_lds_dwordx4 v[216:217], off
	v_lshl_add_u64 v[216:217], s[10:11], 0, v[196:197]
	s_mov_b32 m0, s42
	s_nop 0
	global_load_lds_dwordx4 v[216:217], off
	v_lshl_add_u64 v[216:217], s[10:11], 0, v[200:201]
	s_mov_b32 m0, s43
	s_nop 0
	global_load_lds_dwordx4 v[216:217], off
	v_lshl_add_u64 v[216:217], s[14:15], 0, v[194:195]
	s_mov_b32 m0, s30
	s_nop 0
	global_load_lds_dwordx4 v[216:217], off
	v_lshl_add_u64 v[216:217], s[14:15], 0, v[198:199]
	s_mov_b32 m0, s31
	s_nop 0
	global_load_lds_dwordx4 v[216:217], off
	s_waitcnt vmcnt(8)
	s_waitcnt lgkmcnt(0)
	s_barrier
	s_waitcnt lgkmcnt(0)
	v_mfma_scale_f32_16x16x128_f8f6f4 v[126:129], v[2:9], v[34:41], v[126:129], v214, v214 op_sel_hi:[0,0,0]
	v_mfma_scale_f32_16x16x128_f8f6f4 v[122:125], v[10:17], v[34:41], v[122:125], v214, v214 op_sel_hi:[0,0,0]
	v_mfma_scale_f32_16x16x128_f8f6f4 v[118:121], v[2:9], v[42:49], v[118:121], v214, v214 op_sel_hi:[0,0,0]
	v_mfma_scale_f32_16x16x128_f8f6f4 v[114:117], v[10:17], v[42:49], v[114:117], v214, v214 op_sel_hi:[0,0,0]
	v_mfma_scale_f32_16x16x128_f8f6f4 v[110:113], v[2:9], v[50:57], v[110:113], v214, v214 op_sel_hi:[0,0,0]
	v_mfma_scale_f32_16x16x128_f8f6f4 v[106:109], v[10:17], v[50:57], v[106:109], v214, v214 op_sel_hi:[0,0,0]
	v_mfma_scale_f32_16x16x128_f8f6f4 v[98:101], v[2:9], v[58:65], v[98:101], v214, v214 op_sel_hi:[0,0,0]
	v_mfma_scale_f32_16x16x128_f8f6f4 v[90:93], v[10:17], v[58:65], v[90:93], v214, v214 op_sel_hi:[0,0,0]
	v_mfma_scale_f32_16x16x128_f8f6f4 v[102:105], v[18:25], v[34:41], v[102:105], v214, v214 op_sel_hi:[0,0,0]
	v_mfma_scale_f32_16x16x128_f8f6f4 v[94:97], v[26:33], v[34:41], v[94:97], v214, v214 op_sel_hi:[0,0,0]
	v_mfma_scale_f32_16x16x128_f8f6f4 v[86:89], v[18:25], v[42:49], v[86:89], v214, v214 op_sel_hi:[0,0,0]
	v_mfma_scale_f32_16x16x128_f8f6f4 v[82:85], v[26:33], v[42:49], v[82:85], v214, v214 op_sel_hi:[0,0,0]
	v_mfma_scale_f32_16x16x128_f8f6f4 v[78:81], v[18:25], v[50:57], v[78:81], v214, v214 op_sel_hi:[0,0,0]
	v_mfma_scale_f32_16x16x128_f8f6f4 v[74:77], v[26:33], v[50:57], v[74:77], v214, v214 op_sel_hi:[0,0,0]
	v_mfma_scale_f32_16x16x128_f8f6f4 v[70:73], v[18:25], v[58:65], v[70:73], v214, v214 op_sel_hi:[0,0,0]
	v_mfma_scale_f32_16x16x128_f8f6f4 v[66:69], v[26:33], v[58:65], v[66:69], v214, v214 op_sel_hi:[0,0,0]
	s_barrier
	s_add_u32 s6, s6, 0x10000
	s_addc_u32 s7, s7, 0
	s_cmp_ge_u32 s29, s19
	s_cbranch_scc1 .LBB0_3957

.LBB0_3953:
	s_cmp_lg_u32 s35, s6
	s_cselect_b32 s10, s6, 0
	s_cselect_b32 s11, s7, 0
	s_add_u32 s12, s4, s10
	s_addc_u32 s13, s5, s11
	s_waitcnt lgkmcnt(0)
	s_add_u32 s10, s0, s10
	s_addc_u32 s11, s1, s11
	s_barrier
	s_waitcnt lgkmcnt(0)
	v_mfma_scale_f32_16x16x128_f8f6f4 v[190:193], v[26:33], v[58:65], v[190:193], v214, v214 op_sel_hi:[0,0,0]
	v_mfma_scale_f32_16x16x128_f8f6f4 v[186:189], v[18:25], v[58:65], v[186:189], v214, v214 op_sel_hi:[0,0,0]
	v_mfma_scale_f32_16x16x128_f8f6f4 v[182:185], v[26:33], v[50:57], v[182:185], v214, v214 op_sel_hi:[0,0,0]
	v_mfma_scale_f32_16x16x128_f8f6f4 v[178:181], v[18:25], v[50:57], v[178:181], v214, v214 op_sel_hi:[0,0,0]
	v_mfma_scale_f32_16x16x128_f8f6f4 v[174:177], v[26:33], v[42:49], v[174:177], v214, v214 op_sel_hi:[0,0,0]
	v_mfma_scale_f32_16x16x128_f8f6f4 v[170:173], v[18:25], v[42:49], v[170:173], v214, v214 op_sel_hi:[0,0,0]
	v_mfma_scale_f32_16x16x128_f8f6f4 v[162:165], v[26:33], v[34:41], v[162:165], v214, v214 op_sel_hi:[0,0,0]
	v_mfma_scale_f32_16x16x128_f8f6f4 v[154:157], v[18:25], v[34:41], v[154:157], v214, v214 op_sel_hi:[0,0,0]
	v_mfma_scale_f32_16x16x128_f8f6f4 v[166:169], v[10:17], v[58:65], v[166:169], v214, v214 op_sel_hi:[0,0,0]
	v_mfma_scale_f32_16x16x128_f8f6f4 v[158:161], v[2:9], v[58:65], v[158:161], v214, v214 op_sel_hi:[0,0,0]
	v_mfma_scale_f32_16x16x128_f8f6f4 v[150:153], v[10:17], v[50:57], v[150:153], v214, v214 op_sel_hi:[0,0,0]
	v_mfma_scale_f32_16x16x128_f8f6f4 v[146:149], v[2:9], v[50:57], v[146:149], v214, v214 op_sel_hi:[0,0,0]
	v_mfma_scale_f32_16x16x128_f8f6f4 v[142:145], v[10:17], v[42:49], v[142:145], v214, v214 op_sel_hi:[0,0,0]
	v_mfma_scale_f32_16x16x128_f8f6f4 v[138:141], v[2:9], v[42:49], v[138:141], v214, v214 op_sel_hi:[0,0,0]
	v_mfma_scale_f32_16x16x128_f8f6f4 v[134:137], v[10:17], v[34:41], v[134:137], v214, v214 op_sel_hi:[0,0,0]
	v_mfma_scale_f32_16x16x128_f8f6f4 v[130:133], v[2:9], v[34:41], v[130:133], v214, v214 op_sel_hi:[0,0,0]
	s_barrier
	s_mov_b32 m0, s21
	v_lshl_add_u64 v[216:217], s[10:11], 0, v[196:197]
	s_add_u32 s16, s10, 0x1000
	ds_read_b128 v[58:61], v212 offset:16384
	ds_read_b128 v[50:53], v212 offset:18432
	ds_read_b128 v[62:65], v213 offset:16384
	ds_read_b128 v[54:57], v213 offset:18432
	ds_read_b128 v[42:45], v212 offset:20480
	ds_read_b128 v[34:37], v212 offset:22528
	ds_read_b128 v[46:49], v213 offset:20480
	ds_read_b128 v[38:41], v213 offset:22528
	global_load_lds_dwordx4 v[216:217], off
	v_lshl_add_u64 v[216:217], s[10:11], 0, v[200:201]
	s_mov_b32 m0, s22
	s_addc_u32 s17, s11, 0
	global_load_lds_dwordx4 v[216:217], off
	v_lshl_add_u64 v[216:217], s[16:17], 0, v[196:197]
	s_mov_b32 m0, s23
	s_and_b64 vcc, exec, s[14:15]
	global_load_lds_dwordx4 v[216:217], off
	v_lshl_add_u64 v[216:217], s[16:17], 0, v[200:201]
	s_mov_b32 m0, s24
	s_mov_b64 s[16:17], -1
	global_load_lds_dwordx4 v[216:217], off
	v_lshl_add_u64 v[216:217], s[12:13], 0, v[194:195]
	s_mov_b32 m0, s20
	s_nop 0
	global_load_lds_dwordx4 v[216:217], off
	v_lshl_add_u64 v[216:217], s[12:13], 0, v[198:199]
	s_mov_b32 m0, s25
	s_nop 0
	global_load_lds_dwordx4 v[216:217], off
	s_cbranch_vccz .LBB0_3955
	s_waitcnt vmcnt(8)
	s_mov_b64 s[16:17], 0
